# code placement: every run of >=8 MFMAs padded to start on an 8-byte boundary (one s_nop before misaligned bursts)
# baseline (speedup 1.0000x reference)
; #define PG8_STAGE2(bufoff, gbase, v0, v1) do { \
;         __builtin_amdgcn_global_load_lds((const unsigned*)((const char*)(gbase) + (v0)), (LAS unsigned*)(lds + (bufoff) + ldsw), 16, 0, 0); \
;         __builtin_amdgcn_global_load_lds((const unsigned*)((const char*)(gbase) + (v1)), (LAS unsigned*)(lds + (bufoff) + ldsw + 8192), 16, 0, 0); } while (0)
; #define PG8_STAGE(bufoff, gbase, voff) PG8_STAGE2(bufoff, gbase, (voff)[0], (voff)[1])
; #define PG8_WAIT_V(n) asm volatile("s_waitcnt vmcnt(" #n ")" ::: "memory")
; #define PG8_WAIT_L(n) asm volatile("s_waitcnt lgkmcnt(" #n ")" ::: "memory")
; template <class Epi, class Sched, bool ALIGN_EPI, bool SP2, bool GATHER>
; DI void gemm_phase(LAS unsigned char* lds, const Gemm g, const Sched& S, const Epi& E) {
;     ...
;         const bool has_next = S.next(ui + 1, nxt);
;         const char* nA = (has_next && !GATHER) ? (const char*)g.A + (size_t)nxt.pm * tstep : cA; const char* nB = has_next ? (const char*)g.Bt + (size_t)nxt.pn * tstep : cB;
;         if constexpr (GATHER) { if (has_next) { PG8_GATHER(nxt, gN); } else {
; #pragma unroll
;             for (int h = 0; h < 2; ++h) { gN[h][0] = gC[h][0]; gN[h][1] = gC[h][1]; } } }
;         for (int t = 0; t < nt; t += 2) {
;             if constexpr (Epi::MID_T >= 0) { if (t == Epi::MID_T) { E.mid(acc, cur, wr, wc, fr, fq); PG8_SCHED; } }
;             const bool last = (t == nt - 2);
;             const char* a1 = cA + (size_t)(t + 1) * kstep;
;             const char* a2 = last ? nA : cA + (size_t)(t + 2) * kstep; const char* b2 = last ? nB : cB + (size_t)(t + 2) * kstep;
;             const char* a3 = a2 + kstep; const char* b3 = b2 + kstep;
;             unsigned x00 = gC[0][0], x01 = gC[0][1], x10 = gC[1][0], x11 = gC[1][1];
;             if constexpr (GATHER) { if (last) { x00 = gN[0][0]; x01 = gN[0][1]; x10 = gN[1][0]; x11 = gN[1][1]; } }
;             PG8_LDB(B0, 0, 0); PG8_LDB(B1, 0, 1); PG8_SCHED; PG8_LDA(At, 0, 0); PG8_STAGE2(PG8_SA(1, 1), a1 + hstepA, gC[1][0], gC[1][1]);
;             PG8_WAIT_V(8); PG8_WAIT_L(0); PG8_BAR; PG8_MMA(0, 0, At, B0); PG8_MMA(0, 1, At, B1); PG8_BAR; PG8_SCHED;
;             PG8_LDA(At, 0, 1); PG8_STAGE(PG8_SB(0, 0), b2, voffB); PG8_STAGE(PG8_SB(0, 1), b2 + hstep, voffB); PG8_STAGE2(PG8_SA(0, 0), a2, x00, x01);
;             PG8_WAIT_V(8); PG8_WAIT_L(0); PG8_BAR; PG8_MMA(1, 0, At, B0); PG8_MMA(1, 1, At, B1); PG8_BAR; PG8_SCHED;
.LBB0_102:
	s_ashr_i32 s51, s50, 31
	s_lshl_b64 s[14:15], s[50:51], 20
	s_add_u32 s52, s3, s14
	s_addc_u32 s53, s63, s15
	s_and_b64 s[14:15], s[8:9], exec
	s_cselect_b32 s5, s53, s11
	s_cselect_b32 s7, s52, s10
	s_ashr_i32 s49, s48, 31
	s_lshl_b64 s[14:15], s[48:49], 20
	s_add_u32 s54, s64, s14
	s_addc_u32 s55, s65, s15
	s_and_b64 s[14:15], s[8:9], exec
	s_cselect_b32 s16, s55, s13
	s_cselect_b32 s17, s54, s12
	s_add_u32 s10, s10, 0x80080
	s_addc_u32 s11, s11, 0
	s_add_u32 s22, s12, 0x100
	s_addc_u32 s38, s13, 0
	s_mov_b32 s39, -2
	ds_read_b128 v[4:7], v175
	ds_read_b128 v[8:11], v175 offset:1024
	ds_read_b128 v[158:161], v175 offset:2048
	ds_read_b128 v[162:165], v175 offset:3072
	ds_read_b128 v[166:169], v176
	ds_read_b128 v[180:183], v176 offset:1024
	ds_read_b128 v[184:187], v176 offset:2048
	ds_read_b128 v[188:191], v176 offset:3072
	s_add_u32 s12, s10, 0xfff80080
	s_addc_u32 s13, s11, -1
	s_cmp_eq_u32 s39, 28
	s_cselect_b32 s15, s5, s13
	s_cselect_b32 s14, s7, s12
	s_cselect_b32 s13, s16, s38
	s_cselect_b32 s12, s17, s22
	s_add_i32 m0, s67, 0xc000
	ds_read_b128 v[192:195], v177
	ds_read_b128 v[196:199], v177 offset:1024
	ds_read_b128 v[200:203], v177 offset:2048
	ds_read_b128 v[204:207], v177 offset:3072
	ds_read_b128 v[208:211], v177 offset:4096
	ds_read_b128 v[212:215], v177 offset:5120
	ds_read_b128 v[216:219], v177 offset:6144
	ds_read_b128 v[220:223], v177 offset:7168
	global_load_lds_dwordx4 v150, s[10:11]
	s_add_i32 m0, s67, 0xe000
	s_nop 0
	global_load_lds_dwordx4 v152, s[10:11]
	s_waitcnt vmcnt(8)
	s_waitcnt lgkmcnt(0)
	s_barrier
	s_setprio 1
	s_waitcnt lgkmcnt(0)
	s_nop 0
	v_mfma_f32_16x16x32_bf16 v[136:139], v[4:7], v[192:195], 0
	v_mfma_f32_16x16x32_bf16 v[132:135], v[158:161], v[192:195], 0
	v_mfma_f32_16x16x32_bf16 v[128:131], v[4:7], v[200:203], 0
	v_mfma_f32_16x16x32_bf16 v[124:127], v[158:161], v[200:203], 0
	v_mfma_f32_16x16x32_bf16 v[120:123], v[4:7], v[208:211], 0
	v_mfma_f32_16x16x32_bf16 v[116:119], v[158:161], v[208:211], 0
	v_mfma_f32_16x16x32_bf16 v[112:115], v[4:7], v[216:219], 0
	v_mfma_f32_16x16x32_bf16 v[108:111], v[158:161], v[216:219], 0
	v_mfma_f32_16x16x32_bf16 v[136:139], v[8:11], v[196:199], v[136:139]
	v_mfma_f32_16x16x32_bf16 v[132:135], v[162:165], v[196:199], v[132:135]
	v_mfma_f32_16x16x32_bf16 v[128:131], v[8:11], v[204:207], v[128:131]
	v_mfma_f32_16x16x32_bf16 v[124:127], v[162:165], v[204:207], v[124:127]
	v_mfma_f32_16x16x32_bf16 v[120:123], v[8:11], v[212:215], v[120:123]
	v_mfma_f32_16x16x32_bf16 v[116:119], v[162:165], v[212:215], v[116:119]
	v_mfma_f32_16x16x32_bf16 v[112:115], v[8:11], v[220:223], v[112:115]
	v_mfma_f32_16x16x32_bf16 v[108:111], v[162:165], v[220:223], v[108:111]
	s_setprio 0
	s_setprio 1
	v_mfma_f32_16x16x32_bf16 v[72:75], v[166:169], v[192:195], 0
	v_mfma_f32_16x16x32_bf16 v[68:71], v[184:187], v[192:195], 0
	v_mfma_f32_16x16x32_bf16 v[64:67], v[166:169], v[200:203], 0
	v_mfma_f32_16x16x32_bf16 v[60:63], v[184:187], v[200:203], 0
	v_mfma_f32_16x16x32_bf16 v[56:59], v[166:169], v[208:211], 0
	v_mfma_f32_16x16x32_bf16 v[52:55], v[184:187], v[208:211], 0
	v_mfma_f32_16x16x32_bf16 v[48:51], v[166:169], v[216:219], 0
	v_mfma_f32_16x16x32_bf16 v[44:47], v[184:187], v[216:219], 0
	v_mfma_f32_16x16x32_bf16 v[72:75], v[180:183], v[196:199], v[72:75]
	v_mfma_f32_16x16x32_bf16 v[68:71], v[188:191], v[196:199], v[68:71]
	v_mfma_f32_16x16x32_bf16 v[64:67], v[180:183], v[204:207], v[64:67]
	v_mfma_f32_16x16x32_bf16 v[60:63], v[188:191], v[204:207], v[60:63]
	v_mfma_f32_16x16x32_bf16 v[56:59], v[180:183], v[212:215], v[56:59]
	v_mfma_f32_16x16x32_bf16 v[52:55], v[188:191], v[212:215], v[52:55]
	v_mfma_f32_16x16x32_bf16 v[48:51], v[180:183], v[220:223], v[48:51]
	v_mfma_f32_16x16x32_bf16 v[44:47], v[188:191], v[220:223], v[44:47]
	s_setprio 0
	s_barrier
	s_add_i32 s49, s78, s66
	s_add_u32 s98, s12, 0x80
	s_addc_u32 s99, s13, 0
	s_mov_b32 m0, s49
	ds_read_b128 v[192:195], v177 offset:16384
	ds_read_b128 v[196:199], v177 offset:17408
	ds_read_b128 v[200:203], v177 offset:18432
	ds_read_b128 v[204:207], v177 offset:19456
	ds_read_b128 v[208:211], v177 offset:20480
	ds_read_b128 v[212:215], v177 offset:21504
	ds_read_b128 v[216:219], v177 offset:22528
	ds_read_b128 v[220:223], v177 offset:23552
	global_load_lds_dwordx4 v142, s[12:13]
	s_add_i32 m0, s49, 0x2000
	s_add_u32 s56, s12, 0x80000
	s_addc_u32 s57, s13, 0
	s_add_i32 s49, s79, s66
	global_load_lds_dwordx4 v146, s[12:13]
	s_mov_b32 m0, s49
	s_add_u32 s100, s14, 0x80
	s_addc_u32 s101, s15, 0
	global_load_lds_dwordx4 v142, s[56:57]
	s_add_i32 m0, s49, 0x2000
	s_nop 0
	global_load_lds_dwordx4 v146, s[56:57]
	s_mov_b32 m0, s67
	s_nop 0
	global_load_lds_dwordx4 v140, s[14:15]
	s_mov_b32 m0, s68
	s_nop 0
	global_load_lds_dwordx4 v144, s[14:15]
	s_waitcnt vmcnt(8)
	s_waitcnt lgkmcnt(0)
	s_barrier
; #define PG8_STAGE2(bufoff, gbase, v0, v1) do { \
;         __builtin_amdgcn_global_load_lds((const unsigned*)((const char*)(gbase) + (v0)), (LAS unsigned*)(lds + (bufoff) + ldsw), 16, 0, 0); \
;         __builtin_amdgcn_global_load_lds((const unsigned*)((const char*)(gbase) + (v1)), (LAS unsigned*)(lds + (bufoff) + ldsw + 8192), 16, 0, 0); } while (0)
; #define PG8_LDA(dst, b, h) do { _Pragma("unroll") for (int m = 0; m < 4; ++m) _Pragma("unroll") for (int k = 0; k < 2; ++k) dst[m][k] = *(const LAS bf16x8*)(lds + PG8_SA(b, h) + aoff + m * 2048 + k * 1024); } while (0)
; #define PG8_LDB(dst, b, h) do { _Pragma("unroll") for (int n = 0; n < 2; ++n) _Pragma("unroll") for (int k = 0; k < 2; ++k) dst[n][k] = *(const LAS bf16x8*)(lds + PG8_SB(b, h) + boff + n * 2048 + k * 1024); } while (0)
; #define PG8_MMA(ai, bj, At, Bt) do { __builtin_amdgcn_s_setprio(1); _Pragma("unroll") for (int m = 0; m < 4; ++m) _Pragma("unroll") for (int n = 0; n < 2; ++n) _Pragma("unroll") for (int k = 0; k < 2; ++k) \
;         acc[ai][bj][m][n] = __builtin_amdgcn_mfma_f32_16x16x32_bf16(Bt[n][k], At[m][k], acc[ai][bj][m][n], 0, 0, 0); __builtin_amdgcn_s_setprio(0); } while (0)
; #define PG8_WAIT_V(n) asm volatile("s_waitcnt vmcnt(" #n ")" ::: "memory")
; #define PG8_WAIT_L(n) asm volatile("s_waitcnt lgkmcnt(" #n ")" ::: "memory")
; #define PG8_BAR __builtin_amdgcn_s_barrier()
; #define PG8_SCHED __builtin_amdgcn_sched_barrier(0)
; template <class Epi, class Sched, bool ALIGN_EPI, bool SP2, bool GATHER>
; DI void gemm_phase(LAS unsigned char* lds, const Gemm g, const Sched& S, const Epi& E) {
;     ...
;             PG8_WAIT_V(8); PG8_WAIT_L(0); PG8_BAR; PG8_MMA(1, 0, At, B0); PG8_MMA(1, 1, At, B1); PG8_BAR; PG8_SCHED;
;             PG8_LDB(B0, 1, 0); PG8_LDB(B1, 1, 1); PG8_SCHED; PG8_LDA(At, 1, 0); PG8_STAGE2(PG8_SA(0, 1), a2 + hstepA, x10, x11);
;             PG8_WAIT_V(8); PG8_WAIT_L(0); PG8_BAR; PG8_MMA(0, 0, At, B0); PG8_MMA(0, 1, At, B1); PG8_BAR; PG8_SCHED;
	s_setprio 1
	s_waitcnt lgkmcnt(0)
	s_nop 0
	v_mfma_f32_16x16x32_bf16 v[104:107], v[4:7], v[192:195], 0
	v_mfma_f32_16x16x32_bf16 v[100:103], v[158:161], v[192:195], 0
	v_mfma_f32_16x16x32_bf16 v[96:99], v[4:7], v[200:203], 0
	v_mfma_f32_16x16x32_bf16 v[92:95], v[158:161], v[200:203], 0
	v_mfma_f32_16x16x32_bf16 v[88:91], v[4:7], v[208:211], 0
	v_mfma_f32_16x16x32_bf16 v[84:87], v[158:161], v[208:211], 0
	v_mfma_f32_16x16x32_bf16 v[4:7], v[4:7], v[216:219], 0
	v_mfma_f32_16x16x32_bf16 v[104:107], v[8:11], v[196:199], v[104:107]
	v_mfma_f32_16x16x32_bf16 v[100:103], v[162:165], v[196:199], v[100:103]
	v_mfma_f32_16x16x32_bf16 v[96:99], v[8:11], v[204:207], v[96:99]
	v_mfma_f32_16x16x32_bf16 v[92:95], v[162:165], v[204:207], v[92:95]
	v_mfma_f32_16x16x32_bf16 v[88:91], v[8:11], v[212:215], v[88:91]
	v_mfma_f32_16x16x32_bf16 v[84:87], v[162:165], v[212:215], v[84:87]
	v_mfma_f32_16x16x32_bf16 v[4:7], v[8:11], v[220:223], v[4:7]
	v_mfma_f32_16x16x32_bf16 v[8:11], v[158:161], v[216:219], 0
	v_mfma_f32_16x16x32_bf16 v[8:11], v[162:165], v[220:223], v[8:11]
	s_setprio 0
	s_setprio 1
	v_mfma_f32_16x16x32_bf16 v[40:43], v[166:169], v[192:195], 0
	v_mfma_f32_16x16x32_bf16 v[36:39], v[184:187], v[192:195], 0
	v_mfma_f32_16x16x32_bf16 v[32:35], v[166:169], v[200:203], 0
	v_mfma_f32_16x16x32_bf16 v[28:31], v[184:187], v[200:203], 0
	v_mfma_f32_16x16x32_bf16 v[24:27], v[166:169], v[208:211], 0
	v_mfma_f32_16x16x32_bf16 v[20:23], v[184:187], v[208:211], 0
	v_mfma_f32_16x16x32_bf16 v[16:19], v[166:169], v[216:219], 0
	v_mfma_f32_16x16x32_bf16 v[12:15], v[184:187], v[216:219], 0
	v_mfma_f32_16x16x32_bf16 v[40:43], v[180:183], v[196:199], v[40:43]
	v_mfma_f32_16x16x32_bf16 v[36:39], v[188:191], v[196:199], v[36:39]
	v_mfma_f32_16x16x32_bf16 v[32:35], v[180:183], v[204:207], v[32:35]
	v_mfma_f32_16x16x32_bf16 v[28:31], v[188:191], v[204:207], v[28:31]
	v_mfma_f32_16x16x32_bf16 v[24:27], v[180:183], v[212:215], v[24:27]
	v_mfma_f32_16x16x32_bf16 v[20:23], v[188:191], v[212:215], v[20:23]
	v_mfma_f32_16x16x32_bf16 v[16:19], v[180:183], v[220:223], v[16:19]
	v_mfma_f32_16x16x32_bf16 v[12:15], v[188:191], v[220:223], v[12:15]
	s_setprio 0
	s_barrier
	s_add_i32 s49, 0, 0x18000
	v_add_u32_e32 v3, s49, v172
	s_add_i32 s51, 0, 0x1c000
	ds_read_b128 v[76:79], v3
	ds_read_b128 v[80:83], v3 offset:1024
	ds_read_b128 v[158:161], v3 offset:2048
	ds_read_b128 v[162:165], v3 offset:3072
	v_add_u32_e32 v3, s51, v172
	ds_read_b128 v[166:169], v3
	ds_read_b128 v[180:183], v3 offset:1024
	ds_read_b128 v[184:187], v3 offset:2048
	ds_read_b128 v[188:191], v3 offset:3072
	s_add_u32 s14, s14, 0x80000
	s_addc_u32 s15, s15, 0
	s_mov_b32 m0, s69
	ds_read_b128 v[192:195], v177 offset:32768
	ds_read_b128 v[196:199], v177 offset:33792
	ds_read_b128 v[200:203], v177 offset:34816
	ds_read_b128 v[204:207], v177 offset:35840
	ds_read_b128 v[208:211], v177 offset:36864
	ds_read_b128 v[212:215], v177 offset:37888
	ds_read_b128 v[216:219], v177 offset:38912
	ds_read_b128 v[220:223], v177 offset:39936
	global_load_lds_dwordx4 v140, s[14:15]
	s_mov_b32 m0, s70
	s_nop 0
	global_load_lds_dwordx4 v144, s[14:15]
	s_waitcnt vmcnt(8)
	s_waitcnt lgkmcnt(0)
	s_barrier
	s_setprio 1
	s_waitcnt lgkmcnt(0)
	s_nop 0
	v_mfma_f32_16x16x32_bf16 v[136:139], v[76:79], v[192:195], v[136:139]
	v_mfma_f32_16x16x32_bf16 v[132:135], v[158:161], v[192:195], v[132:135]
	v_mfma_f32_16x16x32_bf16 v[128:131], v[76:79], v[200:203], v[128:131]
	v_mfma_f32_16x16x32_bf16 v[124:127], v[158:161], v[200:203], v[124:127]
	v_mfma_f32_16x16x32_bf16 v[120:123], v[76:79], v[208:211], v[120:123]
	v_mfma_f32_16x16x32_bf16 v[116:119], v[158:161], v[208:211], v[116:119]
	v_mfma_f32_16x16x32_bf16 v[112:115], v[76:79], v[216:219], v[112:115]
	v_mfma_f32_16x16x32_bf16 v[108:111], v[158:161], v[216:219], v[108:111]
	v_mfma_f32_16x16x32_bf16 v[136:139], v[80:83], v[196:199], v[136:139]
	v_mfma_f32_16x16x32_bf16 v[132:135], v[162:165], v[196:199], v[132:135]
	v_mfma_f32_16x16x32_bf16 v[128:131], v[80:83], v[204:207], v[128:131]
	v_mfma_f32_16x16x32_bf16 v[124:127], v[162:165], v[204:207], v[124:127]
	v_mfma_f32_16x16x32_bf16 v[120:123], v[80:83], v[212:215], v[120:123]
	v_mfma_f32_16x16x32_bf16 v[116:119], v[162:165], v[212:215], v[116:119]
	v_mfma_f32_16x16x32_bf16 v[112:115], v[80:83], v[220:223], v[112:115]
	v_mfma_f32_16x16x32_bf16 v[108:111], v[162:165], v[220:223], v[108:111]
	s_setprio 0
	s_setprio 1
	v_mfma_f32_16x16x32_bf16 v[72:75], v[166:169], v[192:195], v[72:75]
	v_mfma_f32_16x16x32_bf16 v[68:71], v[184:187], v[192:195], v[68:71]
	v_mfma_f32_16x16x32_bf16 v[64:67], v[166:169], v[200:203], v[64:67]
	v_mfma_f32_16x16x32_bf16 v[60:63], v[184:187], v[200:203], v[60:63]
	v_mfma_f32_16x16x32_bf16 v[56:59], v[166:169], v[208:211], v[56:59]
	v_mfma_f32_16x16x32_bf16 v[52:55], v[184:187], v[208:211], v[52:55]
	v_mfma_f32_16x16x32_bf16 v[48:51], v[166:169], v[216:219], v[48:51]
	v_mfma_f32_16x16x32_bf16 v[44:47], v[184:187], v[216:219], v[44:47]
	v_mfma_f32_16x16x32_bf16 v[72:75], v[180:183], v[196:199], v[72:75]
	v_mfma_f32_16x16x32_bf16 v[68:71], v[188:191], v[196:199], v[68:71]
	v_mfma_f32_16x16x32_bf16 v[64:67], v[180:183], v[204:207], v[64:67]
	v_mfma_f32_16x16x32_bf16 v[60:63], v[188:191], v[204:207], v[60:63]
	v_mfma_f32_16x16x32_bf16 v[56:59], v[180:183], v[212:215], v[56:59]
	v_mfma_f32_16x16x32_bf16 v[52:55], v[188:191], v[212:215], v[52:55]
	v_mfma_f32_16x16x32_bf16 v[48:51], v[180:183], v[220:223], v[48:51]
	v_mfma_f32_16x16x32_bf16 v[44:47], v[188:191], v[220:223], v[44:47]
	s_setprio 0
	s_barrier
; #define PG8_STAGE2(bufoff, gbase, v0, v1) do { \
;         __builtin_amdgcn_global_load_lds((const unsigned*)((const char*)(gbase) + (v0)), (LAS unsigned*)(lds + (bufoff) + ldsw), 16, 0, 0); \
;         __builtin_amdgcn_global_load_lds((const unsigned*)((const char*)(gbase) + (v1)), (LAS unsigned*)(lds + (bufoff) + ldsw + 8192), 16, 0, 0); } while (0)
; #define PG8_STAGE(bufoff, gbase, voff) PG8_STAGE2(bufoff, gbase, (voff)[0], (voff)[1])
; #define PG8_LDA(dst, b, h) do { _Pragma("unroll") for (int m = 0; m < 4; ++m) _Pragma("unroll") for (int k = 0; k < 2; ++k) dst[m][k] = *(const LAS bf16x8*)(lds + PG8_SA(b, h) + aoff + m * 2048 + k * 1024); } while (0)
; #define PG8_LDB(dst, b, h) do { _Pragma("unroll") for (int n = 0; n < 2; ++n) _Pragma("unroll") for (int k = 0; k < 2; ++k) dst[n][k] = *(const LAS bf16x8*)(lds + PG8_SB(b, h) + boff + n * 2048 + k * 1024); } while (0)
; #define PG8_WAIT_V(n) asm volatile("s_waitcnt vmcnt(" #n ")" ::: "memory")
; #define PG8_WAIT_L(n) asm volatile("s_waitcnt lgkmcnt(" #n ")" ::: "memory")
; #define PG8_BAR __builtin_amdgcn_s_barrier()
; #define PG8_SCHED __builtin_amdgcn_sched_barrier(0)
; template <class Epi, class Sched, bool ALIGN_EPI, bool SP2, bool GATHER>
; DI void gemm_phase(LAS unsigned char* lds, const Gemm g, const Sched& S, const Epi& E) {
;     ...
;             PG8_LDB(B0, 0, 0); PG8_LDB(B1, 0, 1); PG8_SCHED; PG8_LDA(At, 0, 0); PG8_STAGE2(PG8_SA(1, 1), a1 + hstepA, gC[1][0], gC[1][1]);
;             PG8_WAIT_V(8); PG8_WAIT_L(0); PG8_BAR; PG8_MMA(0, 0, At, B0); PG8_MMA(0, 1, At, B1); PG8_BAR; PG8_SCHED;
;             PG8_LDA(At, 0, 1); PG8_STAGE(PG8_SB(0, 0), b2, voffB); PG8_STAGE(PG8_SB(0, 1), b2 + hstep, voffB); PG8_STAGE2(PG8_SA(0, 0), a2, x00, x01);
;             PG8_WAIT_V(8); PG8_WAIT_L(0); PG8_BAR; PG8_MMA(1, 0, At, B0); PG8_MMA(1, 1, At, B1); PG8_BAR; PG8_SCHED;
;             PG8_LDB(B0, 1, 0); PG8_LDB(B1, 1, 1); PG8_SCHED; PG8_LDA(At, 1, 0); PG8_STAGE2(PG8_SA(0, 1), a2 + hstepA, x10, x11);
;             PG8_WAIT_V(8); PG8_WAIT_L(0); PG8_BAR; PG8_MMA(0, 0, At, B0); PG8_MMA(0, 1, At, B1); PG8_BAR; PG8_SCHED;
;             PG8_LDA(At, 1, 1); PG8_STAGE(PG8_SB(1, 0), b3, voffB); PG8_STAGE(PG8_SB(1, 1), b3 + hstep, voffB); PG8_STAGE2(PG8_SA(1, 0), a3, x00, x01);
;             PG8_WAIT_V(8); PG8_WAIT_L(0); PG8_BAR; PG8_MMA(1, 0, At, B0); PG8_MMA(1, 1, At, B1); PG8_BAR; PG8_SCHED;
	s_add_i32 s14, s49, s66
	s_mov_b32 m0, s14
	ds_read_b128 v[192:195], v177 offset:49152
	ds_read_b128 v[196:199], v177 offset:50176
	ds_read_b128 v[200:203], v177 offset:51200
	ds_read_b128 v[204:207], v177 offset:52224
	ds_read_b128 v[208:211], v177 offset:53248
	ds_read_b128 v[212:215], v177 offset:54272
	ds_read_b128 v[216:219], v177 offset:55296
	ds_read_b128 v[220:223], v177 offset:56320
	global_load_lds_dwordx4 v142, s[98:99]
	s_add_i32 m0, s14, 0x2000
	s_add_u32 s12, s12, 0x80080
	s_addc_u32 s13, s13, 0
	s_add_i32 s14, s51, s66
	global_load_lds_dwordx4 v146, s[98:99]
	s_mov_b32 m0, s14
	s_nop 0
	global_load_lds_dwordx4 v142, s[12:13]
	s_add_i32 m0, s14, 0x2000
	s_nop 0
	global_load_lds_dwordx4 v146, s[12:13]
	s_mov_b32 m0, s73
	s_nop 0
	global_load_lds_dwordx4 v140, s[100:101]
	s_mov_b32 m0, s74
	s_nop 0
	global_load_lds_dwordx4 v144, s[100:101]
	s_waitcnt vmcnt(8)
	s_waitcnt lgkmcnt(0)
	s_barrier
	s_setprio 1
	s_waitcnt lgkmcnt(0)
	v_mfma_f32_16x16x32_bf16 v[104:107], v[76:79], v[192:195], v[104:107]
	v_mfma_f32_16x16x32_bf16 v[96:99], v[76:79], v[200:203], v[96:99]
	v_mfma_f32_16x16x32_bf16 v[88:91], v[76:79], v[208:211], v[88:91]
	v_mfma_f32_16x16x32_bf16 v[4:7], v[76:79], v[216:219], v[4:7]
	v_mfma_f32_16x16x32_bf16 v[104:107], v[80:83], v[196:199], v[104:107]
	v_mfma_f32_16x16x32_bf16 v[100:103], v[158:161], v[192:195], v[100:103]
	v_mfma_f32_16x16x32_bf16 v[96:99], v[80:83], v[204:207], v[96:99]
	v_mfma_f32_16x16x32_bf16 v[92:95], v[158:161], v[200:203], v[92:95]
	v_mfma_f32_16x16x32_bf16 v[88:91], v[80:83], v[212:215], v[88:91]
	v_mfma_f32_16x16x32_bf16 v[84:87], v[158:161], v[208:211], v[84:87]
	v_mfma_f32_16x16x32_bf16 v[80:83], v[80:83], v[220:223], v[4:7]
	v_mfma_f32_16x16x32_bf16 v[4:7], v[158:161], v[216:219], v[8:11]
	v_mfma_f32_16x16x32_bf16 v[100:103], v[162:165], v[196:199], v[100:103]
	v_mfma_f32_16x16x32_bf16 v[92:95], v[162:165], v[204:207], v[92:95]
	v_mfma_f32_16x16x32_bf16 v[84:87], v[162:165], v[212:215], v[84:87]
	v_mfma_f32_16x16x32_bf16 v[76:79], v[162:165], v[220:223], v[4:7]
	s_setprio 0
	s_setprio 1
	v_mfma_f32_16x16x32_bf16 v[4:7], v[166:169], v[192:195], v[40:43]
	v_mfma_f32_16x16x32_bf16 v[40:43], v[180:183], v[196:199], v[4:7]
	v_mfma_f32_16x16x32_bf16 v[4:7], v[184:187], v[192:195], v[36:39]
	v_mfma_f32_16x16x32_bf16 v[36:39], v[188:191], v[196:199], v[4:7]
	v_mfma_f32_16x16x32_bf16 v[4:7], v[166:169], v[200:203], v[32:35]
	v_mfma_f32_16x16x32_bf16 v[32:35], v[180:183], v[204:207], v[4:7]
	v_mfma_f32_16x16x32_bf16 v[4:7], v[184:187], v[200:203], v[28:31]
	v_mfma_f32_16x16x32_bf16 v[28:31], v[188:191], v[204:207], v[4:7]
	v_mfma_f32_16x16x32_bf16 v[4:7], v[166:169], v[208:211], v[24:27]
	v_mfma_f32_16x16x32_bf16 v[24:27], v[180:183], v[212:215], v[4:7]
	v_mfma_f32_16x16x32_bf16 v[4:7], v[184:187], v[208:211], v[20:23]
	v_mfma_f32_16x16x32_bf16 v[20:23], v[188:191], v[212:215], v[4:7]
	v_mfma_f32_16x16x32_bf16 v[4:7], v[166:169], v[216:219], v[16:19]
	v_mfma_f32_16x16x32_bf16 v[16:19], v[180:183], v[220:223], v[4:7]
	v_mfma_f32_16x16x32_bf16 v[4:7], v[184:187], v[216:219], v[12:15]
	v_mfma_f32_16x16x32_bf16 v[12:15], v[188:191], v[220:223], v[4:7]
	s_setprio 0
	s_barrier
	s_add_i32 s39, s39, 2
	s_add_u32 s10, s10, 0x100
	s_addc_u32 s11, s11, 0
	s_add_u32 s22, s22, 0x100
	s_addc_u32 s38, s38, 0
	s_cmp_gt_u32 s39, 29
	s_cbranch_scc1 .Lpeel_exit_p1
.LBB0_103:
	ds_read_b128 v[4:7], v175
	ds_read_b128 v[8:11], v175 offset:1024
	ds_read_b128 v[158:161], v175 offset:2048
	ds_read_b128 v[162:165], v175 offset:3072
	ds_read_b128 v[166:169], v176
	ds_read_b128 v[180:183], v176 offset:1024
	ds_read_b128 v[184:187], v176 offset:2048
	ds_read_b128 v[188:191], v176 offset:3072
	s_add_u32 s12, s10, 0xfff80080
	s_addc_u32 s13, s11, -1
	s_cmp_eq_u32 s39, 28
	s_cselect_b32 s15, s5, s13
	s_cselect_b32 s14, s7, s12
	s_cselect_b32 s13, s16, s38
	s_cselect_b32 s12, s17, s22
	s_add_i32 m0, s67, 0xc000
	ds_read_b128 v[192:195], v177
	ds_read_b128 v[196:199], v177 offset:1024
	ds_read_b128 v[200:203], v177 offset:2048
	ds_read_b128 v[204:207], v177 offset:3072
	ds_read_b128 v[208:211], v177 offset:4096
	ds_read_b128 v[212:215], v177 offset:5120
	ds_read_b128 v[216:219], v177 offset:6144
	ds_read_b128 v[220:223], v177 offset:7168
	global_load_lds_dwordx4 v150, s[10:11]
	s_add_i32 m0, s67, 0xe000
	s_nop 0
	global_load_lds_dwordx4 v152, s[10:11]
	s_waitcnt vmcnt(8)
	s_waitcnt lgkmcnt(0)
	s_barrier
	s_setprio 1
	s_waitcnt lgkmcnt(0)
	s_nop 0
	v_mfma_f32_16x16x32_bf16 v[136:139], v[4:7], v[192:195], v[136:139]
	v_mfma_f32_16x16x32_bf16 v[132:135], v[158:161], v[192:195], v[132:135]
	v_mfma_f32_16x16x32_bf16 v[128:131], v[4:7], v[200:203], v[128:131]
	v_mfma_f32_16x16x32_bf16 v[124:127], v[158:161], v[200:203], v[124:127]
	v_mfma_f32_16x16x32_bf16 v[120:123], v[4:7], v[208:211], v[120:123]
	v_mfma_f32_16x16x32_bf16 v[116:119], v[158:161], v[208:211], v[116:119]
	v_mfma_f32_16x16x32_bf16 v[112:115], v[4:7], v[216:219], v[112:115]
	v_mfma_f32_16x16x32_bf16 v[108:111], v[158:161], v[216:219], v[108:111]
	v_mfma_f32_16x16x32_bf16 v[136:139], v[8:11], v[196:199], v[136:139]
	v_mfma_f32_16x16x32_bf16 v[132:135], v[162:165], v[196:199], v[132:135]
	v_mfma_f32_16x16x32_bf16 v[128:131], v[8:11], v[204:207], v[128:131]
	v_mfma_f32_16x16x32_bf16 v[124:127], v[162:165], v[204:207], v[124:127]
	v_mfma_f32_16x16x32_bf16 v[120:123], v[8:11], v[212:215], v[120:123]
	v_mfma_f32_16x16x32_bf16 v[116:119], v[162:165], v[212:215], v[116:119]
	v_mfma_f32_16x16x32_bf16 v[112:115], v[8:11], v[220:223], v[112:115]
	v_mfma_f32_16x16x32_bf16 v[108:111], v[162:165], v[220:223], v[108:111]
	s_setprio 0
	s_setprio 1
	v_mfma_f32_16x16x32_bf16 v[72:75], v[166:169], v[192:195], v[72:75]
	v_mfma_f32_16x16x32_bf16 v[68:71], v[184:187], v[192:195], v[68:71]
	v_mfma_f32_16x16x32_bf16 v[64:67], v[166:169], v[200:203], v[64:67]
	v_mfma_f32_16x16x32_bf16 v[60:63], v[184:187], v[200:203], v[60:63]
	v_mfma_f32_16x16x32_bf16 v[56:59], v[166:169], v[208:211], v[56:59]
	v_mfma_f32_16x16x32_bf16 v[52:55], v[184:187], v[208:211], v[52:55]
	v_mfma_f32_16x16x32_bf16 v[48:51], v[166:169], v[216:219], v[48:51]
	v_mfma_f32_16x16x32_bf16 v[44:47], v[184:187], v[216:219], v[44:47]
	v_mfma_f32_16x16x32_bf16 v[72:75], v[180:183], v[196:199], v[72:75]
	v_mfma_f32_16x16x32_bf16 v[68:71], v[188:191], v[196:199], v[68:71]
	v_mfma_f32_16x16x32_bf16 v[64:67], v[180:183], v[204:207], v[64:67]
	v_mfma_f32_16x16x32_bf16 v[60:63], v[188:191], v[204:207], v[60:63]
	v_mfma_f32_16x16x32_bf16 v[56:59], v[180:183], v[212:215], v[56:59]
	v_mfma_f32_16x16x32_bf16 v[52:55], v[188:191], v[212:215], v[52:55]
	v_mfma_f32_16x16x32_bf16 v[48:51], v[180:183], v[220:223], v[48:51]
	v_mfma_f32_16x16x32_bf16 v[44:47], v[188:191], v[220:223], v[44:47]
	s_setprio 0
	s_barrier
; #define PG8_STAGE2(bufoff, gbase, v0, v1) do { \
;         __builtin_amdgcn_global_load_lds((const unsigned*)((const char*)(gbase) + (v0)), (LAS unsigned*)(lds + (bufoff) + ldsw), 16, 0, 0); \
;         __builtin_amdgcn_global_load_lds((const unsigned*)((const char*)(gbase) + (v1)), (LAS unsigned*)(lds + (bufoff) + ldsw + 8192), 16, 0, 0); } while (0)
; #define PG8_STAGE(bufoff, gbase, voff) PG8_STAGE2(bufoff, gbase, (voff)[0], (voff)[1])
; #define PG8_LDA(dst, b, h) do { _Pragma("unroll") for (int m = 0; m < 4; ++m) _Pragma("unroll") for (int k = 0; k < 2; ++k) dst[m][k] = *(const LAS bf16x8*)(lds + PG8_SA(b, h) + aoff + m * 2048 + k * 1024); } while (0)
; #define PG8_LDB(dst, b, h) do { _Pragma("unroll") for (int n = 0; n < 2; ++n) _Pragma("unroll") for (int k = 0; k < 2; ++k) dst[n][k] = *(const LAS bf16x8*)(lds + PG8_SB(b, h) + boff + n * 2048 + k * 1024); } while (0)
; #define PG8_MMA(ai, bj, At, Bt) do { __builtin_amdgcn_s_setprio(1); _Pragma("unroll") for (int m = 0; m < 4; ++m) _Pragma("unroll") for (int n = 0; n < 2; ++n) _Pragma("unroll") for (int k = 0; k < 2; ++k) \
;         acc[ai][bj][m][n] = __builtin_amdgcn_mfma_f32_16x16x32_bf16(Bt[n][k], At[m][k], acc[ai][bj][m][n], 0, 0, 0); __builtin_amdgcn_s_setprio(0); } while (0)
; #define PG8_WAIT_V(n) asm volatile("s_waitcnt vmcnt(" #n ")" ::: "memory")
; #define PG8_WAIT_L(n) asm volatile("s_waitcnt lgkmcnt(" #n ")" ::: "memory")
; #define PG8_BAR __builtin_amdgcn_s_barrier()
; #define PG8_SCHED __builtin_amdgcn_sched_barrier(0)
; template <class Epi, class Sched, bool ALIGN_EPI, bool SP2, bool GATHER>
; DI void gemm_phase(LAS unsigned char* lds, const Gemm g, const Sched& S, const Epi& E) {
;     ...
;             PG8_LDA(At, 0, 1); PG8_STAGE(PG8_SB(0, 0), b2, voffB); PG8_STAGE(PG8_SB(0, 1), b2 + hstep, voffB); PG8_STAGE2(PG8_SA(0, 0), a2, x00, x01);
;             PG8_WAIT_V(8); PG8_WAIT_L(0); PG8_BAR; PG8_MMA(1, 0, At, B0); PG8_MMA(1, 1, At, B1); PG8_BAR; PG8_SCHED;
;             PG8_LDB(B0, 1, 0); PG8_LDB(B1, 1, 1); PG8_SCHED; PG8_LDA(At, 1, 0); PG8_STAGE2(PG8_SA(0, 1), a2 + hstepA, x10, x11);
;             PG8_WAIT_V(8); PG8_WAIT_L(0); PG8_BAR; PG8_MMA(0, 0, At, B0); PG8_MMA(0, 1, At, B1); PG8_BAR; PG8_SCHED;
	s_add_i32 s49, s78, s66
	s_add_u32 s98, s12, 0x80
	s_addc_u32 s99, s13, 0
	s_mov_b32 m0, s49
	ds_read_b128 v[192:195], v177 offset:16384
	ds_read_b128 v[196:199], v177 offset:17408
	ds_read_b128 v[200:203], v177 offset:18432
	ds_read_b128 v[204:207], v177 offset:19456
	ds_read_b128 v[208:211], v177 offset:20480
	ds_read_b128 v[212:215], v177 offset:21504
	ds_read_b128 v[216:219], v177 offset:22528
	ds_read_b128 v[220:223], v177 offset:23552
	global_load_lds_dwordx4 v142, s[12:13]
	s_add_i32 m0, s49, 0x2000
	s_add_u32 s56, s12, 0x80000
	s_addc_u32 s57, s13, 0
	s_add_i32 s49, s79, s66
	global_load_lds_dwordx4 v146, s[12:13]
	s_mov_b32 m0, s49
	s_add_u32 s100, s14, 0x80
	s_addc_u32 s101, s15, 0
	global_load_lds_dwordx4 v142, s[56:57]
	s_add_i32 m0, s49, 0x2000
	s_nop 0
	global_load_lds_dwordx4 v146, s[56:57]
	s_mov_b32 m0, s67
	s_nop 0
	global_load_lds_dwordx4 v140, s[14:15]
	s_mov_b32 m0, s68
	s_nop 0
	global_load_lds_dwordx4 v144, s[14:15]
	s_waitcnt vmcnt(8)
	s_waitcnt lgkmcnt(0)
	s_barrier
	s_setprio 1
	s_waitcnt lgkmcnt(0)
	s_nop 0
	v_mfma_f32_16x16x32_bf16 v[104:107], v[4:7], v[192:195], v[104:107]
	v_mfma_f32_16x16x32_bf16 v[100:103], v[158:161], v[192:195], v[100:103]
	v_mfma_f32_16x16x32_bf16 v[96:99], v[4:7], v[200:203], v[96:99]
	v_mfma_f32_16x16x32_bf16 v[92:95], v[158:161], v[200:203], v[92:95]
	v_mfma_f32_16x16x32_bf16 v[88:91], v[4:7], v[208:211], v[88:91]
	v_mfma_f32_16x16x32_bf16 v[84:87], v[158:161], v[208:211], v[84:87]
	v_mfma_f32_16x16x32_bf16 v[4:7], v[4:7], v[216:219], v[80:83]
	v_mfma_f32_16x16x32_bf16 v[104:107], v[8:11], v[196:199], v[104:107]
	v_mfma_f32_16x16x32_bf16 v[100:103], v[162:165], v[196:199], v[100:103]
	v_mfma_f32_16x16x32_bf16 v[96:99], v[8:11], v[204:207], v[96:99]
	v_mfma_f32_16x16x32_bf16 v[92:95], v[162:165], v[204:207], v[92:95]
	v_mfma_f32_16x16x32_bf16 v[88:91], v[8:11], v[212:215], v[88:91]
	v_mfma_f32_16x16x32_bf16 v[84:87], v[162:165], v[212:215], v[84:87]
	v_mfma_f32_16x16x32_bf16 v[4:7], v[8:11], v[220:223], v[4:7]
	v_mfma_f32_16x16x32_bf16 v[8:11], v[158:161], v[216:219], v[76:79]
	v_mfma_f32_16x16x32_bf16 v[8:11], v[162:165], v[220:223], v[8:11]
	s_setprio 0
	s_setprio 1
	v_mfma_f32_16x16x32_bf16 v[40:43], v[166:169], v[192:195], v[40:43]
	v_mfma_f32_16x16x32_bf16 v[36:39], v[184:187], v[192:195], v[36:39]
	v_mfma_f32_16x16x32_bf16 v[32:35], v[166:169], v[200:203], v[32:35]
	v_mfma_f32_16x16x32_bf16 v[28:31], v[184:187], v[200:203], v[28:31]
	v_mfma_f32_16x16x32_bf16 v[24:27], v[166:169], v[208:211], v[24:27]
	v_mfma_f32_16x16x32_bf16 v[20:23], v[184:187], v[208:211], v[20:23]
	v_mfma_f32_16x16x32_bf16 v[16:19], v[166:169], v[216:219], v[16:19]
	v_mfma_f32_16x16x32_bf16 v[12:15], v[184:187], v[216:219], v[12:15]
	v_mfma_f32_16x16x32_bf16 v[40:43], v[180:183], v[196:199], v[40:43]
	v_mfma_f32_16x16x32_bf16 v[36:39], v[188:191], v[196:199], v[36:39]
	v_mfma_f32_16x16x32_bf16 v[32:35], v[180:183], v[204:207], v[32:35]
	v_mfma_f32_16x16x32_bf16 v[28:31], v[188:191], v[204:207], v[28:31]
	v_mfma_f32_16x16x32_bf16 v[24:27], v[180:183], v[212:215], v[24:27]
	v_mfma_f32_16x16x32_bf16 v[20:23], v[188:191], v[212:215], v[20:23]
	v_mfma_f32_16x16x32_bf16 v[16:19], v[180:183], v[220:223], v[16:19]
	v_mfma_f32_16x16x32_bf16 v[12:15], v[188:191], v[220:223], v[12:15]
	s_setprio 0
	s_barrier
	s_add_i32 s49, 0, 0x18000
	v_add_u32_e32 v3, s49, v172
	s_add_i32 s51, 0, 0x1c000
	ds_read_b128 v[76:79], v3
	ds_read_b128 v[80:83], v3 offset:1024
	ds_read_b128 v[158:161], v3 offset:2048
	ds_read_b128 v[162:165], v3 offset:3072
	v_add_u32_e32 v3, s51, v172
	ds_read_b128 v[166:169], v3
	ds_read_b128 v[180:183], v3 offset:1024
	ds_read_b128 v[184:187], v3 offset:2048
	ds_read_b128 v[188:191], v3 offset:3072
	s_add_u32 s14, s14, 0x80000
	s_addc_u32 s15, s15, 0
	s_mov_b32 m0, s69
	ds_read_b128 v[192:195], v177 offset:32768
	ds_read_b128 v[196:199], v177 offset:33792
	ds_read_b128 v[200:203], v177 offset:34816
	ds_read_b128 v[204:207], v177 offset:35840
	ds_read_b128 v[208:211], v177 offset:36864
	ds_read_b128 v[212:215], v177 offset:37888
	ds_read_b128 v[216:219], v177 offset:38912
	ds_read_b128 v[220:223], v177 offset:39936
	global_load_lds_dwordx4 v140, s[14:15]
	s_mov_b32 m0, s70
	s_nop 0
	global_load_lds_dwordx4 v144, s[14:15]
	s_waitcnt vmcnt(8)
	s_waitcnt lgkmcnt(0)
	s_barrier
; #define PG8_STAGE2(bufoff, gbase, v0, v1) do { \
;         __builtin_amdgcn_global_load_lds((const unsigned*)((const char*)(gbase) + (v0)), (LAS unsigned*)(lds + (bufoff) + ldsw), 16, 0, 0); \
;         __builtin_amdgcn_global_load_lds((const unsigned*)((const char*)(gbase) + (v1)), (LAS unsigned*)(lds + (bufoff) + ldsw + 8192), 16, 0, 0); } while (0)
; #define PG8_STAGE(bufoff, gbase, voff) PG8_STAGE2(bufoff, gbase, (voff)[0], (voff)[1])
; #define PG8_LDA(dst, b, h) do { _Pragma("unroll") for (int m = 0; m < 4; ++m) _Pragma("unroll") for (int k = 0; k < 2; ++k) dst[m][k] = *(const LAS bf16x8*)(lds + PG8_SA(b, h) + aoff + m * 2048 + k * 1024); } while (0)
; #define PG8_MMA(ai, bj, At, Bt) do { __builtin_amdgcn_s_setprio(1); _Pragma("unroll") for (int m = 0; m < 4; ++m) _Pragma("unroll") for (int n = 0; n < 2; ++n) _Pragma("unroll") for (int k = 0; k < 2; ++k) \
;         acc[ai][bj][m][n] = __builtin_amdgcn_mfma_f32_16x16x32_bf16(Bt[n][k], At[m][k], acc[ai][bj][m][n], 0, 0, 0); __builtin_amdgcn_s_setprio(0); } while (0)
; #define PG8_WAIT_V(n) asm volatile("s_waitcnt vmcnt(" #n ")" ::: "memory")
; #define PG8_WAIT_L(n) asm volatile("s_waitcnt lgkmcnt(" #n ")" ::: "memory")
; #define PG8_BAR __builtin_amdgcn_s_barrier()
; #define PG8_SCHED __builtin_amdgcn_sched_barrier(0)
; template <class Epi, class Sched, bool ALIGN_EPI, bool SP2, bool GATHER>
; DI void gemm_phase(LAS unsigned char* lds, const Gemm g, const Sched& S, const Epi& E) {
;     ...
;             PG8_WAIT_V(8); PG8_WAIT_L(0); PG8_BAR; PG8_MMA(0, 0, At, B0); PG8_MMA(0, 1, At, B1); PG8_BAR; PG8_SCHED;
;             PG8_LDA(At, 1, 1); PG8_STAGE(PG8_SB(1, 0), b3, voffB); PG8_STAGE(PG8_SB(1, 1), b3 + hstep, voffB); PG8_STAGE2(PG8_SA(1, 0), a3, x00, x01);
;             PG8_WAIT_V(8); PG8_WAIT_L(0); PG8_BAR; PG8_MMA(1, 0, At, B0); PG8_MMA(1, 1, At, B1); PG8_BAR; PG8_SCHED;
;         }
	s_setprio 1
	s_waitcnt lgkmcnt(0)
	s_nop 0
	v_mfma_f32_16x16x32_bf16 v[136:139], v[76:79], v[192:195], v[136:139]
	v_mfma_f32_16x16x32_bf16 v[132:135], v[158:161], v[192:195], v[132:135]
	v_mfma_f32_16x16x32_bf16 v[128:131], v[76:79], v[200:203], v[128:131]
	v_mfma_f32_16x16x32_bf16 v[124:127], v[158:161], v[200:203], v[124:127]
	v_mfma_f32_16x16x32_bf16 v[120:123], v[76:79], v[208:211], v[120:123]
	v_mfma_f32_16x16x32_bf16 v[116:119], v[158:161], v[208:211], v[116:119]
	v_mfma_f32_16x16x32_bf16 v[112:115], v[76:79], v[216:219], v[112:115]
	v_mfma_f32_16x16x32_bf16 v[108:111], v[158:161], v[216:219], v[108:111]
	v_mfma_f32_16x16x32_bf16 v[136:139], v[80:83], v[196:199], v[136:139]
	v_mfma_f32_16x16x32_bf16 v[132:135], v[162:165], v[196:199], v[132:135]
	v_mfma_f32_16x16x32_bf16 v[128:131], v[80:83], v[204:207], v[128:131]
	v_mfma_f32_16x16x32_bf16 v[124:127], v[162:165], v[204:207], v[124:127]
	v_mfma_f32_16x16x32_bf16 v[120:123], v[80:83], v[212:215], v[120:123]
	v_mfma_f32_16x16x32_bf16 v[116:119], v[162:165], v[212:215], v[116:119]
	v_mfma_f32_16x16x32_bf16 v[112:115], v[80:83], v[220:223], v[112:115]
	v_mfma_f32_16x16x32_bf16 v[108:111], v[162:165], v[220:223], v[108:111]
	s_setprio 0
	s_setprio 1
	v_mfma_f32_16x16x32_bf16 v[72:75], v[166:169], v[192:195], v[72:75]
	v_mfma_f32_16x16x32_bf16 v[68:71], v[184:187], v[192:195], v[68:71]
	v_mfma_f32_16x16x32_bf16 v[64:67], v[166:169], v[200:203], v[64:67]
	v_mfma_f32_16x16x32_bf16 v[60:63], v[184:187], v[200:203], v[60:63]
	v_mfma_f32_16x16x32_bf16 v[56:59], v[166:169], v[208:211], v[56:59]
	v_mfma_f32_16x16x32_bf16 v[52:55], v[184:187], v[208:211], v[52:55]
	v_mfma_f32_16x16x32_bf16 v[48:51], v[166:169], v[216:219], v[48:51]
	v_mfma_f32_16x16x32_bf16 v[44:47], v[184:187], v[216:219], v[44:47]
	v_mfma_f32_16x16x32_bf16 v[72:75], v[180:183], v[196:199], v[72:75]
	v_mfma_f32_16x16x32_bf16 v[68:71], v[188:191], v[196:199], v[68:71]
	v_mfma_f32_16x16x32_bf16 v[64:67], v[180:183], v[204:207], v[64:67]
	v_mfma_f32_16x16x32_bf16 v[60:63], v[188:191], v[204:207], v[60:63]
	v_mfma_f32_16x16x32_bf16 v[56:59], v[180:183], v[212:215], v[56:59]
	v_mfma_f32_16x16x32_bf16 v[52:55], v[188:191], v[212:215], v[52:55]
	v_mfma_f32_16x16x32_bf16 v[48:51], v[180:183], v[220:223], v[48:51]
	v_mfma_f32_16x16x32_bf16 v[44:47], v[188:191], v[220:223], v[44:47]
	s_setprio 0
	s_barrier
	s_add_i32 s14, s49, s66
	s_mov_b32 m0, s14
	ds_read_b128 v[192:195], v177 offset:49152
	ds_read_b128 v[196:199], v177 offset:50176
	ds_read_b128 v[200:203], v177 offset:51200
	ds_read_b128 v[204:207], v177 offset:52224
	ds_read_b128 v[208:211], v177 offset:53248
	ds_read_b128 v[212:215], v177 offset:54272
	ds_read_b128 v[216:219], v177 offset:55296
	ds_read_b128 v[220:223], v177 offset:56320
	global_load_lds_dwordx4 v142, s[98:99]
	s_add_i32 m0, s14, 0x2000
	s_add_u32 s12, s12, 0x80080
	s_addc_u32 s13, s13, 0
	s_add_i32 s14, s51, s66
	global_load_lds_dwordx4 v146, s[98:99]
	s_mov_b32 m0, s14
	s_nop 0
	global_load_lds_dwordx4 v142, s[12:13]
	s_add_i32 m0, s14, 0x2000
	s_nop 0
	global_load_lds_dwordx4 v146, s[12:13]
	s_mov_b32 m0, s73
	s_nop 0
	global_load_lds_dwordx4 v140, s[100:101]
	s_mov_b32 m0, s74
	s_nop 0
	global_load_lds_dwordx4 v144, s[100:101]
	s_waitcnt vmcnt(8)
	s_waitcnt lgkmcnt(0)
	s_barrier
	s_setprio 1
	s_waitcnt lgkmcnt(0)
	v_mfma_f32_16x16x32_bf16 v[104:107], v[76:79], v[192:195], v[104:107]
	v_mfma_f32_16x16x32_bf16 v[96:99], v[76:79], v[200:203], v[96:99]
	v_mfma_f32_16x16x32_bf16 v[88:91], v[76:79], v[208:211], v[88:91]
	v_mfma_f32_16x16x32_bf16 v[4:7], v[76:79], v[216:219], v[4:7]
	v_mfma_f32_16x16x32_bf16 v[104:107], v[80:83], v[196:199], v[104:107]
	v_mfma_f32_16x16x32_bf16 v[100:103], v[158:161], v[192:195], v[100:103]
	v_mfma_f32_16x16x32_bf16 v[96:99], v[80:83], v[204:207], v[96:99]
	v_mfma_f32_16x16x32_bf16 v[92:95], v[158:161], v[200:203], v[92:95]
	v_mfma_f32_16x16x32_bf16 v[88:91], v[80:83], v[212:215], v[88:91]
	v_mfma_f32_16x16x32_bf16 v[84:87], v[158:161], v[208:211], v[84:87]
	v_mfma_f32_16x16x32_bf16 v[80:83], v[80:83], v[220:223], v[4:7]
	v_mfma_f32_16x16x32_bf16 v[4:7], v[158:161], v[216:219], v[8:11]
	v_mfma_f32_16x16x32_bf16 v[100:103], v[162:165], v[196:199], v[100:103]
	v_mfma_f32_16x16x32_bf16 v[92:95], v[162:165], v[204:207], v[92:95]
	v_mfma_f32_16x16x32_bf16 v[84:87], v[162:165], v[212:215], v[84:87]
	v_mfma_f32_16x16x32_bf16 v[76:79], v[162:165], v[220:223], v[4:7]
	s_setprio 0
	s_setprio 1
	v_mfma_f32_16x16x32_bf16 v[4:7], v[166:169], v[192:195], v[40:43]
	v_mfma_f32_16x16x32_bf16 v[40:43], v[180:183], v[196:199], v[4:7]
	v_mfma_f32_16x16x32_bf16 v[4:7], v[184:187], v[192:195], v[36:39]
	v_mfma_f32_16x16x32_bf16 v[36:39], v[188:191], v[196:199], v[4:7]
	v_mfma_f32_16x16x32_bf16 v[4:7], v[166:169], v[200:203], v[32:35]
	v_mfma_f32_16x16x32_bf16 v[32:35], v[180:183], v[204:207], v[4:7]
	v_mfma_f32_16x16x32_bf16 v[4:7], v[184:187], v[200:203], v[28:31]
	v_mfma_f32_16x16x32_bf16 v[28:31], v[188:191], v[204:207], v[4:7]
	v_mfma_f32_16x16x32_bf16 v[4:7], v[166:169], v[208:211], v[24:27]
	v_mfma_f32_16x16x32_bf16 v[24:27], v[180:183], v[212:215], v[4:7]
	v_mfma_f32_16x16x32_bf16 v[4:7], v[184:187], v[208:211], v[20:23]
	v_mfma_f32_16x16x32_bf16 v[20:23], v[188:191], v[212:215], v[4:7]
	v_mfma_f32_16x16x32_bf16 v[4:7], v[166:169], v[216:219], v[16:19]
	v_mfma_f32_16x16x32_bf16 v[16:19], v[180:183], v[220:223], v[4:7]
	v_mfma_f32_16x16x32_bf16 v[4:7], v[184:187], v[216:219], v[12:15]
	v_mfma_f32_16x16x32_bf16 v[12:15], v[188:191], v[220:223], v[4:7]
	s_setprio 0
	s_barrier
	s_add_i32 s39, s39, 2
	s_add_u32 s10, s10, 0x100
	s_addc_u32 s11, s11, 0
	s_add_u32 s22, s22, 0x100
	s_addc_u32 s38, s38, 0
	s_cmp_gt_u32 s39, 29
	s_cbranch_scc0 .LBB0_103

; #define LDS_WAIT() asm volatile("s_waitcnt lgkmcnt(0)" ::: "memory")
; DI int crow(int reg, int h) { return (reg & 3) + 8 * (reg >> 2) + 4 * h; }
; #define MFMA32(a, b, c) __builtin_amdgcn_mfma_f32_32x32x16_bf16((a), (b), (c), 0, 0, 0)
; #define P3_LOADV(buf, t_) do { const GAS char* vp_ = vb_u + (long)(t_) * 8192; _Pragma("unroll") for (int s2 = 0; s2 < 2; ++s2) _Pragma("unroll") for (int db = 0; db < 4; ++db) vf[buf][db][s2] = *(const GAS u32x4*)(vp_ + (s2 * 4 + db) * 1024 + voff); } while (0)
; DI void p3_attn_mfma(Frame& F, ArgsP A) {
;     ...
;             if (t >= tlo) {
;                 if (t == tlo) P3_LOADV(t & 1, t);
;                 f32x16 acc;
; #pragma unroll
;                 for (int i = 0; i < 16; ++i) acc[i] = tb[32 + (128 - 32 * t + rq - crow(i, h))];
;                 LDS_WAIT(); __builtin_amdgcn_sched_barrier(0);
; #pragma unroll
;                 for (int st = 0; st < 8; ++st) acc = MFMA32(kf[st], qf[st], acc);
;                 __builtin_amdgcn_sched_barrier(0);
;                 float tm = -3.0e38f;
; #pragma unroll
;                 for (int i = 0; i < 16; ++i) {
;                     const int key = crow(i, h);
;                     const bool valid = (t == 0) ? (key >= rq) : ((t == 4) ? (key <= rq) : true);
;                     acc[i] = valid ? acc[i] : -3.0e38f; tm = fmaxf(tm, acc[i]);
;                 }
;                 tm = fmaxf(tm, __shfl_xor(tm, 32));
.LBB0_460:
	v_lshl_add_u32 v2, v241, 2, v237
	ds_read2_b32 v[6:7], v2 offset0:159 offset1:160
	ds_read2_b32 v[8:9], v2 offset0:157 offset1:158
	ds_read2_b32 v[10:11], v2 offset0:151 offset1:152
	ds_read2_b32 v[12:13], v2 offset0:149 offset1:150
	ds_read2_b32 v[14:15], v2 offset0:143 offset1:144
	ds_read2_b32 v[16:17], v2 offset0:141 offset1:142
	ds_read2_b32 v[18:19], v2 offset0:135 offset1:136
	ds_read2_b32 v[20:21], v2 offset0:133 offset1:134
	s_waitcnt lgkmcnt(0)
	s_waitcnt lgkmcnt(7)
	v_mov_b32_e32 v4, v7
	v_mov_b32_e32 v5, v6
	s_waitcnt lgkmcnt(6)
	v_mov_b32_e32 v6, v9
	v_mov_b32_e32 v7, v8
	s_waitcnt lgkmcnt(5)
	v_mov_b32_e32 v8, v11
	v_mov_b32_e32 v9, v10
	s_waitcnt lgkmcnt(4)
	v_mov_b32_e32 v10, v13
	v_mov_b32_e32 v11, v12
	s_waitcnt lgkmcnt(3)
	v_mov_b32_e32 v12, v15
	v_mov_b32_e32 v13, v14
	s_waitcnt lgkmcnt(2)
	v_mov_b32_e32 v14, v17
	v_mov_b32_e32 v15, v16
	s_waitcnt lgkmcnt(1)
	v_mov_b32_e32 v16, v19
	v_mov_b32_e32 v17, v18
	s_waitcnt lgkmcnt(0)
	v_mov_b32_e32 v18, v21
	v_mov_b32_e32 v19, v20
	s_nop 1
	s_nop 0
	v_mfma_f32_32x32x16_bf16 v[4:19], v[208:211], v[172:175], v[4:19]
	v_mfma_f32_32x32x16_bf16 v[4:19], v[204:207], v[164:167], v[4:19]
	v_mfma_f32_32x32x16_bf16 v[4:19], v[200:203], v[156:159], v[4:19]
	v_mfma_f32_32x32x16_bf16 v[4:19], v[196:199], v[148:151], v[4:19]
	v_mfma_f32_32x32x16_bf16 v[4:19], v[192:195], v[176:179], v[4:19]
	v_mfma_f32_32x32x16_bf16 v[4:19], v[188:191], v[168:171], v[4:19]
	v_mfma_f32_32x32x16_bf16 v[4:19], v[184:187], v[160:163], v[4:19]
	v_mfma_f32_32x32x16_bf16 v[4:19], v[180:183], v[152:155], v[4:19]
	v_cmp_ge_i32_e32 vcc, v220, v241
	v_and_b32_e32 v21, 64, v239
	v_xor_b32_e32 v20, 32, v239
	s_nop 8
	v_cndmask_b32_e32 v2, v238, v4, vcc
	v_cmp_ge_i32_e32 vcc, v222, v241
	v_add_u32_e32 v21, 64, v21
	s_nop 0
	v_cndmask_b32_e32 v4, v238, v5, vcc
	v_cmp_ge_i32_e32 vcc, v223, v241
	v_max3_f32 v5, v2, s53, v4
	s_nop 0
	v_cndmask_b32_e32 v6, v238, v6, vcc
	v_cmp_ge_i32_e32 vcc, v224, v241
	s_nop 1
	v_cndmask_b32_e32 v7, v238, v7, vcc
	v_cmp_ge_i32_e32 vcc, v225, v241
	v_max3_f32 v5, v5, v6, v7
	s_nop 0
	v_cndmask_b32_e32 v8, v238, v8, vcc
	v_cmp_ge_i32_e32 vcc, v226, v241
	s_nop 1
	v_cndmask_b32_e32 v9, v238, v9, vcc
	v_cmp_ge_i32_e32 vcc, v227, v241
	v_max3_f32 v5, v5, v8, v9
	s_nop 0
	v_cndmask_b32_e32 v10, v238, v10, vcc
	v_cmp_ge_i32_e32 vcc, v228, v241
	s_nop 1
	v_cndmask_b32_e32 v11, v238, v11, vcc
	v_cmp_ge_i32_e32 vcc, v229, v241
	v_max3_f32 v5, v5, v10, v11
	s_nop 0
	v_cndmask_b32_e32 v12, v238, v12, vcc
	v_cmp_ge_i32_e32 vcc, v230, v241
	s_nop 1
	v_cndmask_b32_e32 v13, v238, v13, vcc
	v_cmp_ge_i32_e32 vcc, v231, v241
	v_max3_f32 v5, v5, v12, v13
	s_nop 0
	v_cndmask_b32_e32 v14, v238, v14, vcc
	v_cmp_ge_i32_e32 vcc, v232, v241
	s_nop 1
	v_cndmask_b32_e32 v15, v238, v15, vcc
	v_cmp_ge_i32_e32 vcc, v233, v241
	v_max3_f32 v5, v5, v14, v15
	s_nop 0
	v_cndmask_b32_e32 v16, v238, v16, vcc
	v_cmp_ge_i32_e32 vcc, v234, v241
	s_nop 1
	v_cndmask_b32_e32 v17, v238, v17, vcc
	v_cmp_ge_i32_e32 vcc, v235, v241
	v_max3_f32 v5, v5, v16, v17
	s_nop 0
	v_cndmask_b32_e32 v18, v238, v18, vcc
	v_cmp_ge_i32_e32 vcc, v236, v241
	s_nop 1
	v_cndmask_b32_e32 v19, v238, v19, vcc
	v_cmp_lt_i32_e32 vcc, v20, v21
	v_max3_f32 v5, v5, v18, v19
	s_nop 0
	v_cndmask_b32_e32 v20, v239, v20, vcc
	v_lshlrev_b32_e32 v20, 2, v20
	ds_bpermute_b32 v21, v20, v5
	v_cmp_lt_f32_e32 vcc, s54, v2
	s_waitcnt lgkmcnt(0)
; #define MFMA32(a, b, c) __builtin_amdgcn_mfma_f32_32x32x16_bf16((a), (b), (c), 0, 0, 0)
; #define P3_LOADK(t_) do { const GAS char* kp_ = kb_u + (long)(t_) * 8192; _Pragma("unroll") for (int st = 0; st < 8; ++st) kf[st] = *(const GAS bf16x8*)(kp_ + 1024 * st + voff); } while (0)
; #define P3_LOADV(buf, t_) do { const GAS char* vp_ = vb_u + (long)(t_) * 8192; _Pragma("unroll") for (int s2 = 0; s2 < 2; ++s2) _Pragma("unroll") for (int db = 0; db < 4; ++db) vf[buf][db][s2] = *(const GAS u32x4*)(vp_ + (s2 * 4 + db) * 1024 + voff); } while (0)
; DI void p3_attn_mfma(Frame& F, ArgsP A) {
;     ...
;                 tm = fmaxf(tm, __shfl_xor(tm, 32));
;                 const float mn = fmaxf(m, tm), alpha = __expf(m - mn);
;                 float ps = 0.f;
; #pragma unroll
;                 for (int i = 0; i < 16; ++i) { const float p = (acc[i] > -1.0e38f) ? __expf(acc[i] - mn) : 0.f; acc[i] = p; ps += p; }
;                 ps += __shfl_xor(ps, 32);
;                 lsum = lsum * alpha + ps; m = mn;
;                 __builtin_amdgcn_sched_barrier(0);
;                 if (t < 4) { P3_LOADK(t + 1); P3_LOADV((t + 1) & 1, t + 1); }
; #pragma unroll
;                 for (int db = 0; db < 4; ++db) {
; #pragma unroll
;                     for (int i = 0; i < 16; ++i) O[db][i] *= alpha; }
;                 const bf16x8 pb0 = pack_step(acc, 0), pb1 = pack_step(acc, 1);
;                 __builtin_amdgcn_sched_barrier(0);
; #pragma unroll
;                 for (int db = 0; db < 4; ++db) O[db] = MFMA32(__builtin_bit_cast(bf16x8, vf[t & 1][db][0]), pb0, O[db]);
; #pragma unroll
;                 for (int db = 0; db < 4; ++db) O[db] = MFMA32(__builtin_bit_cast(bf16x8, vf[t & 1][db][1]), pb1, O[db]);
	v_max3_f32 v243, v5, v21, s53
	v_sub_f32_e32 v21, v2, v243
	v_mul_f32_e32 v21, 0x3fb8aa3b, v21
	v_sub_f32_e32 v22, v4, v243
	v_exp_f32_e32 v21, v21
	v_mul_f32_e32 v22, 0x3fb8aa3b, v22
	v_exp_f32_e32 v22, v22
	v_sub_f32_e32 v23, v7, v243
	v_cndmask_b32_e32 v2, 0, v21, vcc
	v_cmp_lt_f32_e32 vcc, s54, v4
	v_add_f32_e32 v21, 0, v2
	v_mul_f32_e32 v23, 0x3fb8aa3b, v23
	v_cndmask_b32_e32 v22, 0, v22, vcc
	v_add_f32_e32 v4, v22, v21
	v_sub_f32_e32 v21, v6, v243
	v_mul_f32_e32 v21, 0x3fb8aa3b, v21
	v_exp_f32_e32 v21, v21
	v_cmp_lt_f32_e32 vcc, s54, v6
	v_sub_f32_e32 v6, v8, v243
	v_exp_f32_e32 v23, v23
	v_cndmask_b32_e32 v21, 0, v21, vcc
	v_cmp_lt_f32_e32 vcc, s54, v7
	v_mul_f32_e32 v6, 0x3fb8aa3b, v6
	v_sub_f32_e32 v7, v9, v243
	v_exp_f32_e32 v6, v6
	v_mul_f32_e32 v7, 0x3fb8aa3b, v7
	v_exp_f32_e32 v7, v7
	v_cndmask_b32_e32 v23, 0, v23, vcc
	v_cmp_lt_f32_e32 vcc, s54, v8
	v_add_f32_e32 v4, v21, v4
	v_add_f32_e32 v4, v23, v4
	v_cndmask_b32_e32 v24, 0, v6, vcc
	v_cmp_lt_f32_e32 vcc, s54, v9
	v_sub_f32_e32 v6, v10, v243
	v_mul_f32_e32 v6, 0x3fb8aa3b, v6
	v_cndmask_b32_e32 v25, 0, v7, vcc
	v_sub_f32_e32 v7, v11, v243
	v_exp_f32_e32 v6, v6
	v_mul_f32_e32 v7, 0x3fb8aa3b, v7
	v_exp_f32_e32 v7, v7
	v_cmp_lt_f32_e32 vcc, s54, v10
	v_add_f32_e32 v4, v24, v4
	v_add_f32_e32 v4, v25, v4
	v_cndmask_b32_e32 v26, 0, v6, vcc
	v_cmp_lt_f32_e32 vcc, s54, v11
	v_sub_f32_e32 v6, v12, v243
	v_mul_f32_e32 v6, 0x3fb8aa3b, v6
	v_cndmask_b32_e32 v27, 0, v7, vcc
	v_sub_f32_e32 v7, v13, v243
	v_exp_f32_e32 v6, v6
	v_mul_f32_e32 v7, 0x3fb8aa3b, v7
	v_exp_f32_e32 v7, v7
	v_cmp_lt_f32_e32 vcc, s54, v12
	v_add_f32_e32 v4, v26, v4
	v_add_f32_e32 v4, v27, v4
	v_cndmask_b32_e32 v28, 0, v6, vcc
	v_cmp_lt_f32_e32 vcc, s54, v13
	v_sub_f32_e32 v6, v14, v243
	v_mul_f32_e32 v6, 0x3fb8aa3b, v6
	v_cndmask_b32_e32 v29, 0, v7, vcc
	v_sub_f32_e32 v7, v15, v243
	v_exp_f32_e32 v6, v6
	v_mul_f32_e32 v7, 0x3fb8aa3b, v7
	v_exp_f32_e32 v7, v7
	v_cmp_lt_f32_e32 vcc, s54, v14
	v_add_f32_e32 v4, v28, v4
	v_add_f32_e32 v4, v29, v4
	v_cndmask_b32_e32 v30, 0, v6, vcc
	v_cmp_lt_f32_e32 vcc, s54, v15
	v_sub_f32_e32 v6, v16, v243
	v_mul_f32_e32 v6, 0x3fb8aa3b, v6
	v_cndmask_b32_e32 v31, 0, v7, vcc
	v_sub_f32_e32 v7, v17, v243
	v_exp_f32_e32 v6, v6
	v_mul_f32_e32 v7, 0x3fb8aa3b, v7
	v_exp_f32_e32 v7, v7
	v_cmp_lt_f32_e32 vcc, s54, v16
	v_add_f32_e32 v4, v30, v4
	v_add_f32_e32 v4, v31, v4
	v_cndmask_b32_e32 v32, 0, v6, vcc
	v_cmp_lt_f32_e32 vcc, s54, v17
	v_sub_f32_e32 v6, v18, v243
	v_mul_f32_e32 v6, 0x3fb8aa3b, v6
	v_cndmask_b32_e32 v33, 0, v7, vcc
	v_sub_f32_e32 v7, v19, v243
	v_exp_f32_e32 v6, v6
	v_mul_f32_e32 v7, 0x3fb8aa3b, v7
	v_exp_f32_e32 v7, v7
	v_add_f32_e32 v4, v32, v4
	v_cmp_lt_f32_e32 vcc, s54, v18
	v_add_f32_e32 v4, v33, v4
	v_sub_f32_e32 v5, 0xff61b1e6, v243
	v_cndmask_b32_e32 v34, 0, v6, vcc
	v_cmp_lt_f32_e32 vcc, s54, v19
	v_add_f32_e32 v4, v34, v4
	v_mul_f32_e32 v5, 0x3fb8aa3b, v5
	v_cndmask_b32_e32 v35, 0, v7, vcc
	v_add_f32_e32 v4, v35, v4
	ds_bpermute_b32 v6, v20, v4
	v_exp_f32_e32 v5, v5
	s_waitcnt lgkmcnt(0)
	v_add_f32_e32 v242, v4, v6
	v_mul_f32_e32 v4, 0, v5
	v_fmac_f32_e32 v242, 0, v5
	v_add_co_u32_e32 v6, vcc, s55, v212
	v_mov_b32_e32 v5, v4
	s_nop 0
	v_addc_co_u32_e32 v7, vcc, 0, v213, vcc
	global_load_dwordx4 v[104:107], v[6:7], off offset:3072
	global_load_dwordx4 v[116:119], v[6:7], off offset:2048
	global_load_dwordx4 v[124:127], v[6:7], off offset:1024
	global_load_dwordx4 v[128:131], v[6:7], off
	v_add_co_u32_e32 v6, vcc, s56, v212
	v_mov_b32_e32 v8, v4
	s_nop 0
	v_addc_co_u32_e32 v7, vcc, 0, v213, vcc
	global_load_dwordx4 v[84:87], v[6:7], off offset:3072
	global_load_dwordx4 v[96:99], v[6:7], off offset:2048
	global_load_dwordx4 v[112:115], v[6:7], off offset:1024
	global_load_dwordx4 v[120:123], v[6:7], off
	v_add_co_u32_e32 v6, vcc, s55, v214
	v_mov_b32_e32 v9, v4
	s_nop 0
	v_addc_co_u32_e32 v7, vcc, 0, v215, vcc
	global_load_dwordx4 v[180:183], v[6:7], off offset:3072
	global_load_dwordx4 v[184:187], v[6:7], off offset:2048
	global_load_dwordx4 v[188:191], v[6:7], off offset:1024
	global_load_dwordx4 v[192:195], v[6:7], off
	v_add_co_u32_e32 v6, vcc, s56, v214
	v_mov_b32_e32 v10, v4
	s_nop 0
	v_addc_co_u32_e32 v7, vcc, 0, v215, vcc
	global_load_dwordx4 v[196:199], v[6:7], off offset:3072
	global_load_dwordx4 v[200:203], v[6:7], off offset:2048
	global_load_dwordx4 v[204:207], v[6:7], off offset:1024
	global_load_dwordx4 v[208:211], v[6:7], off
	v_mov_b32_e32 v6, v4
	v_mov_b32_e32 v7, v4
	v_mov_b32_e32 v11, v4
	v_mov_b32_e32 v12, v4
	v_mov_b32_e32 v13, v4
	v_mov_b32_e32 v14, v4
	v_mov_b32_e32 v15, v4
	v_mov_b32_e32 v16, v4
	v_mov_b32_e32 v17, v4
	v_mov_b32_e32 v18, v4
	v_mov_b32_e32 v19, v4
	v_cvt_pk_bf16_f32 v68, v2, v22
	v_cvt_pk_bf16_f32 v69, v21, v23
	v_cvt_pk_bf16_f32 v70, v24, v25
	v_cvt_pk_bf16_f32 v71, v26, v27
	v_cvt_pk_bf16_f32 v72, v28, v29
	v_cvt_pk_bf16_f32 v73, v30, v31
	v_cvt_pk_bf16_f32 v74, v32, v33
	v_cvt_pk_bf16_f32 v75, v34, v35
	s_waitcnt vmcnt(23)
	v_mfma_f32_32x32x16_bf16 v[52:67], v[108:111], v[68:71], v[4:19]
	s_waitcnt vmcnt(22)
	v_mfma_f32_32x32x16_bf16 v[36:51], v[100:103], v[68:71], v[4:19]
	s_waitcnt vmcnt(21)
	v_mfma_f32_32x32x16_bf16 v[20:35], v[92:95], v[68:71], v[4:19]
	s_waitcnt vmcnt(20)
	v_mfma_f32_32x32x16_bf16 v[4:19], v[88:91], v[68:71], v[4:19]
	s_waitcnt vmcnt(19)
	v_mfma_f32_32x32x16_bf16 v[52:67], v[144:147], v[72:75], v[52:67]
	s_waitcnt vmcnt(18)
	v_mfma_f32_32x32x16_bf16 v[36:51], v[140:143], v[72:75], v[36:51]
	s_waitcnt vmcnt(17)
	v_mfma_f32_32x32x16_bf16 v[20:35], v[136:139], v[72:75], v[20:35]
	s_waitcnt vmcnt(16)
	v_mfma_f32_32x32x16_bf16 v[4:19], v[132:135], v[72:75], v[4:19]
	s_branch .LBB0_462

; #define LDS_WAIT() asm volatile("s_waitcnt lgkmcnt(0)" ::: "memory")
; DI int crow(int reg, int h) { return (reg & 3) + 8 * (reg >> 2) + 4 * h; }
; #define MFMA32(a, b, c) __builtin_amdgcn_mfma_f32_32x32x16_bf16((a), (b), (c), 0, 0, 0)
; DI void p3_attn_mfma(Frame& F, ArgsP A) {
;     ...
;                 for (int i = 0; i < 16; ++i) acc[i] = tb[32 + (128 - 32 * t + rq - crow(i, h))];
;                 LDS_WAIT(); __builtin_amdgcn_sched_barrier(0);
; #pragma unroll
;                 for (int st = 0; st < 8; ++st) acc = MFMA32(kf[st], qf[st], acc);
;                 __builtin_amdgcn_sched_barrier(0);
;                 float tm = -3.0e38f;
; #pragma unroll
;                 for (int i = 0; i < 16; ++i) {
;                     const int key = crow(i, h);
;                     const bool valid = (t == 0) ? (key >= rq) : ((t == 4) ? (key <= rq) : true);
;                     acc[i] = valid ? acc[i] : -3.0e38f; tm = fmaxf(tm, acc[i]);
;                 }
;                 tm = fmaxf(tm, __shfl_xor(tm, 32));
;                 const float mn = fmaxf(m, tm), alpha = __expf(m - mn);
;                 float ps = 0.f;
; #pragma unroll
;                 for (int i = 0; i < 16; ++i) { const float p = (acc[i] > -1.0e38f) ? __expf(acc[i] - mn) : 0.f; acc[i] = p; ps += p; }
;                 ps += __shfl_xor(ps, 32);
;                 lsum = lsum * alpha + ps; m = mn;
.LBB0_469:
	v_lshl_add_u32 v2, v241, 2, v237
	ds_read2_b32 v[70:71], v2 offset0:95 offset1:96
	ds_read2_b32 v[72:73], v2 offset0:93 offset1:94
	ds_read2_b32 v[74:75], v2 offset0:87 offset1:88
	ds_read2_b32 v[76:77], v2 offset0:85 offset1:86
	ds_read2_b32 v[78:79], v2 offset0:79 offset1:80
	ds_read2_b32 v[80:81], v2 offset0:77 offset1:78
	ds_read2_b32 v[82:83], v2 offset0:71 offset1:72
	s_waitcnt vmcnt(11)
	ds_read2_b32 v[84:85], v2 offset0:69 offset1:70
	s_waitcnt lgkmcnt(0)
	s_waitcnt lgkmcnt(7)
	v_mov_b32_e32 v68, v71
	v_mov_b32_e32 v69, v70
	s_waitcnt lgkmcnt(6)
	v_mov_b32_e32 v70, v73
	v_mov_b32_e32 v71, v72
	s_waitcnt lgkmcnt(5)
	v_mov_b32_e32 v72, v75
	v_mov_b32_e32 v73, v74
	s_waitcnt lgkmcnt(4)
	v_mov_b32_e32 v74, v77
	v_mov_b32_e32 v75, v76
	s_waitcnt lgkmcnt(3)
	v_mov_b32_e32 v76, v79
	v_mov_b32_e32 v77, v78
	s_waitcnt lgkmcnt(2)
	v_mov_b32_e32 v78, v81
	v_mov_b32_e32 v79, v80
	s_waitcnt lgkmcnt(1)
	v_mov_b32_e32 v80, v83
	v_mov_b32_e32 v81, v82
	s_waitcnt lgkmcnt(0)
	v_mov_b32_e32 v82, v85
	v_mov_b32_e32 v83, v84
	s_waitcnt vmcnt(0)
	s_nop 0
	s_nop 0
	v_mfma_f32_32x32x16_bf16 v[68:83], v[208:211], v[172:175], v[68:83]
	v_mfma_f32_32x32x16_bf16 v[68:83], v[204:207], v[164:167], v[68:83]
	v_mfma_f32_32x32x16_bf16 v[68:83], v[200:203], v[156:159], v[68:83]
	v_mfma_f32_32x32x16_bf16 v[68:83], v[196:199], v[148:151], v[68:83]
	v_mfma_f32_32x32x16_bf16 v[68:83], v[192:195], v[176:179], v[68:83]
	v_mfma_f32_32x32x16_bf16 v[68:83], v[188:191], v[168:171], v[68:83]
	v_mfma_f32_32x32x16_bf16 v[68:83], v[184:187], v[160:163], v[68:83]
	v_mfma_f32_32x32x16_bf16 v[68:83], v[180:183], v[152:155], v[68:83]
	s_nop 11
	v_max3_f32 v2, v68, s53, v69
	v_max3_f32 v2, v2, v70, v71
	v_max3_f32 v2, v2, v72, v73
	v_max3_f32 v2, v2, v74, v75
	v_and_b32_e32 v85, 64, v239
	v_max3_f32 v2, v2, v76, v77
	v_xor_b32_e32 v84, 32, v239
	v_add_u32_e32 v85, 64, v85
	v_max3_f32 v2, v2, v78, v79
	v_cmp_lt_i32_e32 vcc, v84, v85
	v_max3_f32 v2, v2, v80, v81
	v_max3_f32 v2, v2, v82, v83
	v_cndmask_b32_e32 v84, v239, v84, vcc
	v_lshlrev_b32_e32 v84, 2, v84
	ds_bpermute_b32 v85, v84, v2
	v_cmp_lt_f32_e32 vcc, s54, v68
	s_waitcnt lgkmcnt(0)
	v_max3_f32 v244, v243, v2, v85
	v_sub_f32_e32 v85, v68, v244
	v_mul_f32_e32 v85, 0x3fb8aa3b, v85
	v_exp_f32_e32 v85, v85
	v_sub_f32_e32 v86, v69, v244
	v_sub_f32_e32 v2, v243, v244
	v_mul_f32_e32 v86, 0x3fb8aa3b, v86
	v_cndmask_b32_e32 v243, 0, v85, vcc
	v_cmp_lt_f32_e32 vcc, s54, v69
	v_sub_f32_e32 v69, v70, v244
	v_exp_f32_e32 v86, v86
	v_mul_f32_e32 v69, 0x3fb8aa3b, v69
	v_sub_f32_e32 v85, v71, v244
	v_exp_f32_e32 v69, v69
	v_mul_f32_e32 v85, 0x3fb8aa3b, v85
	v_exp_f32_e32 v85, v85
	v_cndmask_b32_e32 v245, 0, v86, vcc
	v_cmp_lt_f32_e32 vcc, s54, v70
	v_add_f32_e32 v68, 0, v243
	v_add_f32_e32 v68, v245, v68
	v_cndmask_b32_e32 v70, 0, v69, vcc
	v_cmp_lt_f32_e32 vcc, s54, v71
	v_sub_f32_e32 v69, v72, v244
	v_mul_f32_e32 v69, 0x3fb8aa3b, v69
	v_cndmask_b32_e32 v71, 0, v85, vcc
	v_sub_f32_e32 v85, v73, v244
	v_exp_f32_e32 v69, v69
	v_mul_f32_e32 v85, 0x3fb8aa3b, v85
	v_exp_f32_e32 v85, v85
	v_cmp_lt_f32_e32 vcc, s54, v72
	v_add_f32_e32 v68, v70, v68
	v_add_f32_e32 v68, v71, v68
	v_cndmask_b32_e32 v72, 0, v69, vcc
	v_cmp_lt_f32_e32 vcc, s54, v73
	v_sub_f32_e32 v69, v74, v244
	v_mul_f32_e32 v69, 0x3fb8aa3b, v69
	v_cndmask_b32_e32 v73, 0, v85, vcc
	v_sub_f32_e32 v85, v75, v244
	v_exp_f32_e32 v69, v69
	v_mul_f32_e32 v85, 0x3fb8aa3b, v85
	v_exp_f32_e32 v85, v85
	v_cmp_lt_f32_e32 vcc, s54, v74
	v_add_f32_e32 v68, v72, v68
	v_add_f32_e32 v68, v73, v68
	v_cndmask_b32_e32 v74, 0, v69, vcc
	v_cmp_lt_f32_e32 vcc, s54, v75
	v_sub_f32_e32 v69, v76, v244
	v_mul_f32_e32 v69, 0x3fb8aa3b, v69
	v_cndmask_b32_e32 v75, 0, v85, vcc
	v_sub_f32_e32 v85, v77, v244
	v_exp_f32_e32 v69, v69
	v_mul_f32_e32 v85, 0x3fb8aa3b, v85
	v_exp_f32_e32 v85, v85
	v_cmp_lt_f32_e32 vcc, s54, v76
	v_add_f32_e32 v68, v74, v68
	v_add_f32_e32 v68, v75, v68
	v_cndmask_b32_e32 v76, 0, v69, vcc
	v_cmp_lt_f32_e32 vcc, s54, v77
	v_sub_f32_e32 v69, v78, v244
	v_mul_f32_e32 v69, 0x3fb8aa3b, v69
	v_cndmask_b32_e32 v77, 0, v85, vcc
	v_sub_f32_e32 v85, v79, v244
	v_exp_f32_e32 v69, v69
	v_mul_f32_e32 v85, 0x3fb8aa3b, v85
	v_exp_f32_e32 v85, v85
	v_cmp_lt_f32_e32 vcc, s54, v78
	v_add_f32_e32 v68, v76, v68
	v_add_f32_e32 v68, v77, v68
	v_cndmask_b32_e32 v78, 0, v69, vcc
	v_cmp_lt_f32_e32 vcc, s54, v79
	v_sub_f32_e32 v69, v80, v244
	v_mul_f32_e32 v69, 0x3fb8aa3b, v69
	v_cndmask_b32_e32 v79, 0, v85, vcc
	v_sub_f32_e32 v85, v81, v244
	v_exp_f32_e32 v69, v69
	v_mul_f32_e32 v85, 0x3fb8aa3b, v85
	v_exp_f32_e32 v85, v85
	v_cmp_lt_f32_e32 vcc, s54, v80
	v_add_f32_e32 v68, v78, v68
	v_add_f32_e32 v68, v79, v68
	v_cndmask_b32_e32 v80, 0, v69, vcc
	v_cmp_lt_f32_e32 vcc, s54, v81
	v_sub_f32_e32 v69, v82, v244
	v_mul_f32_e32 v69, 0x3fb8aa3b, v69
	v_cndmask_b32_e32 v81, 0, v85, vcc
	v_sub_f32_e32 v85, v83, v244
	v_exp_f32_e32 v69, v69
	v_mul_f32_e32 v85, 0x3fb8aa3b, v85
	v_exp_f32_e32 v85, v85
	v_add_f32_e32 v68, v80, v68
	v_cmp_lt_f32_e32 vcc, s54, v82
	v_add_f32_e32 v68, v81, v68
	v_mul_f32_e32 v2, 0x3fb8aa3b, v2
	v_cndmask_b32_e32 v82, 0, v69, vcc
	v_cmp_lt_f32_e32 vcc, s54, v83
	v_add_f32_e32 v68, v82, v68
	v_exp_f32_e32 v2, v2
	v_cndmask_b32_e32 v83, 0, v85, vcc
	v_add_f32_e32 v68, v83, v68
	ds_bpermute_b32 v69, v84, v68
	s_waitcnt lgkmcnt(0)
; #define MFMA32(a, b, c) __builtin_amdgcn_mfma_f32_32x32x16_bf16((a), (b), (c), 0, 0, 0)
; #define P3_LOADK(t_) do { const GAS char* kp_ = kb_u + (long)(t_) * 8192; _Pragma("unroll") for (int st = 0; st < 8; ++st) kf[st] = *(const GAS bf16x8*)(kp_ + 1024 * st + voff); } while (0)
; #define P3_LOADV(buf, t_) do { const GAS char* vp_ = vb_u + (long)(t_) * 8192; _Pragma("unroll") for (int s2 = 0; s2 < 2; ++s2) _Pragma("unroll") for (int db = 0; db < 4; ++db) vf[buf][db][s2] = *(const GAS u32x4*)(vp_ + (s2 * 4 + db) * 1024 + voff); } while (0)
; DI void p3_attn_mfma(Frame& F, ArgsP A) {
;     ...
;                 if (t < 4) { P3_LOADK(t + 1); P3_LOADV((t + 1) & 1, t + 1); }
; #pragma unroll
;                 for (int db = 0; db < 4; ++db) {
; #pragma unroll
;                     for (int i = 0; i < 16; ++i) O[db][i] *= alpha; }
;                 const bf16x8 pb0 = pack_step(acc, 0), pb1 = pack_step(acc, 1);
;                 __builtin_amdgcn_sched_barrier(0);
; #pragma unroll
;                 for (int db = 0; db < 4; ++db) O[db] = MFMA32(__builtin_bit_cast(bf16x8, vf[t & 1][db][0]), pb0, O[db]);
; #pragma unroll
;                 for (int db = 0; db < 4; ++db) O[db] = MFMA32(__builtin_bit_cast(bf16x8, vf[t & 1][db][1]), pb1, O[db]);
	v_add_f32_e32 v246, v68, v69
	v_fmac_f32_e32 v246, v242, v2
	v_add_co_u32_e32 v68, vcc, s64, v214
	v_pk_mul_f32 v[66:67], v[66:67], v[2:3] op_sel_hi:[1,0]
	s_nop 0
	v_addc_co_u32_e32 v69, vcc, 0, v215, vcc
	global_load_dwordx4 v[180:183], v[68:69], off offset:3072
	global_load_dwordx4 v[184:187], v[68:69], off offset:2048
	global_load_dwordx4 v[188:191], v[68:69], off offset:1024
	global_load_dwordx4 v[192:195], v[68:69], off
	v_add_co_u32_e32 v68, vcc, s65, v214
	v_pk_mul_f32 v[64:65], v[64:65], v[2:3] op_sel_hi:[1,0]
	s_nop 0
	v_addc_co_u32_e32 v69, vcc, 0, v215, vcc
	global_load_dwordx4 v[196:199], v[68:69], off offset:3072
	global_load_dwordx4 v[200:203], v[68:69], off offset:2048
	global_load_dwordx4 v[204:207], v[68:69], off offset:1024
	global_load_dwordx4 v[208:211], v[68:69], off
	v_add_co_u32_e32 v68, vcc, s64, v212
	v_pk_mul_f32 v[62:63], v[62:63], v[2:3] op_sel_hi:[1,0]
	s_nop 0
	v_addc_co_u32_e32 v69, vcc, 0, v213, vcc
	global_load_dwordx4 v[104:107], v[68:69], off offset:3072
	global_load_dwordx4 v[116:119], v[68:69], off offset:2048
	global_load_dwordx4 v[124:127], v[68:69], off offset:1024
	global_load_dwordx4 v[128:131], v[68:69], off
	v_add_co_u32_e32 v68, vcc, s65, v212
	v_pk_mul_f32 v[60:61], v[60:61], v[2:3] op_sel_hi:[1,0]
	s_nop 0
	v_addc_co_u32_e32 v69, vcc, 0, v213, vcc
	global_load_dwordx4 v[84:87], v[68:69], off offset:3072
	global_load_dwordx4 v[96:99], v[68:69], off offset:2048
	global_load_dwordx4 v[112:115], v[68:69], off offset:1024
	global_load_dwordx4 v[120:123], v[68:69], off
	v_pk_mul_f32 v[58:59], v[58:59], v[2:3] op_sel_hi:[1,0]
	v_pk_mul_f32 v[56:57], v[56:57], v[2:3] op_sel_hi:[1,0]
	v_pk_mul_f32 v[54:55], v[54:55], v[2:3] op_sel_hi:[1,0]
	v_pk_mul_f32 v[52:53], v[52:53], v[2:3] op_sel_hi:[1,0]
	v_pk_mul_f32 v[50:51], v[50:51], v[2:3] op_sel_hi:[1,0]
	v_pk_mul_f32 v[48:49], v[48:49], v[2:3] op_sel_hi:[1,0]
	v_pk_mul_f32 v[46:47], v[46:47], v[2:3] op_sel_hi:[1,0]
	v_pk_mul_f32 v[44:45], v[44:45], v[2:3] op_sel_hi:[1,0]
	v_pk_mul_f32 v[42:43], v[42:43], v[2:3] op_sel_hi:[1,0]
	v_pk_mul_f32 v[40:41], v[40:41], v[2:3] op_sel_hi:[1,0]
	v_pk_mul_f32 v[38:39], v[38:39], v[2:3] op_sel_hi:[1,0]
	v_pk_mul_f32 v[36:37], v[36:37], v[2:3] op_sel_hi:[1,0]
	v_pk_mul_f32 v[34:35], v[34:35], v[2:3] op_sel_hi:[1,0]
	v_pk_mul_f32 v[32:33], v[32:33], v[2:3] op_sel_hi:[1,0]
	v_pk_mul_f32 v[30:31], v[30:31], v[2:3] op_sel_hi:[1,0]
	v_pk_mul_f32 v[28:29], v[28:29], v[2:3] op_sel_hi:[1,0]
	v_pk_mul_f32 v[26:27], v[26:27], v[2:3] op_sel_hi:[1,0]
	v_pk_mul_f32 v[24:25], v[24:25], v[2:3] op_sel_hi:[1,0]
	v_pk_mul_f32 v[22:23], v[22:23], v[2:3] op_sel_hi:[1,0]
	v_pk_mul_f32 v[20:21], v[20:21], v[2:3] op_sel_hi:[1,0]
	v_pk_mul_f32 v[18:19], v[18:19], v[2:3] op_sel_hi:[1,0]
	v_pk_mul_f32 v[16:17], v[16:17], v[2:3] op_sel_hi:[1,0]
	v_pk_mul_f32 v[14:15], v[14:15], v[2:3] op_sel_hi:[1,0]
	v_pk_mul_f32 v[12:13], v[12:13], v[2:3] op_sel_hi:[1,0]
	v_pk_mul_f32 v[10:11], v[10:11], v[2:3] op_sel_hi:[1,0]
	v_pk_mul_f32 v[8:9], v[8:9], v[2:3] op_sel_hi:[1,0]
	v_pk_mul_f32 v[6:7], v[6:7], v[2:3] op_sel_hi:[1,0]
	v_pk_mul_f32 v[4:5], v[4:5], v[2:3] op_sel_hi:[1,0]
	v_cvt_pk_bf16_f32 v68, v243, v245
	v_cvt_pk_bf16_f32 v69, v70, v71
	v_cvt_pk_bf16_f32 v70, v72, v73
	v_cvt_pk_bf16_f32 v71, v74, v75
	v_cvt_pk_bf16_f32 v72, v76, v77
	v_cvt_pk_bf16_f32 v73, v78, v79
	v_cvt_pk_bf16_f32 v74, v80, v81
	v_cvt_pk_bf16_f32 v75, v82, v83
	v_mfma_f32_32x32x16_bf16 v[52:67], v[108:111], v[68:71], v[52:67]
	v_mov_b32_e32 v243, v244
	v_mov_b32_e32 v242, v246
	v_mfma_f32_32x32x16_bf16 v[36:51], v[100:103], v[68:71], v[36:51]
	v_mfma_f32_32x32x16_bf16 v[20:35], v[92:95], v[68:71], v[20:35]
	v_mfma_f32_32x32x16_bf16 v[4:19], v[88:91], v[68:71], v[4:19]
	v_mfma_f32_32x32x16_bf16 v[52:67], v[144:147], v[72:75], v[52:67]
	v_mfma_f32_32x32x16_bf16 v[36:51], v[140:143], v[72:75], v[36:51]
	v_mfma_f32_32x32x16_bf16 v[20:35], v[136:139], v[72:75], v[20:35]
	v_mfma_f32_32x32x16_bf16 v[4:19], v[132:135], v[72:75], v[4:19]

; #define LDS_WAIT() asm volatile("s_waitcnt lgkmcnt(0)" ::: "memory")
; DI int crow(int reg, int h) { return (reg & 3) + 8 * (reg >> 2) + 4 * h; }
; #define MFMA32(a, b, c) __builtin_amdgcn_mfma_f32_32x32x16_bf16((a), (b), (c), 0, 0, 0)
; DI void p3_attn_mfma(Frame& F, ArgsP A) {
;     ...
;                 for (int i = 0; i < 16; ++i) acc[i] = tb[32 + (128 - 32 * t + rq - crow(i, h))];
;                 LDS_WAIT(); __builtin_amdgcn_sched_barrier(0);
; #pragma unroll
;                 for (int st = 0; st < 8; ++st) acc = MFMA32(kf[st], qf[st], acc);
;                 __builtin_amdgcn_sched_barrier(0);
;                 float tm = -3.0e38f;
; #pragma unroll
;                 for (int i = 0; i < 16; ++i) {
;                     const int key = crow(i, h);
;                     const bool valid = (t == 0) ? (key >= rq) : ((t == 4) ? (key <= rq) : true);
;                     acc[i] = valid ? acc[i] : -3.0e38f; tm = fmaxf(tm, acc[i]);
;                 }
;                 tm = fmaxf(tm, __shfl_xor(tm, 32));
;                 const float mn = fmaxf(m, tm), alpha = __expf(m - mn);
;                 float ps = 0.f;
; #pragma unroll
;                 for (int i = 0; i < 16; ++i) { const float p = (acc[i] > -1.0e38f) ? __expf(acc[i] - mn) : 0.f; acc[i] = p; ps += p; }
;                 ps += __shfl_xor(ps, 32);
;                 lsum = lsum * alpha + ps; m = mn;
.LBB0_473:
	v_lshl_add_u32 v2, v241, 2, v237
	ds_read2_b32 v[70:71], v2 offset0:63 offset1:64
	ds_read2_b32 v[72:73], v2 offset0:61 offset1:62
	ds_read2_b32 v[74:75], v2 offset0:55 offset1:56
	ds_read2_b32 v[76:77], v2 offset0:53 offset1:54
	ds_read2_b32 v[78:79], v2 offset0:47 offset1:48
	ds_read2_b32 v[80:81], v2 offset0:45 offset1:46
	ds_read2_b32 v[82:83], v2 offset0:39 offset1:40
	s_waitcnt vmcnt(3)
	ds_read2_b32 v[88:89], v2 offset0:37 offset1:38
	s_waitcnt lgkmcnt(0)
	s_waitcnt lgkmcnt(7)
	v_mov_b32_e32 v68, v71
	v_mov_b32_e32 v69, v70
	s_waitcnt lgkmcnt(6)
	v_mov_b32_e32 v70, v73
	v_mov_b32_e32 v71, v72
	s_waitcnt lgkmcnt(5)
	v_mov_b32_e32 v72, v75
	v_mov_b32_e32 v73, v74
	s_waitcnt lgkmcnt(4)
	v_mov_b32_e32 v74, v77
	v_mov_b32_e32 v75, v76
	s_waitcnt lgkmcnt(3)
	v_mov_b32_e32 v76, v79
	v_mov_b32_e32 v77, v78
	s_waitcnt lgkmcnt(2)
	v_mov_b32_e32 v78, v81
	v_mov_b32_e32 v79, v80
	s_waitcnt lgkmcnt(1)
	v_mov_b32_e32 v80, v83
	v_mov_b32_e32 v81, v82
	s_waitcnt lgkmcnt(0)
	v_mov_b32_e32 v82, v89
	v_mov_b32_e32 v83, v88
	s_waitcnt vmcnt(0)
	s_nop 0
	s_nop 0
	v_mfma_f32_32x32x16_bf16 v[68:83], v[208:211], v[172:175], v[68:83]
	v_mfma_f32_32x32x16_bf16 v[68:83], v[204:207], v[164:167], v[68:83]
	v_mfma_f32_32x32x16_bf16 v[68:83], v[200:203], v[156:159], v[68:83]
	v_mfma_f32_32x32x16_bf16 v[68:83], v[196:199], v[148:151], v[68:83]
	v_mfma_f32_32x32x16_bf16 v[68:83], v[192:195], v[176:179], v[68:83]
	v_mfma_f32_32x32x16_bf16 v[68:83], v[188:191], v[168:171], v[68:83]
	v_mfma_f32_32x32x16_bf16 v[68:83], v[184:187], v[160:163], v[68:83]
	v_mfma_f32_32x32x16_bf16 v[68:83], v[180:183], v[152:155], v[68:83]
	s_nop 11
	v_max3_f32 v2, v68, s53, v69
	v_max3_f32 v2, v2, v70, v71
	v_max3_f32 v2, v2, v72, v73
	v_max3_f32 v2, v2, v74, v75
	v_and_b32_e32 v89, 64, v239
	v_max3_f32 v2, v2, v76, v77
	v_xor_b32_e32 v88, 32, v239
	v_add_u32_e32 v89, 64, v89
	v_max3_f32 v2, v2, v78, v79
	v_cmp_lt_i32_e32 vcc, v88, v89
	v_max3_f32 v2, v2, v80, v81
	v_max3_f32 v2, v2, v82, v83
	v_cndmask_b32_e32 v88, v239, v88, vcc
	v_lshlrev_b32_e32 v88, 2, v88
	ds_bpermute_b32 v89, v88, v2
	v_cmp_lt_f32_e32 vcc, s54, v68
	s_waitcnt lgkmcnt(0)
	v_max3_f32 v244, v243, v2, v89
	v_sub_f32_e32 v89, v68, v244
	v_mul_f32_e32 v89, 0x3fb8aa3b, v89
	v_exp_f32_e32 v89, v89
	v_sub_f32_e32 v90, v69, v244
	v_sub_f32_e32 v2, v243, v244
	v_mul_f32_e32 v90, 0x3fb8aa3b, v90
	v_cndmask_b32_e32 v243, 0, v89, vcc
	v_cmp_lt_f32_e32 vcc, s54, v69
	v_sub_f32_e32 v69, v70, v244
	v_exp_f32_e32 v90, v90
	v_mul_f32_e32 v69, 0x3fb8aa3b, v69
	v_sub_f32_e32 v89, v71, v244
	v_exp_f32_e32 v69, v69
	v_mul_f32_e32 v89, 0x3fb8aa3b, v89
	v_exp_f32_e32 v89, v89
	v_cndmask_b32_e32 v245, 0, v90, vcc
	v_cmp_lt_f32_e32 vcc, s54, v70
	v_add_f32_e32 v68, 0, v243
	v_add_f32_e32 v68, v245, v68
	v_cndmask_b32_e32 v70, 0, v69, vcc
	v_cmp_lt_f32_e32 vcc, s54, v71
	v_sub_f32_e32 v69, v72, v244
	v_mul_f32_e32 v69, 0x3fb8aa3b, v69
	v_cndmask_b32_e32 v71, 0, v89, vcc
	v_sub_f32_e32 v89, v73, v244
	v_exp_f32_e32 v69, v69
	v_mul_f32_e32 v89, 0x3fb8aa3b, v89
	v_exp_f32_e32 v89, v89
	v_cmp_lt_f32_e32 vcc, s54, v72
	v_add_f32_e32 v68, v70, v68
	v_add_f32_e32 v68, v71, v68
	v_cndmask_b32_e32 v72, 0, v69, vcc
	v_cmp_lt_f32_e32 vcc, s54, v73
	v_sub_f32_e32 v69, v74, v244
	v_mul_f32_e32 v69, 0x3fb8aa3b, v69
	v_cndmask_b32_e32 v73, 0, v89, vcc
	v_sub_f32_e32 v89, v75, v244
	v_exp_f32_e32 v69, v69
	v_mul_f32_e32 v89, 0x3fb8aa3b, v89
	v_exp_f32_e32 v89, v89
	v_cmp_lt_f32_e32 vcc, s54, v74
	v_add_f32_e32 v68, v72, v68
	v_add_f32_e32 v68, v73, v68
	v_cndmask_b32_e32 v74, 0, v69, vcc
	v_cmp_lt_f32_e32 vcc, s54, v75
	v_sub_f32_e32 v69, v76, v244
	v_mul_f32_e32 v69, 0x3fb8aa3b, v69
	v_cndmask_b32_e32 v75, 0, v89, vcc
	v_sub_f32_e32 v89, v77, v244
	v_exp_f32_e32 v69, v69
	v_mul_f32_e32 v89, 0x3fb8aa3b, v89
	v_exp_f32_e32 v89, v89
	v_cmp_lt_f32_e32 vcc, s54, v76
	v_add_f32_e32 v68, v74, v68
	v_add_f32_e32 v68, v75, v68
	v_cndmask_b32_e32 v76, 0, v69, vcc
	v_cmp_lt_f32_e32 vcc, s54, v77
	v_sub_f32_e32 v69, v78, v244
	v_mul_f32_e32 v69, 0x3fb8aa3b, v69
	v_cndmask_b32_e32 v77, 0, v89, vcc
	v_sub_f32_e32 v89, v79, v244
	v_exp_f32_e32 v69, v69
	v_mul_f32_e32 v89, 0x3fb8aa3b, v89
	v_exp_f32_e32 v89, v89
	v_cmp_lt_f32_e32 vcc, s54, v78
	v_add_f32_e32 v68, v76, v68
	v_add_f32_e32 v68, v77, v68
	v_cndmask_b32_e32 v78, 0, v69, vcc
	v_cmp_lt_f32_e32 vcc, s54, v79
	v_sub_f32_e32 v69, v80, v244
	v_mul_f32_e32 v69, 0x3fb8aa3b, v69
	v_cndmask_b32_e32 v79, 0, v89, vcc
	v_sub_f32_e32 v89, v81, v244
	v_exp_f32_e32 v69, v69
	v_mul_f32_e32 v89, 0x3fb8aa3b, v89
	v_exp_f32_e32 v89, v89
	v_cmp_lt_f32_e32 vcc, s54, v80
	v_add_f32_e32 v68, v78, v68
	v_add_f32_e32 v68, v79, v68
	v_cndmask_b32_e32 v80, 0, v69, vcc
	v_cmp_lt_f32_e32 vcc, s54, v81
	v_sub_f32_e32 v69, v82, v244
	v_mul_f32_e32 v69, 0x3fb8aa3b, v69
	v_cndmask_b32_e32 v81, 0, v89, vcc
	v_sub_f32_e32 v89, v83, v244
	v_exp_f32_e32 v69, v69
	v_mul_f32_e32 v89, 0x3fb8aa3b, v89
	v_exp_f32_e32 v89, v89
	v_add_f32_e32 v68, v80, v68
	v_cmp_lt_f32_e32 vcc, s54, v82
	v_add_f32_e32 v68, v81, v68
	v_mul_f32_e32 v2, 0x3fb8aa3b, v2
	v_cndmask_b32_e32 v82, 0, v69, vcc
	v_cmp_lt_f32_e32 vcc, s54, v83
	v_add_f32_e32 v68, v82, v68
	v_exp_f32_e32 v2, v2
	v_cndmask_b32_e32 v83, 0, v89, vcc
	v_add_f32_e32 v68, v83, v68
	ds_bpermute_b32 v69, v88, v68
	s_waitcnt lgkmcnt(0)
; #define MFMA32(a, b, c) __builtin_amdgcn_mfma_f32_32x32x16_bf16((a), (b), (c), 0, 0, 0)
; #define P3_LOADK(t_) do { const GAS char* kp_ = kb_u + (long)(t_) * 8192; _Pragma("unroll") for (int st = 0; st < 8; ++st) kf[st] = *(const GAS bf16x8*)(kp_ + 1024 * st + voff); } while (0)
; #define P3_LOADV(buf, t_) do { const GAS char* vp_ = vb_u + (long)(t_) * 8192; _Pragma("unroll") for (int s2 = 0; s2 < 2; ++s2) _Pragma("unroll") for (int db = 0; db < 4; ++db) vf[buf][db][s2] = *(const GAS u32x4*)(vp_ + (s2 * 4 + db) * 1024 + voff); } while (0)
; DI void p3_attn_mfma(Frame& F, ArgsP A) {
;     ...
;                 if (t < 4) { P3_LOADK(t + 1); P3_LOADV((t + 1) & 1, t + 1); }
; #pragma unroll
;                 for (int db = 0; db < 4; ++db) {
; #pragma unroll
;                     for (int i = 0; i < 16; ++i) O[db][i] *= alpha; }
;                 const bf16x8 pb0 = pack_step(acc, 0), pb1 = pack_step(acc, 1);
;                 __builtin_amdgcn_sched_barrier(0);
; #pragma unroll
;                 for (int db = 0; db < 4; ++db) O[db] = MFMA32(__builtin_bit_cast(bf16x8, vf[t & 1][db][0]), pb0, O[db]);
; #pragma unroll
;                 for (int db = 0; db < 4; ++db) O[db] = MFMA32(__builtin_bit_cast(bf16x8, vf[t & 1][db][1]), pb1, O[db]);
	v_add_f32_e32 v246, v68, v69
	v_fmac_f32_e32 v246, v242, v2
	v_add_co_u32_e32 v68, vcc, s66, v214
	v_pk_mul_f32 v[66:67], v[66:67], v[2:3] op_sel_hi:[1,0]
	s_nop 0
	v_addc_co_u32_e32 v69, vcc, 0, v215, vcc
	global_load_dwordx4 v[180:183], v[68:69], off offset:3072
	global_load_dwordx4 v[184:187], v[68:69], off offset:2048
	global_load_dwordx4 v[188:191], v[68:69], off offset:1024
	global_load_dwordx4 v[192:195], v[68:69], off
	v_add_co_u32_e32 v68, vcc, s67, v214
	v_pk_mul_f32 v[64:65], v[64:65], v[2:3] op_sel_hi:[1,0]
	s_nop 0
	v_addc_co_u32_e32 v69, vcc, 0, v215, vcc
	global_load_dwordx4 v[196:199], v[68:69], off offset:3072
	global_load_dwordx4 v[200:203], v[68:69], off offset:2048
	global_load_dwordx4 v[204:207], v[68:69], off offset:1024
	global_load_dwordx4 v[208:211], v[68:69], off
	v_add_co_u32_e32 v68, vcc, s66, v212
	v_pk_mul_f32 v[62:63], v[62:63], v[2:3] op_sel_hi:[1,0]
	s_nop 0
	v_addc_co_u32_e32 v69, vcc, 0, v213, vcc
	global_load_dwordx4 v[132:135], v[68:69], off offset:3072
	global_load_dwordx4 v[136:139], v[68:69], off offset:2048
	global_load_dwordx4 v[140:143], v[68:69], off offset:1024
	global_load_dwordx4 v[144:147], v[68:69], off
	v_add_co_u32_e32 v68, vcc, s67, v212
	v_pk_mul_f32 v[60:61], v[60:61], v[2:3] op_sel_hi:[1,0]
	s_nop 0
	v_addc_co_u32_e32 v69, vcc, 0, v213, vcc
	global_load_dwordx4 v[88:91], v[68:69], off offset:3072
	global_load_dwordx4 v[92:95], v[68:69], off offset:2048
	global_load_dwordx4 v[100:103], v[68:69], off offset:1024
	global_load_dwordx4 v[108:111], v[68:69], off
	v_pk_mul_f32 v[58:59], v[58:59], v[2:3] op_sel_hi:[1,0]
	v_pk_mul_f32 v[56:57], v[56:57], v[2:3] op_sel_hi:[1,0]
	v_pk_mul_f32 v[54:55], v[54:55], v[2:3] op_sel_hi:[1,0]
	v_pk_mul_f32 v[52:53], v[52:53], v[2:3] op_sel_hi:[1,0]
	v_pk_mul_f32 v[50:51], v[50:51], v[2:3] op_sel_hi:[1,0]
	v_pk_mul_f32 v[48:49], v[48:49], v[2:3] op_sel_hi:[1,0]
	v_pk_mul_f32 v[46:47], v[46:47], v[2:3] op_sel_hi:[1,0]
	v_pk_mul_f32 v[44:45], v[44:45], v[2:3] op_sel_hi:[1,0]
	v_pk_mul_f32 v[42:43], v[42:43], v[2:3] op_sel_hi:[1,0]
	v_pk_mul_f32 v[40:41], v[40:41], v[2:3] op_sel_hi:[1,0]
	v_pk_mul_f32 v[38:39], v[38:39], v[2:3] op_sel_hi:[1,0]
	v_pk_mul_f32 v[36:37], v[36:37], v[2:3] op_sel_hi:[1,0]
	v_pk_mul_f32 v[34:35], v[34:35], v[2:3] op_sel_hi:[1,0]
	v_pk_mul_f32 v[32:33], v[32:33], v[2:3] op_sel_hi:[1,0]
	v_pk_mul_f32 v[30:31], v[30:31], v[2:3] op_sel_hi:[1,0]
	v_pk_mul_f32 v[28:29], v[28:29], v[2:3] op_sel_hi:[1,0]
	v_pk_mul_f32 v[26:27], v[26:27], v[2:3] op_sel_hi:[1,0]
	v_pk_mul_f32 v[24:25], v[24:25], v[2:3] op_sel_hi:[1,0]
	v_pk_mul_f32 v[22:23], v[22:23], v[2:3] op_sel_hi:[1,0]
	v_pk_mul_f32 v[20:21], v[20:21], v[2:3] op_sel_hi:[1,0]
	v_pk_mul_f32 v[18:19], v[18:19], v[2:3] op_sel_hi:[1,0]
	v_pk_mul_f32 v[16:17], v[16:17], v[2:3] op_sel_hi:[1,0]
	v_pk_mul_f32 v[14:15], v[14:15], v[2:3] op_sel_hi:[1,0]
	v_pk_mul_f32 v[12:13], v[12:13], v[2:3] op_sel_hi:[1,0]
	v_pk_mul_f32 v[10:11], v[10:11], v[2:3] op_sel_hi:[1,0]
	v_pk_mul_f32 v[8:9], v[8:9], v[2:3] op_sel_hi:[1,0]
	v_pk_mul_f32 v[6:7], v[6:7], v[2:3] op_sel_hi:[1,0]
	v_pk_mul_f32 v[4:5], v[4:5], v[2:3] op_sel_hi:[1,0]
	v_cvt_pk_bf16_f32 v68, v243, v245
	v_cvt_pk_bf16_f32 v69, v70, v71
	v_cvt_pk_bf16_f32 v70, v72, v73
	v_cvt_pk_bf16_f32 v71, v74, v75
	v_cvt_pk_bf16_f32 v72, v76, v77
	v_cvt_pk_bf16_f32 v73, v78, v79
	v_cvt_pk_bf16_f32 v74, v80, v81
	v_cvt_pk_bf16_f32 v75, v82, v83
	v_mfma_f32_32x32x16_bf16 v[52:67], v[120:123], v[68:71], v[52:67]
	v_mov_b32_e32 v243, v244
	v_mov_b32_e32 v242, v246
	v_mfma_f32_32x32x16_bf16 v[36:51], v[112:115], v[68:71], v[36:51]
	v_mfma_f32_32x32x16_bf16 v[20:35], v[96:99], v[68:71], v[20:35]
	v_mfma_f32_32x32x16_bf16 v[4:19], v[84:87], v[68:71], v[4:19]
	v_mfma_f32_32x32x16_bf16 v[52:67], v[128:131], v[72:75], v[52:67]
	v_mfma_f32_32x32x16_bf16 v[36:51], v[124:127], v[72:75], v[36:51]
	v_mfma_f32_32x32x16_bf16 v[20:35], v[116:119], v[72:75], v[20:35]
	v_mfma_f32_32x32x16_bf16 v[4:19], v[104:107], v[72:75], v[4:19]

; #define PG8_STAGE2(bufoff, gbase, v0, v1) do { \
;         __builtin_amdgcn_global_load_lds((const unsigned*)((const char*)(gbase) + (v0)), (LAS unsigned*)(lds + (bufoff) + ldsw), 16, 0, 0); \
;         __builtin_amdgcn_global_load_lds((const unsigned*)((const char*)(gbase) + (v1)), (LAS unsigned*)(lds + (bufoff) + ldsw + 8192), 16, 0, 0); } while (0)
; #define PG8_STAGE(bufoff, gbase, voff) PG8_STAGE2(bufoff, gbase, (voff)[0], (voff)[1])
; #define PG8_LDA(dst, b, h) do { _Pragma("unroll") for (int m = 0; m < 4; ++m) _Pragma("unroll") for (int k = 0; k < 2; ++k) dst[m][k] = *(const LAS bf16x8*)(lds + PG8_SA(b, h) + aoff + m * 2048 + k * 1024); } while (0)
; #define PG8_LDB(dst, b, h) do { _Pragma("unroll") for (int n = 0; n < 2; ++n) _Pragma("unroll") for (int k = 0; k < 2; ++k) dst[n][k] = *(const LAS bf16x8*)(lds + PG8_SB(b, h) + boff + n * 2048 + k * 1024); } while (0)
; #define PG8_WAIT_V(n) asm volatile("s_waitcnt vmcnt(" #n ")" ::: "memory")
; #define PG8_WAIT_L(n) asm volatile("s_waitcnt lgkmcnt(" #n ")" ::: "memory")
; #define PG8_BAR __builtin_amdgcn_s_barrier()
; #define PG8_SCHED __builtin_amdgcn_sched_barrier(0)
; template <class Epi, class Sched, bool ALIGN_EPI, bool SP2, bool GATHER>
; DI void gemm_phase(LAS unsigned char* lds, const Gemm g, const Sched& S, const Epi& E) {
;     ...
;             const bool last = (t == nt - 2);
;             const char* a1 = cA + (size_t)(t + 1) * kstep;
;             const char* a2 = last ? nA : cA + (size_t)(t + 2) * kstep; const char* b2 = last ? nB : cB + (size_t)(t + 2) * kstep;
;             const char* a3 = a2 + kstep; const char* b3 = b2 + kstep;
;             unsigned x00 = gC[0][0], x01 = gC[0][1], x10 = gC[1][0], x11 = gC[1][1];
;             if constexpr (GATHER) { if (last) { x00 = gN[0][0]; x01 = gN[0][1]; x10 = gN[1][0]; x11 = gN[1][1]; } }
;             PG8_LDB(B0, 0, 0); PG8_LDB(B1, 0, 1); PG8_SCHED; PG8_LDA(At, 0, 0); PG8_STAGE2(PG8_SA(1, 1), a1 + hstepA, gC[1][0], gC[1][1]);
;             PG8_WAIT_V(8); PG8_WAIT_L(0); PG8_BAR; PG8_MMA(0, 0, At, B0); PG8_MMA(0, 1, At, B1); PG8_BAR; PG8_SCHED;
;             PG8_LDA(At, 0, 1); PG8_STAGE(PG8_SB(0, 0), b2, voffB); PG8_STAGE(PG8_SB(0, 1), b2 + hstep, voffB); PG8_STAGE2(PG8_SA(0, 0), a2, x00, x01);
;             PG8_WAIT_V(8); PG8_WAIT_L(0); PG8_BAR; PG8_MMA(1, 0, At, B0); PG8_MMA(1, 1, At, B1); PG8_BAR; PG8_SCHED;
.LBB0_601:
	v_add_u32_e32 v3, s74, v180
	ds_read_b128 v[132:135], v3
	ds_read_b128 v[136:139], v3 offset:1024
	ds_read_b128 v[140:143], v3 offset:2048
	ds_read_b128 v[144:147], v3 offset:3072
	v_add_u32_e32 v3, s75, v180
	s_add_u32 s52, s48, s50
	ds_read_b128 v[148:151], v3
	ds_read_b128 v[152:155], v3 offset:1024
	ds_read_b128 v[184:187], v3 offset:2048
	ds_read_b128 v[188:191], v3 offset:3072
	s_addc_u32 s53, s49, s51
	s_add_u32 s52, s52, 0x100
	s_addc_u32 s53, s53, 0
	s_add_u32 s62, s82, s50
	s_addc_u32 s85, s83, s51
	s_cmpk_eq_i32 s50, 0x1300
	s_cselect_b32 s55, s5, s53
	s_cselect_b32 s54, s4, s52
	s_cselect_b32 s53, s47, s85
	s_cselect_b32 s52, s46, s62
	v_lshl_add_u64 v[176:177], v[172:173], 0, s[50:51]
	s_add_i32 m0, s64, 0xc000
	ds_read_b128 v[192:195], v182
	ds_read_b128 v[196:199], v182 offset:1024
	ds_read_b128 v[200:203], v182 offset:2048
	ds_read_b128 v[204:207], v182 offset:3072
	ds_read_b128 v[208:211], v182 offset:4096
	ds_read_b128 v[212:215], v182 offset:5120
	ds_read_b128 v[216:219], v182 offset:6144
	ds_read_b128 v[220:223], v182 offset:7168
	global_load_lds_dwordx4 v[176:177], off
	v_lshl_add_u64 v[176:177], v[174:175], 0, s[50:51]
	s_add_i32 m0, s64, 0xe000
	s_nop 0
	global_load_lds_dwordx4 v[176:177], off
	s_waitcnt vmcnt(8)
	s_waitcnt lgkmcnt(0)
	s_barrier
	s_setprio 1
	s_waitcnt lgkmcnt(0)
	s_nop 0
	v_mfma_f32_16x16x32_bf16 v[128:131], v[132:135], v[192:195], v[128:131]
	v_mfma_f32_16x16x32_bf16 v[124:127], v[140:143], v[192:195], v[124:127]
	v_mfma_f32_16x16x32_bf16 v[112:115], v[132:135], v[200:203], v[112:115]
	v_mfma_f32_16x16x32_bf16 v[108:111], v[140:143], v[200:203], v[108:111]
	v_mfma_f32_16x16x32_bf16 v[96:99], v[132:135], v[208:211], v[96:99]
	v_mfma_f32_16x16x32_bf16 v[92:95], v[140:143], v[208:211], v[92:95]
	v_mfma_f32_16x16x32_bf16 v[80:83], v[132:135], v[216:219], v[80:83]
	v_mfma_f32_16x16x32_bf16 v[76:79], v[140:143], v[216:219], v[76:79]
	v_mfma_f32_16x16x32_bf16 v[128:131], v[136:139], v[196:199], v[128:131]
	v_mfma_f32_16x16x32_bf16 v[124:127], v[144:147], v[196:199], v[124:127]
	v_mfma_f32_16x16x32_bf16 v[112:115], v[136:139], v[204:207], v[112:115]
	v_mfma_f32_16x16x32_bf16 v[108:111], v[144:147], v[204:207], v[108:111]
	v_mfma_f32_16x16x32_bf16 v[96:99], v[136:139], v[212:215], v[96:99]
	v_mfma_f32_16x16x32_bf16 v[92:95], v[144:147], v[212:215], v[92:95]
	v_mfma_f32_16x16x32_bf16 v[80:83], v[136:139], v[220:223], v[80:83]
	v_mfma_f32_16x16x32_bf16 v[76:79], v[144:147], v[220:223], v[76:79]
	s_setprio 0
	s_setprio 1
	v_mfma_f32_16x16x32_bf16 v[120:123], v[148:151], v[192:195], v[120:123]
	v_mfma_f32_16x16x32_bf16 v[116:119], v[184:187], v[192:195], v[116:119]
	v_mfma_f32_16x16x32_bf16 v[104:107], v[148:151], v[200:203], v[104:107]
	v_mfma_f32_16x16x32_bf16 v[100:103], v[184:187], v[200:203], v[100:103]
	v_mfma_f32_16x16x32_bf16 v[88:91], v[148:151], v[208:211], v[88:91]
	v_mfma_f32_16x16x32_bf16 v[84:87], v[184:187], v[208:211], v[84:87]
	v_mfma_f32_16x16x32_bf16 v[72:75], v[148:151], v[216:219], v[72:75]
	v_mfma_f32_16x16x32_bf16 v[68:71], v[184:187], v[216:219], v[68:71]
	v_mfma_f32_16x16x32_bf16 v[120:123], v[152:155], v[196:199], v[120:123]
	v_mfma_f32_16x16x32_bf16 v[116:119], v[188:191], v[196:199], v[116:119]
	v_mfma_f32_16x16x32_bf16 v[104:107], v[152:155], v[204:207], v[104:107]
	v_mfma_f32_16x16x32_bf16 v[100:103], v[188:191], v[204:207], v[100:103]
	v_mfma_f32_16x16x32_bf16 v[88:91], v[152:155], v[212:215], v[88:91]
	v_mfma_f32_16x16x32_bf16 v[84:87], v[188:191], v[212:215], v[84:87]
	v_mfma_f32_16x16x32_bf16 v[72:75], v[152:155], v[220:223], v[72:75]
	v_mfma_f32_16x16x32_bf16 v[68:71], v[188:191], v[220:223], v[68:71]
	s_setprio 0
	s_barrier
	s_add_i32 s62, s74, s63
	v_lshl_add_u64 v[176:177], s[52:53], 0, v[158:159]
	s_mov_b32 m0, s62
	ds_read_b128 v[192:195], v182 offset:16384
	ds_read_b128 v[196:199], v182 offset:17408
	ds_read_b128 v[200:203], v182 offset:18432
	ds_read_b128 v[204:207], v182 offset:19456
	ds_read_b128 v[208:211], v182 offset:20480
	ds_read_b128 v[212:215], v182 offset:21504
	ds_read_b128 v[216:219], v182 offset:22528
	ds_read_b128 v[220:223], v182 offset:23552
	global_load_lds_dwordx4 v[176:177], off
	s_add_i32 m0, s62, 0x2000
	s_add_u32 s86, s52, 0xa0000
	v_lshl_add_u64 v[224:225], s[52:53], 0, v[162:163]
	s_addc_u32 s87, s53, 0
	s_add_i32 s62, s75, s63
	global_load_lds_dwordx4 v[224:225], off
	v_lshl_add_u64 v[226:227], s[86:87], 0, v[158:159]
	s_mov_b32 m0, s62
	v_lshl_add_u64 v[228:229], s[54:55], 0, v[160:161]
	global_load_lds_dwordx4 v[226:227], off
	v_lshl_add_u64 v[226:227], s[86:87], 0, v[162:163]
	s_add_i32 m0, s62, 0x2000
	s_nop 0
	global_load_lds_dwordx4 v[226:227], off
	v_lshl_add_u64 v[226:227], s[54:55], 0, v[156:157]
	s_mov_b32 m0, s64
	s_nop 0
	global_load_lds_dwordx4 v[226:227], off
	s_mov_b32 m0, s65
	s_nop 0
	global_load_lds_dwordx4 v[228:229], off
	s_waitcnt vmcnt(8)
	s_waitcnt lgkmcnt(0)
	s_barrier
; #define PG8_STAGE2(bufoff, gbase, v0, v1) do { \
;         __builtin_amdgcn_global_load_lds((const unsigned*)((const char*)(gbase) + (v0)), (LAS unsigned*)(lds + (bufoff) + ldsw), 16, 0, 0); \
;         __builtin_amdgcn_global_load_lds((const unsigned*)((const char*)(gbase) + (v1)), (LAS unsigned*)(lds + (bufoff) + ldsw + 8192), 16, 0, 0); } while (0)
; #define PG8_LDA(dst, b, h) do { _Pragma("unroll") for (int m = 0; m < 4; ++m) _Pragma("unroll") for (int k = 0; k < 2; ++k) dst[m][k] = *(const LAS bf16x8*)(lds + PG8_SA(b, h) + aoff + m * 2048 + k * 1024); } while (0)
; #define PG8_LDB(dst, b, h) do { _Pragma("unroll") for (int n = 0; n < 2; ++n) _Pragma("unroll") for (int k = 0; k < 2; ++k) dst[n][k] = *(const LAS bf16x8*)(lds + PG8_SB(b, h) + boff + n * 2048 + k * 1024); } while (0)
; #define PG8_MMA(ai, bj, At, Bt) do { __builtin_amdgcn_s_setprio(1); _Pragma("unroll") for (int m = 0; m < 4; ++m) _Pragma("unroll") for (int n = 0; n < 2; ++n) _Pragma("unroll") for (int k = 0; k < 2; ++k) \
;         acc[ai][bj][m][n] = __builtin_amdgcn_mfma_f32_16x16x32_bf16(Bt[n][k], At[m][k], acc[ai][bj][m][n], 0, 0, 0); __builtin_amdgcn_s_setprio(0); } while (0)
; #define PG8_WAIT_V(n) asm volatile("s_waitcnt vmcnt(" #n ")" ::: "memory")
; #define PG8_WAIT_L(n) asm volatile("s_waitcnt lgkmcnt(" #n ")" ::: "memory")
; #define PG8_BAR __builtin_amdgcn_s_barrier()
; #define PG8_SCHED __builtin_amdgcn_sched_barrier(0)
; template <class Epi, class Sched, bool ALIGN_EPI, bool SP2, bool GATHER>
; DI void gemm_phase(LAS unsigned char* lds, const Gemm g, const Sched& S, const Epi& E) {
;     ...
;             PG8_WAIT_V(8); PG8_WAIT_L(0); PG8_BAR; PG8_MMA(1, 0, At, B0); PG8_MMA(1, 1, At, B1); PG8_BAR; PG8_SCHED;
;             PG8_LDB(B0, 1, 0); PG8_LDB(B1, 1, 1); PG8_SCHED; PG8_LDA(At, 1, 0); PG8_STAGE2(PG8_SA(0, 1), a2 + hstepA, x10, x11);
;             PG8_WAIT_V(8); PG8_WAIT_L(0); PG8_BAR; PG8_MMA(0, 0, At, B0); PG8_MMA(0, 1, At, B1); PG8_BAR; PG8_SCHED;
	s_setprio 1
	s_waitcnt lgkmcnt(0)
	s_nop 0
	v_mfma_f32_16x16x32_bf16 v[64:67], v[132:135], v[192:195], v[64:67]
	v_mfma_f32_16x16x32_bf16 v[60:63], v[140:143], v[192:195], v[60:63]
	v_mfma_f32_16x16x32_bf16 v[48:51], v[132:135], v[200:203], v[48:51]
	v_mfma_f32_16x16x32_bf16 v[44:47], v[140:143], v[200:203], v[44:47]
	v_mfma_f32_16x16x32_bf16 v[32:35], v[132:135], v[208:211], v[32:35]
	v_mfma_f32_16x16x32_bf16 v[28:31], v[140:143], v[208:211], v[28:31]
	v_mfma_f32_16x16x32_bf16 v[16:19], v[132:135], v[216:219], v[16:19]
	v_mfma_f32_16x16x32_bf16 v[12:15], v[140:143], v[216:219], v[12:15]
	v_mfma_f32_16x16x32_bf16 v[64:67], v[136:139], v[196:199], v[64:67]
	v_mfma_f32_16x16x32_bf16 v[60:63], v[144:147], v[196:199], v[60:63]
	v_mfma_f32_16x16x32_bf16 v[48:51], v[136:139], v[204:207], v[48:51]
	v_mfma_f32_16x16x32_bf16 v[44:47], v[144:147], v[204:207], v[44:47]
	v_mfma_f32_16x16x32_bf16 v[32:35], v[136:139], v[212:215], v[32:35]
	v_mfma_f32_16x16x32_bf16 v[28:31], v[144:147], v[212:215], v[28:31]
	v_mfma_f32_16x16x32_bf16 v[16:19], v[136:139], v[220:223], v[16:19]
	v_mfma_f32_16x16x32_bf16 v[12:15], v[144:147], v[220:223], v[12:15]
	s_setprio 0
	s_setprio 1
	v_mfma_f32_16x16x32_bf16 v[56:59], v[148:151], v[192:195], v[56:59]
	v_mfma_f32_16x16x32_bf16 v[52:55], v[184:187], v[192:195], v[52:55]
	v_mfma_f32_16x16x32_bf16 v[40:43], v[148:151], v[200:203], v[40:43]
	v_mfma_f32_16x16x32_bf16 v[36:39], v[184:187], v[200:203], v[36:39]
	v_mfma_f32_16x16x32_bf16 v[24:27], v[148:151], v[208:211], v[24:27]
	v_mfma_f32_16x16x32_bf16 v[20:23], v[184:187], v[208:211], v[20:23]
	v_mfma_f32_16x16x32_bf16 v[8:11], v[148:151], v[216:219], v[8:11]
	v_mfma_f32_16x16x32_bf16 v[4:7], v[184:187], v[216:219], v[4:7]
	v_mfma_f32_16x16x32_bf16 v[56:59], v[152:155], v[196:199], v[56:59]
	v_mfma_f32_16x16x32_bf16 v[52:55], v[188:191], v[196:199], v[52:55]
	v_mfma_f32_16x16x32_bf16 v[40:43], v[152:155], v[204:207], v[40:43]
	v_mfma_f32_16x16x32_bf16 v[36:39], v[188:191], v[204:207], v[36:39]
	v_mfma_f32_16x16x32_bf16 v[24:27], v[152:155], v[212:215], v[24:27]
	v_mfma_f32_16x16x32_bf16 v[20:23], v[188:191], v[212:215], v[20:23]
	v_mfma_f32_16x16x32_bf16 v[8:11], v[152:155], v[220:223], v[8:11]
	v_mfma_f32_16x16x32_bf16 v[4:7], v[188:191], v[220:223], v[4:7]
	s_setprio 0
	s_barrier
	s_add_i32 s62, 0, 0x18000
	v_add_u32_e32 v3, s62, v180
	s_add_i32 s85, 0, 0x1c000
	ds_read_b128 v[132:135], v3
	ds_read_b128 v[136:139], v3 offset:1024
	ds_read_b128 v[140:143], v3 offset:2048
	ds_read_b128 v[144:147], v3 offset:3072
	v_add_u32_e32 v3, s85, v180
	ds_read_b128 v[148:151], v3
	ds_read_b128 v[152:155], v3 offset:1024
	ds_read_b128 v[184:187], v3 offset:2048
	ds_read_b128 v[188:191], v3 offset:3072
	s_add_u32 s54, s54, 0xa0000
	s_addc_u32 s55, s55, 0
	s_mov_b32 m0, s66
	v_lshl_add_u64 v[230:231], s[54:55], 0, v[156:157]
	ds_read_b128 v[192:195], v182 offset:32768
	ds_read_b128 v[196:199], v182 offset:33792
	ds_read_b128 v[200:203], v182 offset:34816
	ds_read_b128 v[204:207], v182 offset:35840
	ds_read_b128 v[208:211], v182 offset:36864
	ds_read_b128 v[212:215], v182 offset:37888
	ds_read_b128 v[216:219], v182 offset:38912
	ds_read_b128 v[220:223], v182 offset:39936
	global_load_lds_dwordx4 v[230:231], off
	v_lshl_add_u64 v[230:231], s[54:55], 0, v[160:161]
	s_mov_b32 m0, s67
	s_nop 0
	global_load_lds_dwordx4 v[230:231], off
	s_waitcnt vmcnt(8)
	s_waitcnt lgkmcnt(0)
	s_barrier
	s_setprio 1
	s_waitcnt lgkmcnt(0)
	s_nop 0
	v_mfma_f32_16x16x32_bf16 v[128:131], v[132:135], v[192:195], v[128:131]
	v_mfma_f32_16x16x32_bf16 v[124:127], v[140:143], v[192:195], v[124:127]
	v_mfma_f32_16x16x32_bf16 v[112:115], v[132:135], v[200:203], v[112:115]
	v_mfma_f32_16x16x32_bf16 v[108:111], v[140:143], v[200:203], v[108:111]
	v_mfma_f32_16x16x32_bf16 v[96:99], v[132:135], v[208:211], v[96:99]
	v_mfma_f32_16x16x32_bf16 v[92:95], v[140:143], v[208:211], v[92:95]
	v_mfma_f32_16x16x32_bf16 v[80:83], v[132:135], v[216:219], v[80:83]
	v_mfma_f32_16x16x32_bf16 v[76:79], v[140:143], v[216:219], v[76:79]
	v_mfma_f32_16x16x32_bf16 v[128:131], v[136:139], v[196:199], v[128:131]
	v_mfma_f32_16x16x32_bf16 v[124:127], v[144:147], v[196:199], v[124:127]
	v_mfma_f32_16x16x32_bf16 v[112:115], v[136:139], v[204:207], v[112:115]
	v_mfma_f32_16x16x32_bf16 v[108:111], v[144:147], v[204:207], v[108:111]
	v_mfma_f32_16x16x32_bf16 v[96:99], v[136:139], v[212:215], v[96:99]
	v_mfma_f32_16x16x32_bf16 v[92:95], v[144:147], v[212:215], v[92:95]
	v_mfma_f32_16x16x32_bf16 v[80:83], v[136:139], v[220:223], v[80:83]
	v_mfma_f32_16x16x32_bf16 v[76:79], v[144:147], v[220:223], v[76:79]
	s_setprio 0
	s_setprio 1
	v_mfma_f32_16x16x32_bf16 v[120:123], v[148:151], v[192:195], v[120:123]
	v_mfma_f32_16x16x32_bf16 v[116:119], v[184:187], v[192:195], v[116:119]
	v_mfma_f32_16x16x32_bf16 v[104:107], v[148:151], v[200:203], v[104:107]
	v_mfma_f32_16x16x32_bf16 v[100:103], v[184:187], v[200:203], v[100:103]
	v_mfma_f32_16x16x32_bf16 v[88:91], v[148:151], v[208:211], v[88:91]
	v_mfma_f32_16x16x32_bf16 v[84:87], v[184:187], v[208:211], v[84:87]
	v_mfma_f32_16x16x32_bf16 v[72:75], v[148:151], v[216:219], v[72:75]
	v_mfma_f32_16x16x32_bf16 v[68:71], v[184:187], v[216:219], v[68:71]
	v_mfma_f32_16x16x32_bf16 v[120:123], v[152:155], v[196:199], v[120:123]
	v_mfma_f32_16x16x32_bf16 v[116:119], v[188:191], v[196:199], v[116:119]
	v_mfma_f32_16x16x32_bf16 v[104:107], v[152:155], v[204:207], v[104:107]
	v_mfma_f32_16x16x32_bf16 v[100:103], v[188:191], v[204:207], v[100:103]
	v_mfma_f32_16x16x32_bf16 v[88:91], v[152:155], v[212:215], v[88:91]
	v_mfma_f32_16x16x32_bf16 v[84:87], v[188:191], v[212:215], v[84:87]
	v_mfma_f32_16x16x32_bf16 v[72:75], v[152:155], v[220:223], v[72:75]
	v_mfma_f32_16x16x32_bf16 v[68:71], v[188:191], v[220:223], v[68:71]
	s_setprio 0
	s_barrier
; #define PG8_STAGE2(bufoff, gbase, v0, v1) do { \
;         __builtin_amdgcn_global_load_lds((const unsigned*)((const char*)(gbase) + (v0)), (LAS unsigned*)(lds + (bufoff) + ldsw), 16, 0, 0); \
;         __builtin_amdgcn_global_load_lds((const unsigned*)((const char*)(gbase) + (v1)), (LAS unsigned*)(lds + (bufoff) + ldsw + 8192), 16, 0, 0); } while (0)
; #define PG8_STAGE(bufoff, gbase, voff) PG8_STAGE2(bufoff, gbase, (voff)[0], (voff)[1])
; #define PG8_LDA(dst, b, h) do { _Pragma("unroll") for (int m = 0; m < 4; ++m) _Pragma("unroll") for (int k = 0; k < 2; ++k) dst[m][k] = *(const LAS bf16x8*)(lds + PG8_SA(b, h) + aoff + m * 2048 + k * 1024); } while (0)
; #define PG8_MMA(ai, bj, At, Bt) do { __builtin_amdgcn_s_setprio(1); _Pragma("unroll") for (int m = 0; m < 4; ++m) _Pragma("unroll") for (int n = 0; n < 2; ++n) _Pragma("unroll") for (int k = 0; k < 2; ++k) \
;         acc[ai][bj][m][n] = __builtin_amdgcn_mfma_f32_16x16x32_bf16(Bt[n][k], At[m][k], acc[ai][bj][m][n], 0, 0, 0); __builtin_amdgcn_s_setprio(0); } while (0)
; #define PG8_WAIT_V(n) asm volatile("s_waitcnt vmcnt(" #n ")" ::: "memory")
; #define PG8_WAIT_L(n) asm volatile("s_waitcnt lgkmcnt(" #n ")" ::: "memory")
; #define PG8_BAR __builtin_amdgcn_s_barrier()
; #define PG8_SCHED __builtin_amdgcn_sched_barrier(0)
; template <class Epi, class Sched, bool ALIGN_EPI, bool SP2, bool GATHER>
; DI void gemm_phase(LAS unsigned char* lds, const Gemm g, const Sched& S, const Epi& E) {
;     ...
;             PG8_LDA(At, 1, 1); PG8_STAGE(PG8_SB(1, 0), b3, voffB); PG8_STAGE(PG8_SB(1, 1), b3 + hstep, voffB); PG8_STAGE2(PG8_SA(1, 0), a3, x00, x01);
;             PG8_WAIT_V(8); PG8_WAIT_L(0); PG8_BAR; PG8_MMA(1, 0, At, B0); PG8_MMA(1, 1, At, B1); PG8_BAR; PG8_SCHED;
;         }
	s_add_i32 s54, s62, s63
	v_lshl_add_u64 v[176:177], v[176:177], 0, s[18:19]
	s_mov_b32 m0, s54
	ds_read_b128 v[192:195], v182 offset:49152
	ds_read_b128 v[196:199], v182 offset:50176
	ds_read_b128 v[200:203], v182 offset:51200
	ds_read_b128 v[204:207], v182 offset:52224
	ds_read_b128 v[208:211], v182 offset:53248
	ds_read_b128 v[212:215], v182 offset:54272
	ds_read_b128 v[216:219], v182 offset:55296
	ds_read_b128 v[220:223], v182 offset:56320
	global_load_lds_dwordx4 v[176:177], off
	s_add_i32 m0, s54, 0x2000
	s_add_u32 s52, s52, 0xa0080
	v_lshl_add_u64 v[176:177], v[224:225], 0, s[18:19]
	s_addc_u32 s53, s53, 0
	s_add_i32 s54, s85, s63
	global_load_lds_dwordx4 v[176:177], off
	v_lshl_add_u64 v[176:177], s[52:53], 0, v[158:159]
	s_mov_b32 m0, s54
	s_nop 0
	global_load_lds_dwordx4 v[176:177], off
	v_lshl_add_u64 v[176:177], s[52:53], 0, v[162:163]
	s_add_i32 m0, s54, 0x2000
	s_nop 0
	global_load_lds_dwordx4 v[176:177], off
	v_lshl_add_u64 v[176:177], v[226:227], 0, s[18:19]
	s_mov_b32 m0, s71
	s_nop 0
	global_load_lds_dwordx4 v[176:177], off
	v_lshl_add_u64 v[176:177], v[228:229], 0, s[18:19]
	s_mov_b32 m0, s72
	s_nop 0
	global_load_lds_dwordx4 v[176:177], off
	s_waitcnt vmcnt(8)
	s_waitcnt lgkmcnt(0)
	s_barrier
	s_setprio 1
	s_waitcnt lgkmcnt(0)
	v_mfma_f32_16x16x32_bf16 v[64:67], v[132:135], v[192:195], v[64:67]
	v_mfma_f32_16x16x32_bf16 v[60:63], v[140:143], v[192:195], v[60:63]
	v_mfma_f32_16x16x32_bf16 v[48:51], v[132:135], v[200:203], v[48:51]
	v_mfma_f32_16x16x32_bf16 v[44:47], v[140:143], v[200:203], v[44:47]
	v_mfma_f32_16x16x32_bf16 v[32:35], v[132:135], v[208:211], v[32:35]
	v_mfma_f32_16x16x32_bf16 v[28:31], v[140:143], v[208:211], v[28:31]
	v_mfma_f32_16x16x32_bf16 v[16:19], v[132:135], v[216:219], v[16:19]
	v_mfma_f32_16x16x32_bf16 v[12:15], v[140:143], v[216:219], v[12:15]
	v_mfma_f32_16x16x32_bf16 v[64:67], v[136:139], v[196:199], v[64:67]
	v_mfma_f32_16x16x32_bf16 v[60:63], v[144:147], v[196:199], v[60:63]
	v_mfma_f32_16x16x32_bf16 v[48:51], v[136:139], v[204:207], v[48:51]
	v_mfma_f32_16x16x32_bf16 v[44:47], v[144:147], v[204:207], v[44:47]
	v_mfma_f32_16x16x32_bf16 v[32:35], v[136:139], v[212:215], v[32:35]
	v_mfma_f32_16x16x32_bf16 v[28:31], v[144:147], v[212:215], v[28:31]
	v_mfma_f32_16x16x32_bf16 v[16:19], v[136:139], v[220:223], v[16:19]
	v_mfma_f32_16x16x32_bf16 v[12:15], v[144:147], v[220:223], v[12:15]
	s_setprio 0
	s_setprio 1
	v_mfma_f32_16x16x32_bf16 v[56:59], v[148:151], v[192:195], v[56:59]
	v_mfma_f32_16x16x32_bf16 v[52:55], v[184:187], v[192:195], v[52:55]
	v_mfma_f32_16x16x32_bf16 v[40:43], v[148:151], v[200:203], v[40:43]
	v_mfma_f32_16x16x32_bf16 v[36:39], v[184:187], v[200:203], v[36:39]
	v_mfma_f32_16x16x32_bf16 v[24:27], v[148:151], v[208:211], v[24:27]
	v_mfma_f32_16x16x32_bf16 v[20:23], v[184:187], v[208:211], v[20:23]
	v_mfma_f32_16x16x32_bf16 v[8:11], v[148:151], v[216:219], v[8:11]
	v_mfma_f32_16x16x32_bf16 v[4:7], v[184:187], v[216:219], v[4:7]
	v_mfma_f32_16x16x32_bf16 v[56:59], v[152:155], v[196:199], v[56:59]
	v_mfma_f32_16x16x32_bf16 v[52:55], v[188:191], v[196:199], v[52:55]
	v_mfma_f32_16x16x32_bf16 v[40:43], v[152:155], v[204:207], v[40:43]
	v_mfma_f32_16x16x32_bf16 v[36:39], v[188:191], v[204:207], v[36:39]
	v_mfma_f32_16x16x32_bf16 v[24:27], v[152:155], v[212:215], v[24:27]
	v_mfma_f32_16x16x32_bf16 v[20:23], v[188:191], v[212:215], v[20:23]
	v_mfma_f32_16x16x32_bf16 v[8:11], v[152:155], v[220:223], v[8:11]
	v_mfma_f32_16x16x32_bf16 v[4:7], v[188:191], v[220:223], v[4:7]
	s_setprio 0
	s_barrier
	s_add_i32 s84, s84, 2
	s_add_u32 s50, s50, 0x100
	s_addc_u32 s51, s51, 0
	s_cmp_gt_u32 s84, 37
	s_cbranch_scc1 .LBB0_604

; #define PG8_STAGE2(bufoff, gbase, v0, v1) do { \
;         __builtin_amdgcn_global_load_lds((const unsigned*)((const char*)(gbase) + (v0)), (LAS unsigned*)(lds + (bufoff) + ldsw), 16, 0, 0); \
;         __builtin_amdgcn_global_load_lds((const unsigned*)((const char*)(gbase) + (v1)), (LAS unsigned*)(lds + (bufoff) + ldsw + 8192), 16, 0, 0); } while (0)
; #define PG8_STAGE(bufoff, gbase, voff) PG8_STAGE2(bufoff, gbase, (voff)[0], (voff)[1])
; #define PG8_WAIT_V(n) asm volatile("s_waitcnt vmcnt(" #n ")" ::: "memory")
; #define PG8_WAIT_L(n) asm volatile("s_waitcnt lgkmcnt(" #n ")" ::: "memory")
; template <class Epi, class Sched, bool ALIGN_EPI, bool SP2, bool GATHER>
; DI void gemm_phase(LAS unsigned char* lds, const Gemm g, const Sched& S, const Epi& E) {
;     ...
;         const bool has_next = S.next(ui + 1, nxt);
;         const char* nA = (has_next && !GATHER) ? (const char*)g.A + (size_t)nxt.pm * tstep : cA; const char* nB = has_next ? (const char*)g.Bt + (size_t)nxt.pn * tstep : cB;
;         if constexpr (GATHER) { if (has_next) { PG8_GATHER(nxt, gN); } else {
; #pragma unroll
;             for (int h = 0; h < 2; ++h) { gN[h][0] = gC[h][0]; gN[h][1] = gC[h][1]; } } }
;         for (int t = 0; t < nt; t += 2) {
;             if constexpr (Epi::MID_T >= 0) { if (t == Epi::MID_T) { E.mid(acc, cur, wr, wc, fr, fq); PG8_SCHED; } }
;             const bool last = (t == nt - 2);
;             const char* a1 = cA + (size_t)(t + 1) * kstep;
;             const char* a2 = last ? nA : cA + (size_t)(t + 2) * kstep; const char* b2 = last ? nB : cB + (size_t)(t + 2) * kstep;
;             const char* a3 = a2 + kstep; const char* b3 = b2 + kstep;
;             unsigned x00 = gC[0][0], x01 = gC[0][1], x10 = gC[1][0], x11 = gC[1][1];
;             if constexpr (GATHER) { if (last) { x00 = gN[0][0]; x01 = gN[0][1]; x10 = gN[1][0]; x11 = gN[1][1]; } }
;             PG8_LDB(B0, 0, 0); PG8_LDB(B1, 0, 1); PG8_SCHED; PG8_LDA(At, 0, 0); PG8_STAGE2(PG8_SA(1, 1), a1 + hstepA, gC[1][0], gC[1][1]);
;             PG8_WAIT_V(8); PG8_WAIT_L(0); PG8_BAR; PG8_MMA(0, 0, At, B0); PG8_MMA(0, 1, At, B1); PG8_BAR; PG8_SCHED;
;             PG8_LDA(At, 0, 1); PG8_STAGE(PG8_SB(0, 0), b2, voffB); PG8_STAGE(PG8_SB(0, 1), b2 + hstep, voffB); PG8_STAGE2(PG8_SA(0, 0), a2, x00, x01);
;             PG8_WAIT_V(8); PG8_WAIT_L(0); PG8_BAR; PG8_MMA(1, 0, At, B0); PG8_MMA(1, 1, At, B1); PG8_BAR; PG8_SCHED;
.LBB0_673:
	s_ashr_i32 s27, s26, 31
	s_lshl_b64 s[28:29], s[26:27], 20
	s_add_u32 s28, s38, s28
	s_addc_u32 s29, s39, s29
	s_and_b64 s[30:31], s[4:5], exec
	s_cselect_b32 s27, s29, s37
	s_cselect_b32 s57, s28, s36
	s_ashr_i32 s25, s24, 31
	s_lshl_b64 s[30:31], s[24:25], 20
	s_add_u32 s30, s44, s30
	s_addc_u32 s31, s45, s31
	s_and_b64 s[42:43], s[4:5], exec
	s_cselect_b32 s25, s31, s41
	s_cselect_b32 s63, s30, s40
	s_add_u32 s36, s36, 0x80080
	s_addc_u32 s37, s37, 0
	s_add_u32 s64, s40, 0x100
	s_addc_u32 s65, s41, 0
	s_mov_b32 s66, -2
	ds_read_b128 v[146:149], v154
	ds_read_b128 v[158:161], v154 offset:1024
	ds_read_b128 v[162:165], v154 offset:2048
	ds_read_b128 v[166:169], v154 offset:3072
	ds_read_b128 v[170:173], v155
	ds_read_b128 v[174:177], v155 offset:1024
	ds_read_b128 v[178:181], v155 offset:2048
	ds_read_b128 v[182:185], v155 offset:3072
	s_add_u32 s40, s36, 0xfff80080
	s_addc_u32 s41, s37, -1
	s_cmp_eq_u32 s66, 28
	s_cselect_b32 s43, s27, s41
	s_cselect_b32 s42, s57, s40
	s_cselect_b32 s41, s25, s65
	s_cselect_b32 s40, s63, s64
	v_lshl_add_u64 v[150:151], s[36:37], 0, v[138:139]
	s_add_i32 m0, s35, 0xc000
	ds_read_b128 v[186:189], v156
	ds_read_b128 v[190:193], v156 offset:1024
	ds_read_b128 v[194:197], v156 offset:2048
	ds_read_b128 v[198:201], v156 offset:3072
	ds_read_b128 v[202:205], v156 offset:4096
	ds_read_b128 v[206:209], v156 offset:5120
	ds_read_b128 v[210:213], v156 offset:6144
	ds_read_b128 v[214:217], v156 offset:7168
	global_load_lds_dwordx4 v[150:151], off
	v_lshl_add_u64 v[150:151], s[36:37], 0, v[140:141]
	s_add_i32 m0, s35, 0xe000
	s_nop 0
	global_load_lds_dwordx4 v[150:151], off
	s_waitcnt vmcnt(8)
	s_waitcnt lgkmcnt(0)
	s_barrier
	s_setprio 1
	s_waitcnt lgkmcnt(0)
	s_nop 0
	v_mfma_f32_16x16x32_bf16 v[126:129], v[146:149], v[186:189], 0
	v_mfma_f32_16x16x32_bf16 v[122:125], v[162:165], v[186:189], 0
	v_mfma_f32_16x16x32_bf16 v[110:113], v[146:149], v[194:197], 0
	v_mfma_f32_16x16x32_bf16 v[106:109], v[162:165], v[194:197], 0
	v_mfma_f32_16x16x32_bf16 v[94:97], v[146:149], v[202:205], 0
	v_mfma_f32_16x16x32_bf16 v[90:93], v[162:165], v[202:205], 0
	v_mfma_f32_16x16x32_bf16 v[78:81], v[146:149], v[210:213], 0
	v_mfma_f32_16x16x32_bf16 v[74:77], v[162:165], v[210:213], 0
	v_mfma_f32_16x16x32_bf16 v[126:129], v[158:161], v[190:193], v[126:129]
	v_mfma_f32_16x16x32_bf16 v[122:125], v[166:169], v[190:193], v[122:125]
	v_mfma_f32_16x16x32_bf16 v[110:113], v[158:161], v[198:201], v[110:113]
	v_mfma_f32_16x16x32_bf16 v[106:109], v[166:169], v[198:201], v[106:109]
	v_mfma_f32_16x16x32_bf16 v[94:97], v[158:161], v[206:209], v[94:97]
	v_mfma_f32_16x16x32_bf16 v[90:93], v[166:169], v[206:209], v[90:93]
	v_mfma_f32_16x16x32_bf16 v[78:81], v[158:161], v[214:217], v[78:81]
	v_mfma_f32_16x16x32_bf16 v[74:77], v[166:169], v[214:217], v[74:77]
	s_setprio 0
	s_setprio 1
	v_mfma_f32_16x16x32_bf16 v[118:121], v[170:173], v[186:189], 0
	v_mfma_f32_16x16x32_bf16 v[114:117], v[178:181], v[186:189], 0
	v_mfma_f32_16x16x32_bf16 v[102:105], v[170:173], v[194:197], 0
	v_mfma_f32_16x16x32_bf16 v[98:101], v[178:181], v[194:197], 0
	v_mfma_f32_16x16x32_bf16 v[86:89], v[170:173], v[202:205], 0
	v_mfma_f32_16x16x32_bf16 v[82:85], v[178:181], v[202:205], 0
	v_mfma_f32_16x16x32_bf16 v[70:73], v[170:173], v[210:213], 0
	v_mfma_f32_16x16x32_bf16 v[66:69], v[178:181], v[210:213], 0
	v_mfma_f32_16x16x32_bf16 v[118:121], v[174:177], v[190:193], v[118:121]
	v_mfma_f32_16x16x32_bf16 v[114:117], v[182:185], v[190:193], v[114:117]
	v_mfma_f32_16x16x32_bf16 v[102:105], v[174:177], v[198:201], v[102:105]
	v_mfma_f32_16x16x32_bf16 v[98:101], v[182:185], v[198:201], v[98:101]
	v_mfma_f32_16x16x32_bf16 v[86:89], v[174:177], v[206:209], v[86:89]
	v_mfma_f32_16x16x32_bf16 v[82:85], v[182:185], v[206:209], v[82:85]
	v_mfma_f32_16x16x32_bf16 v[70:73], v[174:177], v[214:217], v[70:73]
	v_mfma_f32_16x16x32_bf16 v[66:69], v[182:185], v[214:217], v[66:69]
	s_setprio 0
	s_barrier
	s_add_i32 s62, s54, s46
	v_lshl_add_u64 v[150:151], s[40:41], 0, v[132:133]
	s_mov_b32 m0, s62
	ds_read_b128 v[186:189], v156 offset:16384
	ds_read_b128 v[190:193], v156 offset:17408
	ds_read_b128 v[194:197], v156 offset:18432
	ds_read_b128 v[198:201], v156 offset:19456
	ds_read_b128 v[202:205], v156 offset:20480
	ds_read_b128 v[206:209], v156 offset:21504
	ds_read_b128 v[210:213], v156 offset:22528
	ds_read_b128 v[214:217], v156 offset:23552
	global_load_lds_dwordx4 v[150:151], off
	s_add_i32 m0, s62, 0x2000
	s_add_u32 s68, s40, 0x80000
	v_lshl_add_u64 v[218:219], s[40:41], 0, v[136:137]
	s_addc_u32 s69, s41, 0
	s_add_i32 s62, s55, s46
	global_load_lds_dwordx4 v[218:219], off
	v_lshl_add_u64 v[220:221], s[68:69], 0, v[132:133]
	s_mov_b32 m0, s62
	v_lshl_add_u64 v[222:223], s[42:43], 0, v[134:135]
	global_load_lds_dwordx4 v[220:221], off
	v_lshl_add_u64 v[220:221], s[68:69], 0, v[136:137]
	s_add_i32 m0, s62, 0x2000
	s_nop 0
	global_load_lds_dwordx4 v[220:221], off
	v_lshl_add_u64 v[220:221], s[42:43], 0, v[130:131]
	s_mov_b32 m0, s35
	s_nop 0
	global_load_lds_dwordx4 v[220:221], off
	s_mov_b32 m0, s47
	s_nop 0
	global_load_lds_dwordx4 v[222:223], off
	s_waitcnt vmcnt(8)
	s_waitcnt lgkmcnt(0)
	s_barrier
; #define PG8_STAGE2(bufoff, gbase, v0, v1) do { \
;         __builtin_amdgcn_global_load_lds((const unsigned*)((const char*)(gbase) + (v0)), (LAS unsigned*)(lds + (bufoff) + ldsw), 16, 0, 0); \
;         __builtin_amdgcn_global_load_lds((const unsigned*)((const char*)(gbase) + (v1)), (LAS unsigned*)(lds + (bufoff) + ldsw + 8192), 16, 0, 0); } while (0)
; #define PG8_LDA(dst, b, h) do { _Pragma("unroll") for (int m = 0; m < 4; ++m) _Pragma("unroll") for (int k = 0; k < 2; ++k) dst[m][k] = *(const LAS bf16x8*)(lds + PG8_SA(b, h) + aoff + m * 2048 + k * 1024); } while (0)
; #define PG8_LDB(dst, b, h) do { _Pragma("unroll") for (int n = 0; n < 2; ++n) _Pragma("unroll") for (int k = 0; k < 2; ++k) dst[n][k] = *(const LAS bf16x8*)(lds + PG8_SB(b, h) + boff + n * 2048 + k * 1024); } while (0)
; #define PG8_MMA(ai, bj, At, Bt) do { __builtin_amdgcn_s_setprio(1); _Pragma("unroll") for (int m = 0; m < 4; ++m) _Pragma("unroll") for (int n = 0; n < 2; ++n) _Pragma("unroll") for (int k = 0; k < 2; ++k) \
;         acc[ai][bj][m][n] = __builtin_amdgcn_mfma_f32_16x16x32_bf16(Bt[n][k], At[m][k], acc[ai][bj][m][n], 0, 0, 0); __builtin_amdgcn_s_setprio(0); } while (0)
; #define PG8_WAIT_V(n) asm volatile("s_waitcnt vmcnt(" #n ")" ::: "memory")
; #define PG8_WAIT_L(n) asm volatile("s_waitcnt lgkmcnt(" #n ")" ::: "memory")
; #define PG8_BAR __builtin_amdgcn_s_barrier()
; #define PG8_SCHED __builtin_amdgcn_sched_barrier(0)
; template <class Epi, class Sched, bool ALIGN_EPI, bool SP2, bool GATHER>
; DI void gemm_phase(LAS unsigned char* lds, const Gemm g, const Sched& S, const Epi& E) {
;     ...
;             PG8_WAIT_V(8); PG8_WAIT_L(0); PG8_BAR; PG8_MMA(1, 0, At, B0); PG8_MMA(1, 1, At, B1); PG8_BAR; PG8_SCHED;
;             PG8_LDB(B0, 1, 0); PG8_LDB(B1, 1, 1); PG8_SCHED; PG8_LDA(At, 1, 0); PG8_STAGE2(PG8_SA(0, 1), a2 + hstepA, x10, x11);
;             PG8_WAIT_V(8); PG8_WAIT_L(0); PG8_BAR; PG8_MMA(0, 0, At, B0); PG8_MMA(0, 1, At, B1); PG8_BAR; PG8_SCHED;
	s_setprio 1
	s_waitcnt lgkmcnt(0)
	s_nop 0
	v_mfma_f32_16x16x32_bf16 v[62:65], v[146:149], v[186:189], 0
	v_mfma_f32_16x16x32_bf16 v[58:61], v[162:165], v[186:189], 0
	v_mfma_f32_16x16x32_bf16 v[46:49], v[146:149], v[194:197], 0
	v_mfma_f32_16x16x32_bf16 v[42:45], v[162:165], v[194:197], 0
	v_mfma_f32_16x16x32_bf16 v[22:25], v[146:149], v[202:205], 0
	v_mfma_f32_16x16x32_bf16 v[18:21], v[162:165], v[202:205], 0
	v_mfma_f32_16x16x32_bf16 v[6:9], v[146:149], v[210:213], 0
	v_mfma_f32_16x16x32_bf16 v[2:5], v[162:165], v[210:213], 0
	v_mfma_f32_16x16x32_bf16 v[62:65], v[158:161], v[190:193], v[62:65]
	v_mfma_f32_16x16x32_bf16 v[58:61], v[166:169], v[190:193], v[58:61]
	v_mfma_f32_16x16x32_bf16 v[46:49], v[158:161], v[198:201], v[46:49]
	v_mfma_f32_16x16x32_bf16 v[42:45], v[166:169], v[198:201], v[42:45]
	v_mfma_f32_16x16x32_bf16 v[22:25], v[158:161], v[206:209], v[22:25]
	v_mfma_f32_16x16x32_bf16 v[18:21], v[166:169], v[206:209], v[18:21]
	v_mfma_f32_16x16x32_bf16 v[6:9], v[158:161], v[214:217], v[6:9]
	v_mfma_f32_16x16x32_bf16 v[2:5], v[166:169], v[214:217], v[2:5]
	s_setprio 0
	s_setprio 1
	v_mfma_f32_16x16x32_bf16 v[54:57], v[170:173], v[186:189], 0
	v_mfma_f32_16x16x32_bf16 v[50:53], v[178:181], v[186:189], 0
	v_mfma_f32_16x16x32_bf16 v[30:33], v[170:173], v[194:197], 0
	v_mfma_f32_16x16x32_bf16 v[26:29], v[178:181], v[194:197], 0
	v_mfma_f32_16x16x32_bf16 v[34:37], v[170:173], v[202:205], 0
	v_mfma_f32_16x16x32_bf16 v[38:41], v[178:181], v[202:205], 0
	v_mfma_f32_16x16x32_bf16 v[10:13], v[170:173], v[210:213], 0
	v_mfma_f32_16x16x32_bf16 v[14:17], v[178:181], v[210:213], 0
	v_mfma_f32_16x16x32_bf16 v[54:57], v[174:177], v[190:193], v[54:57]
	v_mfma_f32_16x16x32_bf16 v[50:53], v[182:185], v[190:193], v[50:53]
	v_mfma_f32_16x16x32_bf16 v[30:33], v[174:177], v[198:201], v[30:33]
	v_mfma_f32_16x16x32_bf16 v[26:29], v[182:185], v[198:201], v[26:29]
	v_mfma_f32_16x16x32_bf16 v[34:37], v[174:177], v[206:209], v[34:37]
	v_mfma_f32_16x16x32_bf16 v[38:41], v[182:185], v[206:209], v[38:41]
	v_mfma_f32_16x16x32_bf16 v[10:13], v[174:177], v[214:217], v[10:13]
	v_mfma_f32_16x16x32_bf16 v[14:17], v[182:185], v[214:217], v[14:17]
	s_setprio 0
	s_barrier
	s_add_i32 s62, 0, 0x18000
	v_add_u32_e32 v157, s62, v152
	s_add_i32 s67, 0, 0x1c000
	ds_read_b128 v[146:149], v157
	ds_read_b128 v[158:161], v157 offset:1024
	ds_read_b128 v[162:165], v157 offset:2048
	ds_read_b128 v[166:169], v157 offset:3072
	v_add_u32_e32 v157, s67, v152
	ds_read_b128 v[170:173], v157
	ds_read_b128 v[174:177], v157 offset:1024
	ds_read_b128 v[178:181], v157 offset:2048
	ds_read_b128 v[182:185], v157 offset:3072
	s_add_u32 s42, s42, 0x80000
	s_addc_u32 s43, s43, 0
	s_mov_b32 m0, s48
	v_lshl_add_u64 v[224:225], s[42:43], 0, v[130:131]
	ds_read_b128 v[186:189], v156 offset:32768
	ds_read_b128 v[190:193], v156 offset:33792
	ds_read_b128 v[194:197], v156 offset:34816
	ds_read_b128 v[198:201], v156 offset:35840
	ds_read_b128 v[202:205], v156 offset:36864
	ds_read_b128 v[206:209], v156 offset:37888
	ds_read_b128 v[210:213], v156 offset:38912
	ds_read_b128 v[214:217], v156 offset:39936
	global_load_lds_dwordx4 v[224:225], off
	v_lshl_add_u64 v[224:225], s[42:43], 0, v[134:135]
	s_mov_b32 m0, s49
	s_nop 0
	global_load_lds_dwordx4 v[224:225], off
	s_waitcnt vmcnt(8)
	s_waitcnt lgkmcnt(0)
	s_barrier
	s_setprio 1
	s_waitcnt lgkmcnt(0)
	s_nop 0
	v_mfma_f32_16x16x32_bf16 v[126:129], v[146:149], v[186:189], v[126:129]
	v_mfma_f32_16x16x32_bf16 v[122:125], v[162:165], v[186:189], v[122:125]
	v_mfma_f32_16x16x32_bf16 v[110:113], v[146:149], v[194:197], v[110:113]
	v_mfma_f32_16x16x32_bf16 v[106:109], v[162:165], v[194:197], v[106:109]
	v_mfma_f32_16x16x32_bf16 v[94:97], v[146:149], v[202:205], v[94:97]
	v_mfma_f32_16x16x32_bf16 v[90:93], v[162:165], v[202:205], v[90:93]
	v_mfma_f32_16x16x32_bf16 v[78:81], v[146:149], v[210:213], v[78:81]
	v_mfma_f32_16x16x32_bf16 v[74:77], v[162:165], v[210:213], v[74:77]
	v_mfma_f32_16x16x32_bf16 v[126:129], v[158:161], v[190:193], v[126:129]
	v_mfma_f32_16x16x32_bf16 v[122:125], v[166:169], v[190:193], v[122:125]
	v_mfma_f32_16x16x32_bf16 v[110:113], v[158:161], v[198:201], v[110:113]
	v_mfma_f32_16x16x32_bf16 v[106:109], v[166:169], v[198:201], v[106:109]
	v_mfma_f32_16x16x32_bf16 v[94:97], v[158:161], v[206:209], v[94:97]
	v_mfma_f32_16x16x32_bf16 v[90:93], v[166:169], v[206:209], v[90:93]
	v_mfma_f32_16x16x32_bf16 v[78:81], v[158:161], v[214:217], v[78:81]
	v_mfma_f32_16x16x32_bf16 v[74:77], v[166:169], v[214:217], v[74:77]
	s_setprio 0
	s_setprio 1
	v_mfma_f32_16x16x32_bf16 v[118:121], v[170:173], v[186:189], v[118:121]
	v_mfma_f32_16x16x32_bf16 v[114:117], v[178:181], v[186:189], v[114:117]
	v_mfma_f32_16x16x32_bf16 v[102:105], v[170:173], v[194:197], v[102:105]
	v_mfma_f32_16x16x32_bf16 v[98:101], v[178:181], v[194:197], v[98:101]
	v_mfma_f32_16x16x32_bf16 v[86:89], v[170:173], v[202:205], v[86:89]
	v_mfma_f32_16x16x32_bf16 v[82:85], v[178:181], v[202:205], v[82:85]
	v_mfma_f32_16x16x32_bf16 v[70:73], v[170:173], v[210:213], v[70:73]
	v_mfma_f32_16x16x32_bf16 v[66:69], v[178:181], v[210:213], v[66:69]
	v_mfma_f32_16x16x32_bf16 v[118:121], v[174:177], v[190:193], v[118:121]
	v_mfma_f32_16x16x32_bf16 v[114:117], v[182:185], v[190:193], v[114:117]
	v_mfma_f32_16x16x32_bf16 v[102:105], v[174:177], v[198:201], v[102:105]
	v_mfma_f32_16x16x32_bf16 v[98:101], v[182:185], v[198:201], v[98:101]
	v_mfma_f32_16x16x32_bf16 v[86:89], v[174:177], v[206:209], v[86:89]
	v_mfma_f32_16x16x32_bf16 v[82:85], v[182:185], v[206:209], v[82:85]
	v_mfma_f32_16x16x32_bf16 v[70:73], v[174:177], v[214:217], v[70:73]
	v_mfma_f32_16x16x32_bf16 v[66:69], v[182:185], v[214:217], v[66:69]
	s_setprio 0
	s_barrier
; #define PG8_STAGE2(bufoff, gbase, v0, v1) do { \
;         __builtin_amdgcn_global_load_lds((const unsigned*)((const char*)(gbase) + (v0)), (LAS unsigned*)(lds + (bufoff) + ldsw), 16, 0, 0); \
;         __builtin_amdgcn_global_load_lds((const unsigned*)((const char*)(gbase) + (v1)), (LAS unsigned*)(lds + (bufoff) + ldsw + 8192), 16, 0, 0); } while (0)
; #define PG8_STAGE(bufoff, gbase, voff) PG8_STAGE2(bufoff, gbase, (voff)[0], (voff)[1])
; #define PG8_LDA(dst, b, h) do { _Pragma("unroll") for (int m = 0; m < 4; ++m) _Pragma("unroll") for (int k = 0; k < 2; ++k) dst[m][k] = *(const LAS bf16x8*)(lds + PG8_SA(b, h) + aoff + m * 2048 + k * 1024); } while (0)
; #define PG8_LDB(dst, b, h) do { _Pragma("unroll") for (int n = 0; n < 2; ++n) _Pragma("unroll") for (int k = 0; k < 2; ++k) dst[n][k] = *(const LAS bf16x8*)(lds + PG8_SB(b, h) + boff + n * 2048 + k * 1024); } while (0)
; #define PG8_WAIT_V(n) asm volatile("s_waitcnt vmcnt(" #n ")" ::: "memory")
; #define PG8_WAIT_L(n) asm volatile("s_waitcnt lgkmcnt(" #n ")" ::: "memory")
; #define PG8_BAR __builtin_amdgcn_s_barrier()
; #define PG8_SCHED __builtin_amdgcn_sched_barrier(0)
; template <class Epi, class Sched, bool ALIGN_EPI, bool SP2, bool GATHER>
; DI void gemm_phase(LAS unsigned char* lds, const Gemm g, const Sched& S, const Epi& E) {
;     ...
;             PG8_LDB(B0, 0, 0); PG8_LDB(B1, 0, 1); PG8_SCHED; PG8_LDA(At, 0, 0); PG8_STAGE2(PG8_SA(1, 1), a1 + hstepA, gC[1][0], gC[1][1]);
;             PG8_WAIT_V(8); PG8_WAIT_L(0); PG8_BAR; PG8_MMA(0, 0, At, B0); PG8_MMA(0, 1, At, B1); PG8_BAR; PG8_SCHED;
;             PG8_LDA(At, 0, 1); PG8_STAGE(PG8_SB(0, 0), b2, voffB); PG8_STAGE(PG8_SB(0, 1), b2 + hstep, voffB); PG8_STAGE2(PG8_SA(0, 0), a2, x00, x01);
;             PG8_WAIT_V(8); PG8_WAIT_L(0); PG8_BAR; PG8_MMA(1, 0, At, B0); PG8_MMA(1, 1, At, B1); PG8_BAR; PG8_SCHED;
;             PG8_LDB(B0, 1, 0); PG8_LDB(B1, 1, 1); PG8_SCHED; PG8_LDA(At, 1, 0); PG8_STAGE2(PG8_SA(0, 1), a2 + hstepA, x10, x11);
;             PG8_WAIT_V(8); PG8_WAIT_L(0); PG8_BAR; PG8_MMA(0, 0, At, B0); PG8_MMA(0, 1, At, B1); PG8_BAR; PG8_SCHED;
;             PG8_LDA(At, 1, 1); PG8_STAGE(PG8_SB(1, 0), b3, voffB); PG8_STAGE(PG8_SB(1, 1), b3 + hstep, voffB); PG8_STAGE2(PG8_SA(1, 0), a3, x00, x01);
;             PG8_WAIT_V(8); PG8_WAIT_L(0); PG8_BAR; PG8_MMA(1, 0, At, B0); PG8_MMA(1, 1, At, B1); PG8_BAR; PG8_SCHED;
;         }
	s_add_i32 s42, s62, s46
	v_lshl_add_u64 v[150:151], v[150:151], 0, s[12:13]
	s_mov_b32 m0, s42
	ds_read_b128 v[186:189], v156 offset:49152
	ds_read_b128 v[190:193], v156 offset:50176
	ds_read_b128 v[194:197], v156 offset:51200
	ds_read_b128 v[198:201], v156 offset:52224
	ds_read_b128 v[202:205], v156 offset:53248
	ds_read_b128 v[206:209], v156 offset:54272
	ds_read_b128 v[210:213], v156 offset:55296
	ds_read_b128 v[214:217], v156 offset:56320
	global_load_lds_dwordx4 v[150:151], off
	s_add_i32 m0, s42, 0x2000
	s_add_u32 s40, s40, 0x80080
	v_lshl_add_u64 v[150:151], v[218:219], 0, s[12:13]
	s_addc_u32 s41, s41, 0
	s_add_i32 s42, s67, s46
	global_load_lds_dwordx4 v[150:151], off
	v_lshl_add_u64 v[150:151], s[40:41], 0, v[132:133]
	s_mov_b32 m0, s42
	s_nop 0
	global_load_lds_dwordx4 v[150:151], off
	v_lshl_add_u64 v[150:151], s[40:41], 0, v[136:137]
	s_add_i32 m0, s42, 0x2000
	s_nop 0
	global_load_lds_dwordx4 v[150:151], off
	v_lshl_add_u64 v[150:151], v[220:221], 0, s[12:13]
	s_mov_b32 m0, s51
	s_nop 0
	global_load_lds_dwordx4 v[150:151], off
	v_lshl_add_u64 v[150:151], v[222:223], 0, s[12:13]
	s_mov_b32 m0, s52
	s_nop 0
	global_load_lds_dwordx4 v[150:151], off
	s_waitcnt vmcnt(8)
	s_waitcnt lgkmcnt(0)
	s_barrier
	s_setprio 1
	s_waitcnt lgkmcnt(0)
	v_mfma_f32_16x16x32_bf16 v[62:65], v[146:149], v[186:189], v[62:65]
	v_mfma_f32_16x16x32_bf16 v[58:61], v[162:165], v[186:189], v[58:61]
	v_mfma_f32_16x16x32_bf16 v[46:49], v[146:149], v[194:197], v[46:49]
	v_mfma_f32_16x16x32_bf16 v[42:45], v[162:165], v[194:197], v[42:45]
	v_mfma_f32_16x16x32_bf16 v[22:25], v[146:149], v[202:205], v[22:25]
	v_mfma_f32_16x16x32_bf16 v[18:21], v[162:165], v[202:205], v[18:21]
	v_mfma_f32_16x16x32_bf16 v[6:9], v[146:149], v[210:213], v[6:9]
	v_mfma_f32_16x16x32_bf16 v[2:5], v[162:165], v[210:213], v[2:5]
	v_mfma_f32_16x16x32_bf16 v[62:65], v[158:161], v[190:193], v[62:65]
	v_mfma_f32_16x16x32_bf16 v[58:61], v[166:169], v[190:193], v[58:61]
	v_mfma_f32_16x16x32_bf16 v[46:49], v[158:161], v[198:201], v[46:49]
	v_mfma_f32_16x16x32_bf16 v[42:45], v[166:169], v[198:201], v[42:45]
	v_mfma_f32_16x16x32_bf16 v[22:25], v[158:161], v[206:209], v[22:25]
	v_mfma_f32_16x16x32_bf16 v[18:21], v[166:169], v[206:209], v[18:21]
	v_mfma_f32_16x16x32_bf16 v[6:9], v[158:161], v[214:217], v[6:9]
	v_mfma_f32_16x16x32_bf16 v[2:5], v[166:169], v[214:217], v[2:5]
	s_setprio 0
	s_setprio 1
	v_mfma_f32_16x16x32_bf16 v[54:57], v[170:173], v[186:189], v[54:57]
	v_mfma_f32_16x16x32_bf16 v[50:53], v[178:181], v[186:189], v[50:53]
	v_mfma_f32_16x16x32_bf16 v[30:33], v[170:173], v[194:197], v[30:33]
	v_mfma_f32_16x16x32_bf16 v[26:29], v[178:181], v[194:197], v[26:29]
	v_mfma_f32_16x16x32_bf16 v[34:37], v[170:173], v[202:205], v[34:37]
	v_mfma_f32_16x16x32_bf16 v[38:41], v[178:181], v[202:205], v[38:41]
	v_mfma_f32_16x16x32_bf16 v[10:13], v[170:173], v[210:213], v[10:13]
	v_mfma_f32_16x16x32_bf16 v[14:17], v[178:181], v[210:213], v[14:17]
	v_mfma_f32_16x16x32_bf16 v[54:57], v[174:177], v[190:193], v[54:57]
	v_mfma_f32_16x16x32_bf16 v[50:53], v[182:185], v[190:193], v[50:53]
	v_mfma_f32_16x16x32_bf16 v[30:33], v[174:177], v[198:201], v[30:33]
	v_mfma_f32_16x16x32_bf16 v[26:29], v[182:185], v[198:201], v[26:29]
	v_mfma_f32_16x16x32_bf16 v[34:37], v[174:177], v[206:209], v[34:37]
	v_mfma_f32_16x16x32_bf16 v[38:41], v[182:185], v[206:209], v[38:41]
	v_mfma_f32_16x16x32_bf16 v[10:13], v[174:177], v[214:217], v[10:13]
	v_mfma_f32_16x16x32_bf16 v[14:17], v[182:185], v[214:217], v[14:17]
	s_setprio 0
	s_barrier
	s_add_i32 s66, s66, 2
	s_add_u32 s36, s36, 0x100
	s_addc_u32 s37, s37, 0
	s_add_u32 s64, s64, 0x100
	s_addc_u32 s65, s65, 0
	s_cmp_gt_u32 s66, 29
	s_cbranch_scc1 .Lpeel_exit_p6
.LBB0_674:
	ds_read_b128 v[146:149], v154
	ds_read_b128 v[158:161], v154 offset:1024
	ds_read_b128 v[162:165], v154 offset:2048
	ds_read_b128 v[166:169], v154 offset:3072
	ds_read_b128 v[170:173], v155
	ds_read_b128 v[174:177], v155 offset:1024
	ds_read_b128 v[178:181], v155 offset:2048
	ds_read_b128 v[182:185], v155 offset:3072
	s_add_u32 s40, s36, 0xfff80080
	s_addc_u32 s41, s37, -1
	s_cmp_eq_u32 s66, 28
	s_cselect_b32 s43, s27, s41
	s_cselect_b32 s42, s57, s40
	s_cselect_b32 s41, s25, s65
	s_cselect_b32 s40, s63, s64
	v_lshl_add_u64 v[150:151], s[36:37], 0, v[138:139]
	s_add_i32 m0, s35, 0xc000
	ds_read_b128 v[186:189], v156
	ds_read_b128 v[190:193], v156 offset:1024
	ds_read_b128 v[194:197], v156 offset:2048
	ds_read_b128 v[198:201], v156 offset:3072
	ds_read_b128 v[202:205], v156 offset:4096
	ds_read_b128 v[206:209], v156 offset:5120
	ds_read_b128 v[210:213], v156 offset:6144
	ds_read_b128 v[214:217], v156 offset:7168
	global_load_lds_dwordx4 v[150:151], off
	v_lshl_add_u64 v[150:151], s[36:37], 0, v[140:141]
	s_add_i32 m0, s35, 0xe000
	s_nop 0
	global_load_lds_dwordx4 v[150:151], off
	s_waitcnt vmcnt(8)
	s_waitcnt lgkmcnt(0)
	s_barrier
; #define PG8_STAGE2(bufoff, gbase, v0, v1) do { \
;         __builtin_amdgcn_global_load_lds((const unsigned*)((const char*)(gbase) + (v0)), (LAS unsigned*)(lds + (bufoff) + ldsw), 16, 0, 0); \
;         __builtin_amdgcn_global_load_lds((const unsigned*)((const char*)(gbase) + (v1)), (LAS unsigned*)(lds + (bufoff) + ldsw + 8192), 16, 0, 0); } while (0)
; #define PG8_STAGE(bufoff, gbase, voff) PG8_STAGE2(bufoff, gbase, (voff)[0], (voff)[1])
; #define PG8_LDA(dst, b, h) do { _Pragma("unroll") for (int m = 0; m < 4; ++m) _Pragma("unroll") for (int k = 0; k < 2; ++k) dst[m][k] = *(const LAS bf16x8*)(lds + PG8_SA(b, h) + aoff + m * 2048 + k * 1024); } while (0)
; #define PG8_MMA(ai, bj, At, Bt) do { __builtin_amdgcn_s_setprio(1); _Pragma("unroll") for (int m = 0; m < 4; ++m) _Pragma("unroll") for (int n = 0; n < 2; ++n) _Pragma("unroll") for (int k = 0; k < 2; ++k) \
;         acc[ai][bj][m][n] = __builtin_amdgcn_mfma_f32_16x16x32_bf16(Bt[n][k], At[m][k], acc[ai][bj][m][n], 0, 0, 0); __builtin_amdgcn_s_setprio(0); } while (0)
; #define PG8_WAIT_V(n) asm volatile("s_waitcnt vmcnt(" #n ")" ::: "memory")
; #define PG8_WAIT_L(n) asm volatile("s_waitcnt lgkmcnt(" #n ")" ::: "memory")
; #define PG8_BAR __builtin_amdgcn_s_barrier()
; #define PG8_SCHED __builtin_amdgcn_sched_barrier(0)
; template <class Epi, class Sched, bool ALIGN_EPI, bool SP2, bool GATHER>
; DI void gemm_phase(LAS unsigned char* lds, const Gemm g, const Sched& S, const Epi& E) {
;     ...
;             PG8_WAIT_V(8); PG8_WAIT_L(0); PG8_BAR; PG8_MMA(0, 0, At, B0); PG8_MMA(0, 1, At, B1); PG8_BAR; PG8_SCHED;
;             PG8_LDA(At, 0, 1); PG8_STAGE(PG8_SB(0, 0), b2, voffB); PG8_STAGE(PG8_SB(0, 1), b2 + hstep, voffB); PG8_STAGE2(PG8_SA(0, 0), a2, x00, x01);
;             PG8_WAIT_V(8); PG8_WAIT_L(0); PG8_BAR; PG8_MMA(1, 0, At, B0); PG8_MMA(1, 1, At, B1); PG8_BAR; PG8_SCHED;
	s_setprio 1
	s_waitcnt lgkmcnt(0)
	s_nop 0
	v_mfma_f32_16x16x32_bf16 v[126:129], v[146:149], v[186:189], v[126:129]
	v_mfma_f32_16x16x32_bf16 v[122:125], v[162:165], v[186:189], v[122:125]
	v_mfma_f32_16x16x32_bf16 v[110:113], v[146:149], v[194:197], v[110:113]
	v_mfma_f32_16x16x32_bf16 v[106:109], v[162:165], v[194:197], v[106:109]
	v_mfma_f32_16x16x32_bf16 v[94:97], v[146:149], v[202:205], v[94:97]
	v_mfma_f32_16x16x32_bf16 v[90:93], v[162:165], v[202:205], v[90:93]
	v_mfma_f32_16x16x32_bf16 v[78:81], v[146:149], v[210:213], v[78:81]
	v_mfma_f32_16x16x32_bf16 v[74:77], v[162:165], v[210:213], v[74:77]
	v_mfma_f32_16x16x32_bf16 v[126:129], v[158:161], v[190:193], v[126:129]
	v_mfma_f32_16x16x32_bf16 v[122:125], v[166:169], v[190:193], v[122:125]
	v_mfma_f32_16x16x32_bf16 v[110:113], v[158:161], v[198:201], v[110:113]
	v_mfma_f32_16x16x32_bf16 v[106:109], v[166:169], v[198:201], v[106:109]
	v_mfma_f32_16x16x32_bf16 v[94:97], v[158:161], v[206:209], v[94:97]
	v_mfma_f32_16x16x32_bf16 v[90:93], v[166:169], v[206:209], v[90:93]
	v_mfma_f32_16x16x32_bf16 v[78:81], v[158:161], v[214:217], v[78:81]
	v_mfma_f32_16x16x32_bf16 v[74:77], v[166:169], v[214:217], v[74:77]
	s_setprio 0
	s_setprio 1
	v_mfma_f32_16x16x32_bf16 v[118:121], v[170:173], v[186:189], v[118:121]
	v_mfma_f32_16x16x32_bf16 v[114:117], v[178:181], v[186:189], v[114:117]
	v_mfma_f32_16x16x32_bf16 v[102:105], v[170:173], v[194:197], v[102:105]
	v_mfma_f32_16x16x32_bf16 v[98:101], v[178:181], v[194:197], v[98:101]
	v_mfma_f32_16x16x32_bf16 v[86:89], v[170:173], v[202:205], v[86:89]
	v_mfma_f32_16x16x32_bf16 v[82:85], v[178:181], v[202:205], v[82:85]
	v_mfma_f32_16x16x32_bf16 v[70:73], v[170:173], v[210:213], v[70:73]
	v_mfma_f32_16x16x32_bf16 v[66:69], v[178:181], v[210:213], v[66:69]
	v_mfma_f32_16x16x32_bf16 v[118:121], v[174:177], v[190:193], v[118:121]
	v_mfma_f32_16x16x32_bf16 v[114:117], v[182:185], v[190:193], v[114:117]
	v_mfma_f32_16x16x32_bf16 v[102:105], v[174:177], v[198:201], v[102:105]
	v_mfma_f32_16x16x32_bf16 v[98:101], v[182:185], v[198:201], v[98:101]
	v_mfma_f32_16x16x32_bf16 v[86:89], v[174:177], v[206:209], v[86:89]
	v_mfma_f32_16x16x32_bf16 v[82:85], v[182:185], v[206:209], v[82:85]
	v_mfma_f32_16x16x32_bf16 v[70:73], v[174:177], v[214:217], v[70:73]
	v_mfma_f32_16x16x32_bf16 v[66:69], v[182:185], v[214:217], v[66:69]
	s_setprio 0
	s_barrier
	s_add_i32 s62, s54, s46
	v_lshl_add_u64 v[150:151], s[40:41], 0, v[132:133]
	s_mov_b32 m0, s62
	ds_read_b128 v[186:189], v156 offset:16384
	ds_read_b128 v[190:193], v156 offset:17408
	ds_read_b128 v[194:197], v156 offset:18432
	ds_read_b128 v[198:201], v156 offset:19456
	ds_read_b128 v[202:205], v156 offset:20480
	ds_read_b128 v[206:209], v156 offset:21504
	ds_read_b128 v[210:213], v156 offset:22528
	ds_read_b128 v[214:217], v156 offset:23552
	global_load_lds_dwordx4 v[150:151], off
	s_add_i32 m0, s62, 0x2000
	s_add_u32 s68, s40, 0x80000
	v_lshl_add_u64 v[218:219], s[40:41], 0, v[136:137]
	s_addc_u32 s69, s41, 0
	s_add_i32 s62, s55, s46
	global_load_lds_dwordx4 v[218:219], off
	v_lshl_add_u64 v[220:221], s[68:69], 0, v[132:133]
	s_mov_b32 m0, s62
	v_lshl_add_u64 v[222:223], s[42:43], 0, v[134:135]
	global_load_lds_dwordx4 v[220:221], off
	v_lshl_add_u64 v[220:221], s[68:69], 0, v[136:137]
	s_add_i32 m0, s62, 0x2000
	s_nop 0
	global_load_lds_dwordx4 v[220:221], off
	v_lshl_add_u64 v[220:221], s[42:43], 0, v[130:131]
	s_mov_b32 m0, s35
	s_nop 0
	global_load_lds_dwordx4 v[220:221], off
	s_mov_b32 m0, s47
	s_nop 0
	global_load_lds_dwordx4 v[222:223], off
	s_waitcnt vmcnt(8)
	s_waitcnt lgkmcnt(0)
	s_barrier
	s_setprio 1
	s_waitcnt lgkmcnt(0)
	s_nop 0
	v_mfma_f32_16x16x32_bf16 v[62:65], v[146:149], v[186:189], v[62:65]
	v_mfma_f32_16x16x32_bf16 v[58:61], v[162:165], v[186:189], v[58:61]
	v_mfma_f32_16x16x32_bf16 v[46:49], v[146:149], v[194:197], v[46:49]
	v_mfma_f32_16x16x32_bf16 v[42:45], v[162:165], v[194:197], v[42:45]
	v_mfma_f32_16x16x32_bf16 v[22:25], v[146:149], v[202:205], v[22:25]
	v_mfma_f32_16x16x32_bf16 v[18:21], v[162:165], v[202:205], v[18:21]
	v_mfma_f32_16x16x32_bf16 v[6:9], v[146:149], v[210:213], v[6:9]
	v_mfma_f32_16x16x32_bf16 v[2:5], v[162:165], v[210:213], v[2:5]
	v_mfma_f32_16x16x32_bf16 v[62:65], v[158:161], v[190:193], v[62:65]
	v_mfma_f32_16x16x32_bf16 v[58:61], v[166:169], v[190:193], v[58:61]
	v_mfma_f32_16x16x32_bf16 v[46:49], v[158:161], v[198:201], v[46:49]
	v_mfma_f32_16x16x32_bf16 v[42:45], v[166:169], v[198:201], v[42:45]
	v_mfma_f32_16x16x32_bf16 v[22:25], v[158:161], v[206:209], v[22:25]
	v_mfma_f32_16x16x32_bf16 v[18:21], v[166:169], v[206:209], v[18:21]
	v_mfma_f32_16x16x32_bf16 v[6:9], v[158:161], v[214:217], v[6:9]
	v_mfma_f32_16x16x32_bf16 v[2:5], v[166:169], v[214:217], v[2:5]
	s_setprio 0
	s_setprio 1
	v_mfma_f32_16x16x32_bf16 v[54:57], v[170:173], v[186:189], v[54:57]
	v_mfma_f32_16x16x32_bf16 v[50:53], v[178:181], v[186:189], v[50:53]
	v_mfma_f32_16x16x32_bf16 v[30:33], v[170:173], v[194:197], v[30:33]
	v_mfma_f32_16x16x32_bf16 v[26:29], v[178:181], v[194:197], v[26:29]
	v_mfma_f32_16x16x32_bf16 v[34:37], v[170:173], v[202:205], v[34:37]
	v_mfma_f32_16x16x32_bf16 v[38:41], v[178:181], v[202:205], v[38:41]
	v_mfma_f32_16x16x32_bf16 v[10:13], v[170:173], v[210:213], v[10:13]
	v_mfma_f32_16x16x32_bf16 v[14:17], v[178:181], v[210:213], v[14:17]
	v_mfma_f32_16x16x32_bf16 v[54:57], v[174:177], v[190:193], v[54:57]
	v_mfma_f32_16x16x32_bf16 v[50:53], v[182:185], v[190:193], v[50:53]
	v_mfma_f32_16x16x32_bf16 v[30:33], v[174:177], v[198:201], v[30:33]
	v_mfma_f32_16x16x32_bf16 v[26:29], v[182:185], v[198:201], v[26:29]
	v_mfma_f32_16x16x32_bf16 v[34:37], v[174:177], v[206:209], v[34:37]
	v_mfma_f32_16x16x32_bf16 v[38:41], v[182:185], v[206:209], v[38:41]
	v_mfma_f32_16x16x32_bf16 v[10:13], v[174:177], v[214:217], v[10:13]
	v_mfma_f32_16x16x32_bf16 v[14:17], v[182:185], v[214:217], v[14:17]
	s_setprio 0
	s_barrier
; #define PG8_STAGE2(bufoff, gbase, v0, v1) do { \
;         __builtin_amdgcn_global_load_lds((const unsigned*)((const char*)(gbase) + (v0)), (LAS unsigned*)(lds + (bufoff) + ldsw), 16, 0, 0); \
;         __builtin_amdgcn_global_load_lds((const unsigned*)((const char*)(gbase) + (v1)), (LAS unsigned*)(lds + (bufoff) + ldsw + 8192), 16, 0, 0); } while (0)
; #define PG8_LDA(dst, b, h) do { _Pragma("unroll") for (int m = 0; m < 4; ++m) _Pragma("unroll") for (int k = 0; k < 2; ++k) dst[m][k] = *(const LAS bf16x8*)(lds + PG8_SA(b, h) + aoff + m * 2048 + k * 1024); } while (0)
; #define PG8_LDB(dst, b, h) do { _Pragma("unroll") for (int n = 0; n < 2; ++n) _Pragma("unroll") for (int k = 0; k < 2; ++k) dst[n][k] = *(const LAS bf16x8*)(lds + PG8_SB(b, h) + boff + n * 2048 + k * 1024); } while (0)
; #define PG8_MMA(ai, bj, At, Bt) do { __builtin_amdgcn_s_setprio(1); _Pragma("unroll") for (int m = 0; m < 4; ++m) _Pragma("unroll") for (int n = 0; n < 2; ++n) _Pragma("unroll") for (int k = 0; k < 2; ++k) \
;         acc[ai][bj][m][n] = __builtin_amdgcn_mfma_f32_16x16x32_bf16(Bt[n][k], At[m][k], acc[ai][bj][m][n], 0, 0, 0); __builtin_amdgcn_s_setprio(0); } while (0)
; #define PG8_WAIT_V(n) asm volatile("s_waitcnt vmcnt(" #n ")" ::: "memory")
; #define PG8_WAIT_L(n) asm volatile("s_waitcnt lgkmcnt(" #n ")" ::: "memory")
; #define PG8_BAR __builtin_amdgcn_s_barrier()
; #define PG8_SCHED __builtin_amdgcn_sched_barrier(0)
; template <class Epi, class Sched, bool ALIGN_EPI, bool SP2, bool GATHER>
; DI void gemm_phase(LAS unsigned char* lds, const Gemm g, const Sched& S, const Epi& E) {
;     ...
;             PG8_LDB(B0, 1, 0); PG8_LDB(B1, 1, 1); PG8_SCHED; PG8_LDA(At, 1, 0); PG8_STAGE2(PG8_SA(0, 1), a2 + hstepA, x10, x11);
;             PG8_WAIT_V(8); PG8_WAIT_L(0); PG8_BAR; PG8_MMA(0, 0, At, B0); PG8_MMA(0, 1, At, B1); PG8_BAR; PG8_SCHED;
	s_add_i32 s62, 0, 0x18000
	v_add_u32_e32 v157, s62, v152
	s_add_i32 s67, 0, 0x1c000
	ds_read_b128 v[146:149], v157
	ds_read_b128 v[158:161], v157 offset:1024
	ds_read_b128 v[162:165], v157 offset:2048
	ds_read_b128 v[166:169], v157 offset:3072
	v_add_u32_e32 v157, s67, v152
	ds_read_b128 v[170:173], v157
	ds_read_b128 v[174:177], v157 offset:1024
	ds_read_b128 v[178:181], v157 offset:2048
	ds_read_b128 v[182:185], v157 offset:3072
	s_add_u32 s42, s42, 0x80000
	s_addc_u32 s43, s43, 0
	s_mov_b32 m0, s48
	v_lshl_add_u64 v[224:225], s[42:43], 0, v[130:131]
	ds_read_b128 v[186:189], v156 offset:32768
	ds_read_b128 v[190:193], v156 offset:33792
	ds_read_b128 v[194:197], v156 offset:34816
	ds_read_b128 v[198:201], v156 offset:35840
	ds_read_b128 v[202:205], v156 offset:36864
	ds_read_b128 v[206:209], v156 offset:37888
	ds_read_b128 v[210:213], v156 offset:38912
	ds_read_b128 v[214:217], v156 offset:39936
	global_load_lds_dwordx4 v[224:225], off
	v_lshl_add_u64 v[224:225], s[42:43], 0, v[134:135]
	s_mov_b32 m0, s49
	s_nop 0
	global_load_lds_dwordx4 v[224:225], off
	s_waitcnt vmcnt(8)
	s_waitcnt lgkmcnt(0)
	s_barrier
	s_setprio 1
	s_waitcnt lgkmcnt(0)
	s_nop 0
	v_mfma_f32_16x16x32_bf16 v[126:129], v[146:149], v[186:189], v[126:129]
	v_mfma_f32_16x16x32_bf16 v[122:125], v[162:165], v[186:189], v[122:125]
	v_mfma_f32_16x16x32_bf16 v[110:113], v[146:149], v[194:197], v[110:113]
	v_mfma_f32_16x16x32_bf16 v[106:109], v[162:165], v[194:197], v[106:109]
	v_mfma_f32_16x16x32_bf16 v[94:97], v[146:149], v[202:205], v[94:97]
	v_mfma_f32_16x16x32_bf16 v[90:93], v[162:165], v[202:205], v[90:93]
	v_mfma_f32_16x16x32_bf16 v[78:81], v[146:149], v[210:213], v[78:81]
	v_mfma_f32_16x16x32_bf16 v[74:77], v[162:165], v[210:213], v[74:77]
	v_mfma_f32_16x16x32_bf16 v[126:129], v[158:161], v[190:193], v[126:129]
	v_mfma_f32_16x16x32_bf16 v[122:125], v[166:169], v[190:193], v[122:125]
	v_mfma_f32_16x16x32_bf16 v[110:113], v[158:161], v[198:201], v[110:113]
	v_mfma_f32_16x16x32_bf16 v[106:109], v[166:169], v[198:201], v[106:109]
	v_mfma_f32_16x16x32_bf16 v[94:97], v[158:161], v[206:209], v[94:97]
	v_mfma_f32_16x16x32_bf16 v[90:93], v[166:169], v[206:209], v[90:93]
	v_mfma_f32_16x16x32_bf16 v[78:81], v[158:161], v[214:217], v[78:81]
	v_mfma_f32_16x16x32_bf16 v[74:77], v[166:169], v[214:217], v[74:77]
	s_setprio 0
	s_setprio 1
	v_mfma_f32_16x16x32_bf16 v[118:121], v[170:173], v[186:189], v[118:121]
	v_mfma_f32_16x16x32_bf16 v[114:117], v[178:181], v[186:189], v[114:117]
	v_mfma_f32_16x16x32_bf16 v[102:105], v[170:173], v[194:197], v[102:105]
	v_mfma_f32_16x16x32_bf16 v[98:101], v[178:181], v[194:197], v[98:101]
	v_mfma_f32_16x16x32_bf16 v[86:89], v[170:173], v[202:205], v[86:89]
	v_mfma_f32_16x16x32_bf16 v[82:85], v[178:181], v[202:205], v[82:85]
	v_mfma_f32_16x16x32_bf16 v[70:73], v[170:173], v[210:213], v[70:73]
	v_mfma_f32_16x16x32_bf16 v[66:69], v[178:181], v[210:213], v[66:69]
	v_mfma_f32_16x16x32_bf16 v[118:121], v[174:177], v[190:193], v[118:121]
	v_mfma_f32_16x16x32_bf16 v[114:117], v[182:185], v[190:193], v[114:117]
	v_mfma_f32_16x16x32_bf16 v[102:105], v[174:177], v[198:201], v[102:105]
	v_mfma_f32_16x16x32_bf16 v[98:101], v[182:185], v[198:201], v[98:101]
	v_mfma_f32_16x16x32_bf16 v[86:89], v[174:177], v[206:209], v[86:89]
	v_mfma_f32_16x16x32_bf16 v[82:85], v[182:185], v[206:209], v[82:85]
	v_mfma_f32_16x16x32_bf16 v[70:73], v[174:177], v[214:217], v[70:73]
	v_mfma_f32_16x16x32_bf16 v[66:69], v[182:185], v[214:217], v[66:69]
	s_setprio 0
	s_barrier
; #define PG8_STAGE2(bufoff, gbase, v0, v1) do { \
;         __builtin_amdgcn_global_load_lds((const unsigned*)((const char*)(gbase) + (v0)), (LAS unsigned*)(lds + (bufoff) + ldsw), 16, 0, 0); \
;         __builtin_amdgcn_global_load_lds((const unsigned*)((const char*)(gbase) + (v1)), (LAS unsigned*)(lds + (bufoff) + ldsw + 8192), 16, 0, 0); } while (0)
; #define PG8_STAGE(bufoff, gbase, voff) PG8_STAGE2(bufoff, gbase, (voff)[0], (voff)[1])
; #define PG8_LDA(dst, b, h) do { _Pragma("unroll") for (int m = 0; m < 4; ++m) _Pragma("unroll") for (int k = 0; k < 2; ++k) dst[m][k] = *(const LAS bf16x8*)(lds + PG8_SA(b, h) + aoff + m * 2048 + k * 1024); } while (0)
; #define PG8_MMA(ai, bj, At, Bt) do { __builtin_amdgcn_s_setprio(1); _Pragma("unroll") for (int m = 0; m < 4; ++m) _Pragma("unroll") for (int n = 0; n < 2; ++n) _Pragma("unroll") for (int k = 0; k < 2; ++k) \
;         acc[ai][bj][m][n] = __builtin_amdgcn_mfma_f32_16x16x32_bf16(Bt[n][k], At[m][k], acc[ai][bj][m][n], 0, 0, 0); __builtin_amdgcn_s_setprio(0); } while (0)
; #define PG8_WAIT_V(n) asm volatile("s_waitcnt vmcnt(" #n ")" ::: "memory")
; #define PG8_WAIT_L(n) asm volatile("s_waitcnt lgkmcnt(" #n ")" ::: "memory")
; #define PG8_BAR __builtin_amdgcn_s_barrier()
; #define PG8_SCHED __builtin_amdgcn_sched_barrier(0)
; template <class Epi, class Sched, bool ALIGN_EPI, bool SP2, bool GATHER>
; DI void gemm_phase(LAS unsigned char* lds, const Gemm g, const Sched& S, const Epi& E) {
;     ...
;             PG8_LDA(At, 1, 1); PG8_STAGE(PG8_SB(1, 0), b3, voffB); PG8_STAGE(PG8_SB(1, 1), b3 + hstep, voffB); PG8_STAGE2(PG8_SA(1, 0), a3, x00, x01);
;             PG8_WAIT_V(8); PG8_WAIT_L(0); PG8_BAR; PG8_MMA(1, 0, At, B0); PG8_MMA(1, 1, At, B1); PG8_BAR; PG8_SCHED;
;         }
	s_add_i32 s42, s62, s46
	v_lshl_add_u64 v[150:151], v[150:151], 0, s[12:13]
	s_mov_b32 m0, s42
	ds_read_b128 v[186:189], v156 offset:49152
	ds_read_b128 v[190:193], v156 offset:50176
	ds_read_b128 v[194:197], v156 offset:51200
	ds_read_b128 v[198:201], v156 offset:52224
	ds_read_b128 v[202:205], v156 offset:53248
	ds_read_b128 v[206:209], v156 offset:54272
	ds_read_b128 v[210:213], v156 offset:55296
	ds_read_b128 v[214:217], v156 offset:56320
	global_load_lds_dwordx4 v[150:151], off
	s_add_i32 m0, s42, 0x2000
	s_add_u32 s40, s40, 0x80080
	v_lshl_add_u64 v[150:151], v[218:219], 0, s[12:13]
	s_addc_u32 s41, s41, 0
	s_add_i32 s42, s67, s46
	global_load_lds_dwordx4 v[150:151], off
	v_lshl_add_u64 v[150:151], s[40:41], 0, v[132:133]
	s_mov_b32 m0, s42
	s_nop 0
	global_load_lds_dwordx4 v[150:151], off
	v_lshl_add_u64 v[150:151], s[40:41], 0, v[136:137]
	s_add_i32 m0, s42, 0x2000
	s_nop 0
	global_load_lds_dwordx4 v[150:151], off
	v_lshl_add_u64 v[150:151], v[220:221], 0, s[12:13]
	s_mov_b32 m0, s51
	s_nop 0
	global_load_lds_dwordx4 v[150:151], off
	v_lshl_add_u64 v[150:151], v[222:223], 0, s[12:13]
	s_mov_b32 m0, s52
	s_nop 0
	global_load_lds_dwordx4 v[150:151], off
	s_waitcnt vmcnt(8)
	s_waitcnt lgkmcnt(0)
	s_barrier
	s_setprio 1
	s_waitcnt lgkmcnt(0)
	v_mfma_f32_16x16x32_bf16 v[62:65], v[146:149], v[186:189], v[62:65]
	v_mfma_f32_16x16x32_bf16 v[58:61], v[162:165], v[186:189], v[58:61]
	v_mfma_f32_16x16x32_bf16 v[46:49], v[146:149], v[194:197], v[46:49]
	v_mfma_f32_16x16x32_bf16 v[42:45], v[162:165], v[194:197], v[42:45]
	v_mfma_f32_16x16x32_bf16 v[22:25], v[146:149], v[202:205], v[22:25]
	v_mfma_f32_16x16x32_bf16 v[18:21], v[162:165], v[202:205], v[18:21]
	v_mfma_f32_16x16x32_bf16 v[6:9], v[146:149], v[210:213], v[6:9]
	v_mfma_f32_16x16x32_bf16 v[2:5], v[162:165], v[210:213], v[2:5]
	v_mfma_f32_16x16x32_bf16 v[62:65], v[158:161], v[190:193], v[62:65]
	v_mfma_f32_16x16x32_bf16 v[58:61], v[166:169], v[190:193], v[58:61]
	v_mfma_f32_16x16x32_bf16 v[46:49], v[158:161], v[198:201], v[46:49]
	v_mfma_f32_16x16x32_bf16 v[42:45], v[166:169], v[198:201], v[42:45]
	v_mfma_f32_16x16x32_bf16 v[22:25], v[158:161], v[206:209], v[22:25]
	v_mfma_f32_16x16x32_bf16 v[18:21], v[166:169], v[206:209], v[18:21]
	v_mfma_f32_16x16x32_bf16 v[6:9], v[158:161], v[214:217], v[6:9]
	v_mfma_f32_16x16x32_bf16 v[2:5], v[166:169], v[214:217], v[2:5]
	s_setprio 0
	s_setprio 1
	v_mfma_f32_16x16x32_bf16 v[54:57], v[170:173], v[186:189], v[54:57]
	v_mfma_f32_16x16x32_bf16 v[50:53], v[178:181], v[186:189], v[50:53]
	v_mfma_f32_16x16x32_bf16 v[30:33], v[170:173], v[194:197], v[30:33]
	v_mfma_f32_16x16x32_bf16 v[26:29], v[178:181], v[194:197], v[26:29]
	v_mfma_f32_16x16x32_bf16 v[34:37], v[170:173], v[202:205], v[34:37]
	v_mfma_f32_16x16x32_bf16 v[38:41], v[178:181], v[202:205], v[38:41]
	v_mfma_f32_16x16x32_bf16 v[10:13], v[170:173], v[210:213], v[10:13]
	v_mfma_f32_16x16x32_bf16 v[14:17], v[178:181], v[210:213], v[14:17]
	v_mfma_f32_16x16x32_bf16 v[54:57], v[174:177], v[190:193], v[54:57]
	v_mfma_f32_16x16x32_bf16 v[50:53], v[182:185], v[190:193], v[50:53]
	v_mfma_f32_16x16x32_bf16 v[30:33], v[174:177], v[198:201], v[30:33]
	v_mfma_f32_16x16x32_bf16 v[26:29], v[182:185], v[198:201], v[26:29]
	v_mfma_f32_16x16x32_bf16 v[34:37], v[174:177], v[206:209], v[34:37]
	v_mfma_f32_16x16x32_bf16 v[38:41], v[182:185], v[206:209], v[38:41]
	v_mfma_f32_16x16x32_bf16 v[10:13], v[174:177], v[214:217], v[10:13]
	v_mfma_f32_16x16x32_bf16 v[14:17], v[182:185], v[214:217], v[14:17]
	s_setprio 0
	s_barrier
	s_add_i32 s66, s66, 2
	s_add_u32 s36, s36, 0x100
	s_addc_u32 s37, s37, 0
	s_add_u32 s64, s64, 0x100
	s_addc_u32 s65, s65, 0
	s_cmp_gt_u32 s66, 29
	s_cbranch_scc0 .LBB0_674

; #define PG8_STAGE2(bufoff, gbase, v0, v1) do { \
;         __builtin_amdgcn_global_load_lds((const unsigned*)((const char*)(gbase) + (v0)), (LAS unsigned*)(lds + (bufoff) + ldsw), 16, 0, 0); \
;         __builtin_amdgcn_global_load_lds((const unsigned*)((const char*)(gbase) + (v1)), (LAS unsigned*)(lds + (bufoff) + ldsw + 8192), 16, 0, 0); } while (0)
; #define PG8_STAGE(bufoff, gbase, voff) PG8_STAGE2(bufoff, gbase, (voff)[0], (voff)[1])
; #define PG8_LDA(dst, b, h) do { _Pragma("unroll") for (int m = 0; m < 4; ++m) _Pragma("unroll") for (int k = 0; k < 2; ++k) dst[m][k] = *(const LAS bf16x8*)(lds + PG8_SA(b, h) + aoff + m * 2048 + k * 1024); } while (0)
; #define PG8_LDB(dst, b, h) do { _Pragma("unroll") for (int n = 0; n < 2; ++n) _Pragma("unroll") for (int k = 0; k < 2; ++k) dst[n][k] = *(const LAS bf16x8*)(lds + PG8_SB(b, h) + boff + n * 2048 + k * 1024); } while (0)
; #define PG8_WAIT_V(n) asm volatile("s_waitcnt vmcnt(" #n ")" ::: "memory")
; #define PG8_WAIT_L(n) asm volatile("s_waitcnt lgkmcnt(" #n ")" ::: "memory")
; #define PG8_BAR __builtin_amdgcn_s_barrier()
; #define PG8_SCHED __builtin_amdgcn_sched_barrier(0)
; template <class Epi, class Sched, bool ALIGN_EPI, bool SP2, bool GATHER>
; DI void gemm_phase(LAS unsigned char* lds, const Gemm g, const Sched& S, const Epi& E) {
;     ...
;             const bool last = (t == nt - 2);
;             const char* a1 = cA + (size_t)(t + 1) * kstep;
;             const char* a2 = last ? nA : cA + (size_t)(t + 2) * kstep; const char* b2 = last ? nB : cB + (size_t)(t + 2) * kstep;
;             const char* a3 = a2 + kstep; const char* b3 = b2 + kstep;
;             unsigned x00 = gC[0][0], x01 = gC[0][1], x10 = gC[1][0], x11 = gC[1][1];
;             if constexpr (GATHER) { if (last) { x00 = gN[0][0]; x01 = gN[0][1]; x10 = gN[1][0]; x11 = gN[1][1]; } }
;             PG8_LDB(B0, 0, 0); PG8_LDB(B1, 0, 1); PG8_SCHED; PG8_LDA(At, 0, 0); PG8_STAGE2(PG8_SA(1, 1), a1 + hstepA, gC[1][0], gC[1][1]);
;             PG8_WAIT_V(8); PG8_WAIT_L(0); PG8_BAR; PG8_MMA(0, 0, At, B0); PG8_MMA(0, 1, At, B1); PG8_BAR; PG8_SCHED;
;             PG8_LDA(At, 0, 1); PG8_STAGE(PG8_SB(0, 0), b2, voffB); PG8_STAGE(PG8_SB(0, 1), b2 + hstep, voffB); PG8_STAGE2(PG8_SA(0, 0), a2, x00, x01);
;             PG8_WAIT_V(8); PG8_WAIT_L(0); PG8_BAR; PG8_MMA(1, 0, At, B0); PG8_MMA(1, 1, At, B1); PG8_BAR; PG8_SCHED;
.LBB0_905:
	v_add_u32_e32 v151, s53, v155
	ds_read_b128 v[160:163], v151
	ds_read_b128 v[164:167], v151 offset:1024
	ds_read_b128 v[168:171], v151 offset:2048
	ds_read_b128 v[172:175], v151 offset:3072
	v_add_u32_e32 v151, s54, v155
	ds_read_b128 v[176:179], v151
	ds_read_b128 v[180:183], v151 offset:1024
	ds_read_b128 v[184:187], v151 offset:2048
	ds_read_b128 v[188:191], v151 offset:3072
	s_add_u32 s42, s36, 0x80
	s_addc_u32 s43, s37, 0
	s_and_b64 s[40:41], s[40:41], exec
	s_cselect_b32 s43, s5, s43
	s_cselect_b32 s42, s4, s42
	s_cselect_b32 s41, s29, s66
	s_cselect_b32 s40, s64, s65
	v_lshl_add_u64 v[224:225], s[36:37], 0, v[140:141]
	s_add_i32 m0, s35, 0xc000
	ds_read_b128 v[192:195], v157
	ds_read_b128 v[196:199], v157 offset:1024
	ds_read_b128 v[200:203], v157 offset:2048
	ds_read_b128 v[204:207], v157 offset:3072
	ds_read_b128 v[208:211], v157 offset:4096
	ds_read_b128 v[212:215], v157 offset:5120
	ds_read_b128 v[216:219], v157 offset:6144
	ds_read_b128 v[220:223], v157 offset:7168
	global_load_lds_dwordx4 v[224:225], off
	v_lshl_add_u64 v[224:225], s[36:37], 0, v[144:145]
	s_add_i32 m0, s35, 0xe000
	s_nop 0
	global_load_lds_dwordx4 v[224:225], off
	s_waitcnt vmcnt(8)
	s_waitcnt lgkmcnt(0)
	s_barrier
	s_setprio 1
	s_waitcnt lgkmcnt(0)
	v_mfma_f32_16x16x32_bf16 v[122:125], v[160:163], v[192:195], v[122:125]
	v_mfma_f32_16x16x32_bf16 v[126:129], v[168:171], v[192:195], v[126:129]
	v_mfma_f32_16x16x32_bf16 v[106:109], v[160:163], v[200:203], v[106:109]
	v_mfma_f32_16x16x32_bf16 v[110:113], v[168:171], v[200:203], v[110:113]
	v_mfma_f32_16x16x32_bf16 v[90:93], v[160:163], v[208:211], v[90:93]
	v_mfma_f32_16x16x32_bf16 v[94:97], v[168:171], v[208:211], v[94:97]
	v_mfma_f32_16x16x32_bf16 v[74:77], v[160:163], v[216:219], v[74:77]
	v_mfma_f32_16x16x32_bf16 v[78:81], v[168:171], v[216:219], v[78:81]
	v_mfma_f32_16x16x32_bf16 v[122:125], v[164:167], v[196:199], v[122:125]
	v_mfma_f32_16x16x32_bf16 v[126:129], v[172:175], v[196:199], v[126:129]
	v_mfma_f32_16x16x32_bf16 v[106:109], v[164:167], v[204:207], v[106:109]
	v_mfma_f32_16x16x32_bf16 v[110:113], v[172:175], v[204:207], v[110:113]
	v_mfma_f32_16x16x32_bf16 v[90:93], v[164:167], v[212:215], v[90:93]
	v_mfma_f32_16x16x32_bf16 v[94:97], v[172:175], v[212:215], v[94:97]
	v_mfma_f32_16x16x32_bf16 v[74:77], v[164:167], v[220:223], v[74:77]
	v_mfma_f32_16x16x32_bf16 v[78:81], v[172:175], v[220:223], v[78:81]
	s_setprio 0
	s_setprio 1
	v_mfma_f32_16x16x32_bf16 v[114:117], v[176:179], v[192:195], v[114:117]
	v_mfma_f32_16x16x32_bf16 v[118:121], v[184:187], v[192:195], v[118:121]
	v_mfma_f32_16x16x32_bf16 v[98:101], v[176:179], v[200:203], v[98:101]
	v_mfma_f32_16x16x32_bf16 v[102:105], v[184:187], v[200:203], v[102:105]
	v_mfma_f32_16x16x32_bf16 v[82:85], v[176:179], v[208:211], v[82:85]
	v_mfma_f32_16x16x32_bf16 v[86:89], v[184:187], v[208:211], v[86:89]
	v_mfma_f32_16x16x32_bf16 v[66:69], v[176:179], v[216:219], v[66:69]
	v_mfma_f32_16x16x32_bf16 v[70:73], v[184:187], v[216:219], v[70:73]
	v_mfma_f32_16x16x32_bf16 v[114:117], v[180:183], v[196:199], v[114:117]
	v_mfma_f32_16x16x32_bf16 v[118:121], v[188:191], v[196:199], v[118:121]
	v_mfma_f32_16x16x32_bf16 v[98:101], v[180:183], v[204:207], v[98:101]
	v_mfma_f32_16x16x32_bf16 v[102:105], v[188:191], v[204:207], v[102:105]
	v_mfma_f32_16x16x32_bf16 v[82:85], v[180:183], v[212:215], v[82:85]
	v_mfma_f32_16x16x32_bf16 v[86:89], v[188:191], v[212:215], v[86:89]
	v_mfma_f32_16x16x32_bf16 v[66:69], v[180:183], v[220:223], v[66:69]
	v_mfma_f32_16x16x32_bf16 v[70:73], v[188:191], v[220:223], v[70:73]
	s_setprio 0
	s_barrier
	s_add_i32 s68, s53, s45
	v_lshl_add_u64 v[224:225], s[40:41], 0, v[132:133]
	s_mov_b32 m0, s68
	ds_read_b128 v[192:195], v157 offset:16384
	ds_read_b128 v[196:199], v157 offset:17408
	ds_read_b128 v[200:203], v157 offset:18432
	ds_read_b128 v[204:207], v157 offset:19456
	ds_read_b128 v[208:211], v157 offset:20480
	ds_read_b128 v[212:215], v157 offset:21504
	ds_read_b128 v[216:219], v157 offset:22528
	ds_read_b128 v[220:223], v157 offset:23552
	global_load_lds_dwordx4 v[224:225], off
	s_add_i32 m0, s68, 0x2000
	s_add_u32 s68, s40, 0x80000
	v_lshl_add_u64 v[226:227], s[40:41], 0, v[130:131]
	s_addc_u32 s69, s41, 0
	s_add_i32 s70, s54, s45
	global_load_lds_dwordx4 v[226:227], off
	v_lshl_add_u64 v[228:229], s[68:69], 0, v[132:133]
	s_mov_b32 m0, s70
	v_mov_b32_e32 v151, v135
	global_load_lds_dwordx4 v[228:229], off
	v_lshl_add_u64 v[228:229], s[68:69], 0, v[130:131]
	s_add_i32 m0, s70, 0x2000
	s_nop 0
	global_load_lds_dwordx4 v[228:229], off
	s_mov_b32 m0, s35
	v_lshl_add_u64 v[228:229], s[42:43], 0, v[134:135]
	global_load_lds_dwordx4 v134, s[42:43]
	s_mov_b32 m0, s46
	s_nop 0
	global_load_lds_dwordx4 v150, s[42:43]
	s_waitcnt vmcnt(8)
	s_waitcnt lgkmcnt(0)
	v_lshl_add_u64 v[150:151], s[42:43], 0, v[150:151]
	s_barrier
; #define PG8_STAGE2(bufoff, gbase, v0, v1) do { \
;         __builtin_amdgcn_global_load_lds((const unsigned*)((const char*)(gbase) + (v0)), (LAS unsigned*)(lds + (bufoff) + ldsw), 16, 0, 0); \
;         __builtin_amdgcn_global_load_lds((const unsigned*)((const char*)(gbase) + (v1)), (LAS unsigned*)(lds + (bufoff) + ldsw + 8192), 16, 0, 0); } while (0)
; #define PG8_STAGE(bufoff, gbase, voff) PG8_STAGE2(bufoff, gbase, (voff)[0], (voff)[1])
; #define PG8_LDA(dst, b, h) do { _Pragma("unroll") for (int m = 0; m < 4; ++m) _Pragma("unroll") for (int k = 0; k < 2; ++k) dst[m][k] = *(const LAS bf16x8*)(lds + PG8_SA(b, h) + aoff + m * 2048 + k * 1024); } while (0)
; #define PG8_LDB(dst, b, h) do { _Pragma("unroll") for (int n = 0; n < 2; ++n) _Pragma("unroll") for (int k = 0; k < 2; ++k) dst[n][k] = *(const LAS bf16x8*)(lds + PG8_SB(b, h) + boff + n * 2048 + k * 1024); } while (0)
; #define PG8_WAIT_V(n) asm volatile("s_waitcnt vmcnt(" #n ")" ::: "memory")
; #define PG8_WAIT_L(n) asm volatile("s_waitcnt lgkmcnt(" #n ")" ::: "memory")
; #define PG8_BAR __builtin_amdgcn_s_barrier()
; #define PG8_SCHED __builtin_amdgcn_sched_barrier(0)
; template <class Epi, class Sched, bool ALIGN_EPI, bool SP2, bool GATHER>
; DI void gemm_phase(LAS unsigned char* lds, const Gemm g, const Sched& S, const Epi& E) {
;     ...
;             PG8_LDB(B0, 0, 0); PG8_LDB(B1, 0, 1); PG8_SCHED; PG8_LDA(At, 0, 0); PG8_STAGE2(PG8_SA(1, 1), a1 + hstepA, gC[1][0], gC[1][1]);
;             PG8_WAIT_V(8); PG8_WAIT_L(0); PG8_BAR; PG8_MMA(0, 0, At, B0); PG8_MMA(0, 1, At, B1); PG8_BAR; PG8_SCHED;
;             PG8_LDA(At, 0, 1); PG8_STAGE(PG8_SB(0, 0), b2, voffB); PG8_STAGE(PG8_SB(0, 1), b2 + hstep, voffB); PG8_STAGE2(PG8_SA(0, 0), a2, x00, x01);
;             PG8_WAIT_V(8); PG8_WAIT_L(0); PG8_BAR; PG8_MMA(1, 0, At, B0); PG8_MMA(1, 1, At, B1); PG8_BAR; PG8_SCHED;
;             PG8_LDB(B0, 1, 0); PG8_LDB(B1, 1, 1); PG8_SCHED; PG8_LDA(At, 1, 0); PG8_STAGE2(PG8_SA(0, 1), a2 + hstepA, x10, x11);
;             PG8_WAIT_V(8); PG8_WAIT_L(0); PG8_BAR; PG8_MMA(0, 0, At, B0); PG8_MMA(0, 1, At, B1); PG8_BAR; PG8_SCHED;
;             PG8_LDA(At, 1, 1); PG8_STAGE(PG8_SB(1, 0), b3, voffB); PG8_STAGE(PG8_SB(1, 1), b3 + hstep, voffB); PG8_STAGE2(PG8_SA(1, 0), a3, x00, x01);
;             PG8_WAIT_V(8); PG8_WAIT_L(0); PG8_BAR; PG8_MMA(1, 0, At, B0); PG8_MMA(1, 1, At, B1); PG8_BAR; PG8_SCHED;
	s_setprio 1
	s_waitcnt lgkmcnt(0)
	s_nop 0
	v_mfma_f32_16x16x32_bf16 v[58:61], v[160:163], v[192:195], v[58:61]
	v_mfma_f32_16x16x32_bf16 v[62:65], v[168:171], v[192:195], v[62:65]
	v_mfma_f32_16x16x32_bf16 v[42:45], v[160:163], v[200:203], v[42:45]
	v_mfma_f32_16x16x32_bf16 v[46:49], v[168:171], v[200:203], v[46:49]
	v_mfma_f32_16x16x32_bf16 v[26:29], v[160:163], v[208:211], v[26:29]
	v_mfma_f32_16x16x32_bf16 v[30:33], v[168:171], v[208:211], v[30:33]
	v_mfma_f32_16x16x32_bf16 v[10:13], v[160:163], v[216:219], v[10:13]
	v_mfma_f32_16x16x32_bf16 v[14:17], v[168:171], v[216:219], v[14:17]
	v_mfma_f32_16x16x32_bf16 v[58:61], v[164:167], v[196:199], v[58:61]
	v_mfma_f32_16x16x32_bf16 v[62:65], v[172:175], v[196:199], v[62:65]
	v_mfma_f32_16x16x32_bf16 v[42:45], v[164:167], v[204:207], v[42:45]
	v_mfma_f32_16x16x32_bf16 v[46:49], v[172:175], v[204:207], v[46:49]
	v_mfma_f32_16x16x32_bf16 v[26:29], v[164:167], v[212:215], v[26:29]
	v_mfma_f32_16x16x32_bf16 v[30:33], v[172:175], v[212:215], v[30:33]
	v_mfma_f32_16x16x32_bf16 v[10:13], v[164:167], v[220:223], v[10:13]
	v_mfma_f32_16x16x32_bf16 v[14:17], v[172:175], v[220:223], v[14:17]
	s_setprio 0
	s_setprio 1
	v_mfma_f32_16x16x32_bf16 v[50:53], v[176:179], v[192:195], v[50:53]
	v_mfma_f32_16x16x32_bf16 v[54:57], v[184:187], v[192:195], v[54:57]
	v_mfma_f32_16x16x32_bf16 v[34:37], v[176:179], v[200:203], v[34:37]
	v_mfma_f32_16x16x32_bf16 v[38:41], v[184:187], v[200:203], v[38:41]
	v_mfma_f32_16x16x32_bf16 v[18:21], v[176:179], v[208:211], v[18:21]
	v_mfma_f32_16x16x32_bf16 v[22:25], v[184:187], v[208:211], v[22:25]
	v_mfma_f32_16x16x32_bf16 v[2:5], v[176:179], v[216:219], v[2:5]
	v_mfma_f32_16x16x32_bf16 v[6:9], v[184:187], v[216:219], v[6:9]
	v_mfma_f32_16x16x32_bf16 v[50:53], v[180:183], v[196:199], v[50:53]
	v_mfma_f32_16x16x32_bf16 v[54:57], v[188:191], v[196:199], v[54:57]
	v_mfma_f32_16x16x32_bf16 v[34:37], v[180:183], v[204:207], v[34:37]
	v_mfma_f32_16x16x32_bf16 v[38:41], v[188:191], v[204:207], v[38:41]
	v_mfma_f32_16x16x32_bf16 v[18:21], v[180:183], v[212:215], v[18:21]
	v_mfma_f32_16x16x32_bf16 v[22:25], v[188:191], v[212:215], v[22:25]
	v_mfma_f32_16x16x32_bf16 v[2:5], v[180:183], v[220:223], v[2:5]
	v_mfma_f32_16x16x32_bf16 v[6:9], v[188:191], v[220:223], v[6:9]
	s_setprio 0
	s_barrier
	s_add_i32 s68, 0, 0x18000
	v_add_u32_e32 v134, s68, v155
	s_add_i32 s69, 0, 0x1c000
	ds_read_b128 v[160:163], v134
	ds_read_b128 v[164:167], v134 offset:1024
	ds_read_b128 v[168:171], v134 offset:2048
	ds_read_b128 v[172:175], v134 offset:3072
	v_add_u32_e32 v134, s69, v155
	ds_read_b128 v[176:179], v134
	ds_read_b128 v[180:183], v134 offset:1024
	ds_read_b128 v[184:187], v134 offset:2048
	ds_read_b128 v[188:191], v134 offset:3072
	s_mov_b32 m0, s47
	v_lshl_add_u64 v[148:149], s[42:43], 0, v[148:149]
	ds_read_b128 v[192:195], v157 offset:32768
	ds_read_b128 v[196:199], v157 offset:33792
	ds_read_b128 v[200:203], v157 offset:34816
	ds_read_b128 v[204:207], v157 offset:35840
	ds_read_b128 v[208:211], v157 offset:36864
	ds_read_b128 v[212:215], v157 offset:37888
	ds_read_b128 v[216:219], v157 offset:38912
	ds_read_b128 v[220:223], v157 offset:39936
	global_load_lds_dwordx4 v[148:149], off
	v_lshl_add_u64 v[146:147], s[42:43], 0, v[146:147]
	s_mov_b32 m0, s48
	s_nop 0
	global_load_lds_dwordx4 v[146:147], off
	s_waitcnt vmcnt(8)
	s_waitcnt lgkmcnt(0)
	s_barrier
	s_setprio 1
	s_waitcnt lgkmcnt(0)
	v_mfma_f32_16x16x32_bf16 v[122:125], v[160:163], v[192:195], v[122:125]
	v_mfma_f32_16x16x32_bf16 v[126:129], v[168:171], v[192:195], v[126:129]
	v_mfma_f32_16x16x32_bf16 v[106:109], v[160:163], v[200:203], v[106:109]
	v_mfma_f32_16x16x32_bf16 v[110:113], v[168:171], v[200:203], v[110:113]
	v_mfma_f32_16x16x32_bf16 v[90:93], v[160:163], v[208:211], v[90:93]
	v_mfma_f32_16x16x32_bf16 v[94:97], v[168:171], v[208:211], v[94:97]
	v_mfma_f32_16x16x32_bf16 v[74:77], v[160:163], v[216:219], v[74:77]
	v_mfma_f32_16x16x32_bf16 v[78:81], v[168:171], v[216:219], v[78:81]
	v_mfma_f32_16x16x32_bf16 v[122:125], v[164:167], v[196:199], v[122:125]
	v_mfma_f32_16x16x32_bf16 v[126:129], v[172:175], v[196:199], v[126:129]
	v_mfma_f32_16x16x32_bf16 v[106:109], v[164:167], v[204:207], v[106:109]
	v_mfma_f32_16x16x32_bf16 v[110:113], v[172:175], v[204:207], v[110:113]
	v_mfma_f32_16x16x32_bf16 v[90:93], v[164:167], v[212:215], v[90:93]
	v_mfma_f32_16x16x32_bf16 v[94:97], v[172:175], v[212:215], v[94:97]
	v_mfma_f32_16x16x32_bf16 v[74:77], v[164:167], v[220:223], v[74:77]
	v_mfma_f32_16x16x32_bf16 v[78:81], v[172:175], v[220:223], v[78:81]
	s_setprio 0
	s_setprio 1
	v_mfma_f32_16x16x32_bf16 v[114:117], v[176:179], v[192:195], v[114:117]
	v_mfma_f32_16x16x32_bf16 v[118:121], v[184:187], v[192:195], v[118:121]
	v_mfma_f32_16x16x32_bf16 v[98:101], v[176:179], v[200:203], v[98:101]
	v_mfma_f32_16x16x32_bf16 v[102:105], v[184:187], v[200:203], v[102:105]
	v_mfma_f32_16x16x32_bf16 v[82:85], v[176:179], v[208:211], v[82:85]
	v_mfma_f32_16x16x32_bf16 v[86:89], v[184:187], v[208:211], v[86:89]
	v_mfma_f32_16x16x32_bf16 v[66:69], v[176:179], v[216:219], v[66:69]
	v_mfma_f32_16x16x32_bf16 v[70:73], v[184:187], v[216:219], v[70:73]
	v_mfma_f32_16x16x32_bf16 v[114:117], v[180:183], v[196:199], v[114:117]
	v_mfma_f32_16x16x32_bf16 v[118:121], v[188:191], v[196:199], v[118:121]
	v_mfma_f32_16x16x32_bf16 v[98:101], v[180:183], v[204:207], v[98:101]
	v_mfma_f32_16x16x32_bf16 v[102:105], v[188:191], v[204:207], v[102:105]
	v_mfma_f32_16x16x32_bf16 v[82:85], v[180:183], v[212:215], v[82:85]
	v_mfma_f32_16x16x32_bf16 v[86:89], v[188:191], v[212:215], v[86:89]
	v_mfma_f32_16x16x32_bf16 v[66:69], v[180:183], v[220:223], v[66:69]
	v_mfma_f32_16x16x32_bf16 v[70:73], v[188:191], v[220:223], v[70:73]
	s_setprio 0
	s_barrier
; #define PG8_STAGE2(bufoff, gbase, v0, v1) do { \
;         __builtin_amdgcn_global_load_lds((const unsigned*)((const char*)(gbase) + (v0)), (LAS unsigned*)(lds + (bufoff) + ldsw), 16, 0, 0); \
;         __builtin_amdgcn_global_load_lds((const unsigned*)((const char*)(gbase) + (v1)), (LAS unsigned*)(lds + (bufoff) + ldsw + 8192), 16, 0, 0); } while (0)
; #define PG8_STAGE(bufoff, gbase, voff) PG8_STAGE2(bufoff, gbase, (voff)[0], (voff)[1])
; #define PG8_LDA(dst, b, h) do { _Pragma("unroll") for (int m = 0; m < 4; ++m) _Pragma("unroll") for (int k = 0; k < 2; ++k) dst[m][k] = *(const LAS bf16x8*)(lds + PG8_SA(b, h) + aoff + m * 2048 + k * 1024); } while (0)
; #define PG8_MMA(ai, bj, At, Bt) do { __builtin_amdgcn_s_setprio(1); _Pragma("unroll") for (int m = 0; m < 4; ++m) _Pragma("unroll") for (int n = 0; n < 2; ++n) _Pragma("unroll") for (int k = 0; k < 2; ++k) \
;         acc[ai][bj][m][n] = __builtin_amdgcn_mfma_f32_16x16x32_bf16(Bt[n][k], At[m][k], acc[ai][bj][m][n], 0, 0, 0); __builtin_amdgcn_s_setprio(0); } while (0)
; #define PG8_WAIT_V(n) asm volatile("s_waitcnt vmcnt(" #n ")" ::: "memory")
; #define PG8_WAIT_L(n) asm volatile("s_waitcnt lgkmcnt(" #n ")" ::: "memory")
; #define PG8_BAR __builtin_amdgcn_s_barrier()
; #define PG8_SCHED __builtin_amdgcn_sched_barrier(0)
; template <class Epi, class Sched, bool ALIGN_EPI, bool SP2, bool GATHER>
; DI void gemm_phase(LAS unsigned char* lds, const Gemm g, const Sched& S, const Epi& E) {
;     ...
;             PG8_LDA(At, 1, 1); PG8_STAGE(PG8_SB(1, 0), b3, voffB); PG8_STAGE(PG8_SB(1, 1), b3 + hstep, voffB); PG8_STAGE2(PG8_SA(1, 0), a3, x00, x01);
;             PG8_WAIT_V(8); PG8_WAIT_L(0); PG8_BAR; PG8_MMA(1, 0, At, B0); PG8_MMA(1, 1, At, B1); PG8_BAR; PG8_SCHED;
;         }
	s_add_i32 s42, s68, s45
	v_lshl_add_u64 v[220:221], v[224:225], 0, s[14:15]
	s_mov_b32 m0, s42
	ds_read_b128 v[146:149], v157 offset:49152
	ds_read_b128 v[192:195], v157 offset:50176
	ds_read_b128 v[196:199], v157 offset:51200
	ds_read_b128 v[200:203], v157 offset:52224
	ds_read_b128 v[204:207], v157 offset:53248
	ds_read_b128 v[208:211], v157 offset:54272
	ds_read_b128 v[212:215], v157 offset:55296
	ds_read_b128 v[216:219], v157 offset:56320
	global_load_lds_dwordx4 v[220:221], off
	s_add_i32 m0, s42, 0x2000
	s_add_u32 s40, s40, 0x80080
	v_lshl_add_u64 v[220:221], v[226:227], 0, s[14:15]
	s_addc_u32 s41, s41, 0
	s_add_i32 s42, s69, s45
	global_load_lds_dwordx4 v[220:221], off
	v_lshl_add_u64 v[220:221], s[40:41], 0, v[132:133]
	s_mov_b32 m0, s42
	v_lshl_add_u64 v[150:151], v[150:151], 0, s[14:15]
	global_load_lds_dwordx4 v[220:221], off
	v_lshl_add_u64 v[220:221], s[40:41], 0, v[130:131]
	s_add_i32 m0, s42, 0x2000
	s_nop 0
	global_load_lds_dwordx4 v[220:221], off
	v_lshl_add_u64 v[220:221], v[228:229], 0, s[14:15]
	s_mov_b32 m0, s50
	s_nop 0
	global_load_lds_dwordx4 v[220:221], off
	s_mov_b32 m0, s51
	s_nop 0
	global_load_lds_dwordx4 v[150:151], off
	s_waitcnt vmcnt(8)
	s_waitcnt lgkmcnt(0)
	s_barrier
	s_setprio 1
	s_waitcnt lgkmcnt(0)
	s_nop 0
	v_mfma_f32_16x16x32_bf16 v[58:61], v[160:163], v[146:149], v[58:61]
	v_mfma_f32_16x16x32_bf16 v[62:65], v[168:171], v[146:149], v[62:65]
	v_mfma_f32_16x16x32_bf16 v[42:45], v[160:163], v[196:199], v[42:45]
	v_mfma_f32_16x16x32_bf16 v[46:49], v[168:171], v[196:199], v[46:49]
	v_mfma_f32_16x16x32_bf16 v[26:29], v[160:163], v[204:207], v[26:29]
	v_mfma_f32_16x16x32_bf16 v[30:33], v[168:171], v[204:207], v[30:33]
	v_mfma_f32_16x16x32_bf16 v[10:13], v[160:163], v[212:215], v[10:13]
	v_mfma_f32_16x16x32_bf16 v[14:17], v[168:171], v[212:215], v[14:17]
	v_mfma_f32_16x16x32_bf16 v[58:61], v[164:167], v[192:195], v[58:61]
	v_mfma_f32_16x16x32_bf16 v[62:65], v[172:175], v[192:195], v[62:65]
	v_mfma_f32_16x16x32_bf16 v[42:45], v[164:167], v[200:203], v[42:45]
	v_mfma_f32_16x16x32_bf16 v[46:49], v[172:175], v[200:203], v[46:49]
	v_mfma_f32_16x16x32_bf16 v[26:29], v[164:167], v[208:211], v[26:29]
	v_mfma_f32_16x16x32_bf16 v[30:33], v[172:175], v[208:211], v[30:33]
	v_mfma_f32_16x16x32_bf16 v[10:13], v[164:167], v[216:219], v[10:13]
	v_mfma_f32_16x16x32_bf16 v[14:17], v[172:175], v[216:219], v[14:17]
	s_setprio 0
	s_setprio 1
	v_mfma_f32_16x16x32_bf16 v[50:53], v[176:179], v[146:149], v[50:53]
	v_mfma_f32_16x16x32_bf16 v[54:57], v[184:187], v[146:149], v[54:57]
	v_mfma_f32_16x16x32_bf16 v[34:37], v[176:179], v[196:199], v[34:37]
	v_mfma_f32_16x16x32_bf16 v[38:41], v[184:187], v[196:199], v[38:41]
	v_mfma_f32_16x16x32_bf16 v[18:21], v[176:179], v[204:207], v[18:21]
	v_mfma_f32_16x16x32_bf16 v[22:25], v[184:187], v[204:207], v[22:25]
	v_mfma_f32_16x16x32_bf16 v[2:5], v[176:179], v[212:215], v[2:5]
	v_mfma_f32_16x16x32_bf16 v[6:9], v[184:187], v[212:215], v[6:9]
	v_mfma_f32_16x16x32_bf16 v[50:53], v[180:183], v[192:195], v[50:53]
	v_mfma_f32_16x16x32_bf16 v[54:57], v[188:191], v[192:195], v[54:57]
	v_mfma_f32_16x16x32_bf16 v[34:37], v[180:183], v[200:203], v[34:37]
	v_mfma_f32_16x16x32_bf16 v[38:41], v[188:191], v[200:203], v[38:41]
	v_mfma_f32_16x16x32_bf16 v[18:21], v[180:183], v[208:211], v[18:21]
	v_mfma_f32_16x16x32_bf16 v[22:25], v[188:191], v[208:211], v[22:25]
	v_mfma_f32_16x16x32_bf16 v[2:5], v[180:183], v[216:219], v[2:5]
	v_mfma_f32_16x16x32_bf16 v[6:9], v[188:191], v[216:219], v[6:9]
	s_setprio 0
	s_barrier
	s_add_i32 s67, s67, 2
	s_add_u32 s36, s36, 0x100
	s_addc_u32 s37, s37, 0
	s_add_u32 s65, s65, 0x100
	s_addc_u32 s66, s66, 0
	s_cmp_gt_u32 s67, 29
	s_cbranch_scc1 .LBB0_908

; #define PG8_STAGE2(bufoff, gbase, v0, v1) do { \
;         __builtin_amdgcn_global_load_lds((const unsigned*)((const char*)(gbase) + (v0)), (LAS unsigned*)(lds + (bufoff) + ldsw), 16, 0, 0); \
;         __builtin_amdgcn_global_load_lds((const unsigned*)((const char*)(gbase) + (v1)), (LAS unsigned*)(lds + (bufoff) + ldsw + 8192), 16, 0, 0); } while (0)
; #define PG8_STAGE(bufoff, gbase, voff) PG8_STAGE2(bufoff, gbase, (voff)[0], (voff)[1])
; #define PG8_WAIT_V(n) asm volatile("s_waitcnt vmcnt(" #n ")" ::: "memory")
; #define PG8_WAIT_L(n) asm volatile("s_waitcnt lgkmcnt(" #n ")" ::: "memory")
; template <class Epi, class Sched, bool ALIGN_EPI, bool SP2, bool GATHER>
; DI void gemm_phase(LAS unsigned char* lds, const Gemm g, const Sched& S, const Epi& E) {
;     ...
;         const bool has_next = S.next(ui + 1, nxt);
;         const char* nA = (has_next && !GATHER) ? (const char*)g.A + (size_t)nxt.pm * tstep : cA; const char* nB = has_next ? (const char*)g.Bt + (size_t)nxt.pn * tstep : cB;
;         if constexpr (GATHER) { if (has_next) { PG8_GATHER(nxt, gN); } else {
; #pragma unroll
;             for (int h = 0; h < 2; ++h) { gN[h][0] = gC[h][0]; gN[h][1] = gC[h][1]; } } }
;         for (int t = 0; t < nt; t += 2) {
;             if constexpr (Epi::MID_T >= 0) { if (t == Epi::MID_T) { E.mid(acc, cur, wr, wc, fr, fq); PG8_SCHED; } }
;             const bool last = (t == nt - 2);
;             const char* a1 = cA + (size_t)(t + 1) * kstep;
;             const char* a2 = last ? nA : cA + (size_t)(t + 2) * kstep; const char* b2 = last ? nB : cB + (size_t)(t + 2) * kstep;
;             const char* a3 = a2 + kstep; const char* b3 = b2 + kstep;
;             unsigned x00 = gC[0][0], x01 = gC[0][1], x10 = gC[1][0], x11 = gC[1][1];
;             if constexpr (GATHER) { if (last) { x00 = gN[0][0]; x01 = gN[0][1]; x10 = gN[1][0]; x11 = gN[1][1]; } }
;             PG8_LDB(B0, 0, 0); PG8_LDB(B1, 0, 1); PG8_SCHED; PG8_LDA(At, 0, 0); PG8_STAGE2(PG8_SA(1, 1), a1 + hstepA, gC[1][0], gC[1][1]);
;             PG8_WAIT_V(8); PG8_WAIT_L(0); PG8_BAR; PG8_MMA(0, 0, At, B0); PG8_MMA(0, 1, At, B1); PG8_BAR; PG8_SCHED;
;             PG8_LDA(At, 0, 1); PG8_STAGE(PG8_SB(0, 0), b2, voffB); PG8_STAGE(PG8_SB(0, 1), b2 + hstep, voffB); PG8_STAGE2(PG8_SA(0, 0), a2, x00, x01);
;             PG8_WAIT_V(8); PG8_WAIT_L(0); PG8_BAR; PG8_MMA(1, 0, At, B0); PG8_MMA(1, 1, At, B1); PG8_BAR; PG8_SCHED;
.LBB0_995:
	s_ashr_i32 s15, s14, 31
	s_lshl_b64 s[20:21], s[14:15], 18
	s_add_u32 s20, s37, s20
	s_addc_u32 s21, s38, s21
	s_and_b64 s[22:23], s[18:19], exec
	s_cselect_b32 s15, s21, s29
	s_cselect_b32 s25, s20, s28
	s_ashr_i32 s17, s16, 31
	s_lshl_b64 s[22:23], s[16:17], 18
	s_add_u32 s22, s39, s22
	s_addc_u32 s23, s40, s23
	s_and_b64 s[34:35], s[18:19], exec
	s_cselect_b32 s17, s23, s31
	s_cselect_b32 s50, s22, s30
	s_add_u32 s28, s28, 0x20080
	s_addc_u32 s29, s29, 0
	s_add_u32 s51, s30, 0x100
	s_addc_u32 s52, s31, 0
	s_mov_b32 s53, -2
	ds_read_b128 v[144:147], v154
	ds_read_b128 v[148:151], v154 offset:1024
	ds_read_b128 v[158:161], v154 offset:2048
	ds_read_b128 v[162:165], v154 offset:3072
	ds_read_b128 v[166:169], v155
	ds_read_b128 v[170:173], v155 offset:1024
	ds_read_b128 v[174:177], v155 offset:2048
	ds_read_b128 v[178:181], v155 offset:3072
	s_add_u32 s30, s28, 0xfffe0080
	s_addc_u32 s31, s29, -1
	s_cmp_eq_u32 s53, 4
	s_cselect_b32 s35, s15, s31
	s_cselect_b32 s34, s25, s30
	s_cselect_b32 s31, s17, s52
	s_cselect_b32 s30, s50, s51
	v_lshl_add_u64 v[214:215], s[28:29], 0, v[140:141]
	s_add_i32 m0, s27, 0xc000
	ds_read_b128 v[182:185], v156
	ds_read_b128 v[186:189], v156 offset:1024
	ds_read_b128 v[190:193], v156 offset:2048
	ds_read_b128 v[194:197], v156 offset:3072
	ds_read_b128 v[198:201], v156 offset:4096
	ds_read_b128 v[202:205], v156 offset:5120
	ds_read_b128 v[206:209], v156 offset:6144
	ds_read_b128 v[210:213], v156 offset:7168
	global_load_lds_dwordx4 v[214:215], off
	v_lshl_add_u64 v[214:215], s[28:29], 0, v[142:143]
	s_add_i32 m0, s27, 0xe000
	s_nop 0
	global_load_lds_dwordx4 v[214:215], off
	s_waitcnt vmcnt(8)
	s_waitcnt lgkmcnt(0)
	s_barrier
	s_setprio 1
	s_waitcnt lgkmcnt(0)
	v_mfma_f32_16x16x32_bf16 v[126:129], v[144:147], v[182:185], 0
	v_mfma_f32_16x16x32_bf16 v[122:125], v[158:161], v[182:185], 0
	v_mfma_f32_16x16x32_bf16 v[110:113], v[144:147], v[190:193], 0
	v_mfma_f32_16x16x32_bf16 v[106:109], v[158:161], v[190:193], 0
	v_mfma_f32_16x16x32_bf16 v[94:97], v[144:147], v[198:201], 0
	v_mfma_f32_16x16x32_bf16 v[90:93], v[158:161], v[198:201], 0
	v_mfma_f32_16x16x32_bf16 v[78:81], v[144:147], v[206:209], 0
	v_mfma_f32_16x16x32_bf16 v[74:77], v[158:161], v[206:209], 0
	v_mfma_f32_16x16x32_bf16 v[126:129], v[148:151], v[186:189], v[126:129]
	v_mfma_f32_16x16x32_bf16 v[122:125], v[162:165], v[186:189], v[122:125]
	v_mfma_f32_16x16x32_bf16 v[110:113], v[148:151], v[194:197], v[110:113]
	v_mfma_f32_16x16x32_bf16 v[106:109], v[162:165], v[194:197], v[106:109]
	v_mfma_f32_16x16x32_bf16 v[94:97], v[148:151], v[202:205], v[94:97]
	v_mfma_f32_16x16x32_bf16 v[90:93], v[162:165], v[202:205], v[90:93]
	v_mfma_f32_16x16x32_bf16 v[78:81], v[148:151], v[210:213], v[78:81]
	v_mfma_f32_16x16x32_bf16 v[74:77], v[162:165], v[210:213], v[74:77]
	s_setprio 0
	s_setprio 1
	v_mfma_f32_16x16x32_bf16 v[118:121], v[166:169], v[182:185], 0
	v_mfma_f32_16x16x32_bf16 v[114:117], v[174:177], v[182:185], 0
	v_mfma_f32_16x16x32_bf16 v[102:105], v[166:169], v[190:193], 0
	v_mfma_f32_16x16x32_bf16 v[98:101], v[174:177], v[190:193], 0
	v_mfma_f32_16x16x32_bf16 v[86:89], v[166:169], v[198:201], 0
	v_mfma_f32_16x16x32_bf16 v[82:85], v[174:177], v[198:201], 0
	v_mfma_f32_16x16x32_bf16 v[70:73], v[166:169], v[206:209], 0
	v_mfma_f32_16x16x32_bf16 v[66:69], v[174:177], v[206:209], 0
	v_mfma_f32_16x16x32_bf16 v[118:121], v[170:173], v[186:189], v[118:121]
	v_mfma_f32_16x16x32_bf16 v[114:117], v[178:181], v[186:189], v[114:117]
	v_mfma_f32_16x16x32_bf16 v[102:105], v[170:173], v[194:197], v[102:105]
	v_mfma_f32_16x16x32_bf16 v[98:101], v[178:181], v[194:197], v[98:101]
	v_mfma_f32_16x16x32_bf16 v[86:89], v[170:173], v[202:205], v[86:89]
	v_mfma_f32_16x16x32_bf16 v[82:85], v[178:181], v[202:205], v[82:85]
	v_mfma_f32_16x16x32_bf16 v[70:73], v[170:173], v[210:213], v[70:73]
	v_mfma_f32_16x16x32_bf16 v[66:69], v[178:181], v[210:213], v[66:69]
	s_setprio 0
	s_barrier
	s_add_i32 s54, s48, s41
	v_lshl_add_u64 v[214:215], s[30:31], 0, v[132:133]
	s_mov_b32 m0, s54
	ds_read_b128 v[182:185], v156 offset:16384
	ds_read_b128 v[186:189], v156 offset:17408
	ds_read_b128 v[190:193], v156 offset:18432
	ds_read_b128 v[194:197], v156 offset:19456
	ds_read_b128 v[198:201], v156 offset:20480
	ds_read_b128 v[202:205], v156 offset:21504
	ds_read_b128 v[206:209], v156 offset:22528
	ds_read_b128 v[210:213], v156 offset:23552
	global_load_lds_dwordx4 v[214:215], off
	s_add_i32 m0, s54, 0x2000
	s_add_u32 s54, s30, 0x20000
	v_lshl_add_u64 v[216:217], s[30:31], 0, v[136:137]
	s_addc_u32 s55, s31, 0
	s_add_i32 s56, s49, s41
	global_load_lds_dwordx4 v[216:217], off
	v_lshl_add_u64 v[218:219], s[54:55], 0, v[132:133]
	s_mov_b32 m0, s56
	v_lshl_add_u64 v[220:221], s[34:35], 0, v[134:135]
	global_load_lds_dwordx4 v[218:219], off
	v_lshl_add_u64 v[218:219], s[54:55], 0, v[136:137]
	s_add_i32 m0, s56, 0x2000
	s_nop 0
	global_load_lds_dwordx4 v[218:219], off
	v_lshl_add_u64 v[218:219], s[34:35], 0, v[130:131]
	s_mov_b32 m0, s27
	s_nop 0
	global_load_lds_dwordx4 v[218:219], off
	s_mov_b32 m0, s42
	s_nop 0
	global_load_lds_dwordx4 v[220:221], off
	s_waitcnt vmcnt(8)
	s_waitcnt lgkmcnt(0)
	s_barrier
; #define PG8_STAGE2(bufoff, gbase, v0, v1) do { \
;         __builtin_amdgcn_global_load_lds((const unsigned*)((const char*)(gbase) + (v0)), (LAS unsigned*)(lds + (bufoff) + ldsw), 16, 0, 0); \
;         __builtin_amdgcn_global_load_lds((const unsigned*)((const char*)(gbase) + (v1)), (LAS unsigned*)(lds + (bufoff) + ldsw + 8192), 16, 0, 0); } while (0)
; #define PG8_LDA(dst, b, h) do { _Pragma("unroll") for (int m = 0; m < 4; ++m) _Pragma("unroll") for (int k = 0; k < 2; ++k) dst[m][k] = *(const LAS bf16x8*)(lds + PG8_SA(b, h) + aoff + m * 2048 + k * 1024); } while (0)
; #define PG8_LDB(dst, b, h) do { _Pragma("unroll") for (int n = 0; n < 2; ++n) _Pragma("unroll") for (int k = 0; k < 2; ++k) dst[n][k] = *(const LAS bf16x8*)(lds + PG8_SB(b, h) + boff + n * 2048 + k * 1024); } while (0)
; #define PG8_MMA(ai, bj, At, Bt) do { __builtin_amdgcn_s_setprio(1); _Pragma("unroll") for (int m = 0; m < 4; ++m) _Pragma("unroll") for (int n = 0; n < 2; ++n) _Pragma("unroll") for (int k = 0; k < 2; ++k) \
;         acc[ai][bj][m][n] = __builtin_amdgcn_mfma_f32_16x16x32_bf16(Bt[n][k], At[m][k], acc[ai][bj][m][n], 0, 0, 0); __builtin_amdgcn_s_setprio(0); } while (0)
; #define PG8_WAIT_V(n) asm volatile("s_waitcnt vmcnt(" #n ")" ::: "memory")
; #define PG8_WAIT_L(n) asm volatile("s_waitcnt lgkmcnt(" #n ")" ::: "memory")
; #define PG8_BAR __builtin_amdgcn_s_barrier()
; #define PG8_SCHED __builtin_amdgcn_sched_barrier(0)
; template <class Epi, class Sched, bool ALIGN_EPI, bool SP2, bool GATHER>
; DI void gemm_phase(LAS unsigned char* lds, const Gemm g, const Sched& S, const Epi& E) {
;     ...
;             PG8_WAIT_V(8); PG8_WAIT_L(0); PG8_BAR; PG8_MMA(1, 0, At, B0); PG8_MMA(1, 1, At, B1); PG8_BAR; PG8_SCHED;
;             PG8_LDB(B0, 1, 0); PG8_LDB(B1, 1, 1); PG8_SCHED; PG8_LDA(At, 1, 0); PG8_STAGE2(PG8_SA(0, 1), a2 + hstepA, x10, x11);
;             PG8_WAIT_V(8); PG8_WAIT_L(0); PG8_BAR; PG8_MMA(0, 0, At, B0); PG8_MMA(0, 1, At, B1); PG8_BAR; PG8_SCHED;
	s_setprio 1
	s_waitcnt lgkmcnt(0)
	s_nop 0
	v_mfma_f32_16x16x32_bf16 v[62:65], v[144:147], v[182:185], 0
	v_mfma_f32_16x16x32_bf16 v[58:61], v[158:161], v[182:185], 0
	v_mfma_f32_16x16x32_bf16 v[46:49], v[144:147], v[190:193], 0
	v_mfma_f32_16x16x32_bf16 v[42:45], v[158:161], v[190:193], 0
	v_mfma_f32_16x16x32_bf16 v[14:17], v[144:147], v[198:201], 0
	v_mfma_f32_16x16x32_bf16 v[10:13], v[158:161], v[198:201], 0
	v_mfma_f32_16x16x32_bf16 v[6:9], v[144:147], v[206:209], 0
	v_mfma_f32_16x16x32_bf16 v[2:5], v[158:161], v[206:209], 0
	v_mfma_f32_16x16x32_bf16 v[62:65], v[148:151], v[186:189], v[62:65]
	v_mfma_f32_16x16x32_bf16 v[58:61], v[162:165], v[186:189], v[58:61]
	v_mfma_f32_16x16x32_bf16 v[46:49], v[148:151], v[194:197], v[46:49]
	v_mfma_f32_16x16x32_bf16 v[42:45], v[162:165], v[194:197], v[42:45]
	v_mfma_f32_16x16x32_bf16 v[14:17], v[148:151], v[202:205], v[14:17]
	v_mfma_f32_16x16x32_bf16 v[10:13], v[162:165], v[202:205], v[10:13]
	v_mfma_f32_16x16x32_bf16 v[6:9], v[148:151], v[210:213], v[6:9]
	v_mfma_f32_16x16x32_bf16 v[2:5], v[162:165], v[210:213], v[2:5]
	s_setprio 0
	s_setprio 1
	v_mfma_f32_16x16x32_bf16 v[54:57], v[166:169], v[182:185], 0
	v_mfma_f32_16x16x32_bf16 v[50:53], v[174:177], v[182:185], 0
	v_mfma_f32_16x16x32_bf16 v[30:33], v[166:169], v[190:193], 0
	v_mfma_f32_16x16x32_bf16 v[26:29], v[174:177], v[190:193], 0
	v_mfma_f32_16x16x32_bf16 v[34:37], v[166:169], v[198:201], 0
	v_mfma_f32_16x16x32_bf16 v[38:41], v[174:177], v[198:201], 0
	v_mfma_f32_16x16x32_bf16 v[18:21], v[166:169], v[206:209], 0
	v_mfma_f32_16x16x32_bf16 v[22:25], v[174:177], v[206:209], 0
	v_mfma_f32_16x16x32_bf16 v[54:57], v[170:173], v[186:189], v[54:57]
	v_mfma_f32_16x16x32_bf16 v[50:53], v[178:181], v[186:189], v[50:53]
	v_mfma_f32_16x16x32_bf16 v[30:33], v[170:173], v[194:197], v[30:33]
	v_mfma_f32_16x16x32_bf16 v[26:29], v[178:181], v[194:197], v[26:29]
	v_mfma_f32_16x16x32_bf16 v[34:37], v[170:173], v[202:205], v[34:37]
	v_mfma_f32_16x16x32_bf16 v[38:41], v[178:181], v[202:205], v[38:41]
	v_mfma_f32_16x16x32_bf16 v[18:21], v[170:173], v[210:213], v[18:21]
	v_mfma_f32_16x16x32_bf16 v[22:25], v[178:181], v[210:213], v[22:25]
	s_setprio 0
	s_barrier
	s_add_i32 s54, 0, 0x18000
	v_add_u32_e32 v138, s54, v152
	s_add_i32 s55, 0, 0x1c000
	ds_read_b128 v[144:147], v138
	ds_read_b128 v[148:151], v138 offset:1024
	ds_read_b128 v[158:161], v138 offset:2048
	ds_read_b128 v[162:165], v138 offset:3072
	v_add_u32_e32 v138, s55, v152
	ds_read_b128 v[166:169], v138
	ds_read_b128 v[170:173], v138 offset:1024
	ds_read_b128 v[174:177], v138 offset:2048
	ds_read_b128 v[178:181], v138 offset:3072
	s_add_u32 s34, s34, 0x20000
	s_addc_u32 s35, s35, 0
	s_mov_b32 m0, s43
	v_lshl_add_u64 v[222:223], s[34:35], 0, v[130:131]
	ds_read_b128 v[182:185], v156 offset:32768
	ds_read_b128 v[186:189], v156 offset:33792
	ds_read_b128 v[190:193], v156 offset:34816
	ds_read_b128 v[194:197], v156 offset:35840
	ds_read_b128 v[198:201], v156 offset:36864
	ds_read_b128 v[202:205], v156 offset:37888
	ds_read_b128 v[206:209], v156 offset:38912
	ds_read_b128 v[210:213], v156 offset:39936
	global_load_lds_dwordx4 v[222:223], off
	v_lshl_add_u64 v[222:223], s[34:35], 0, v[134:135]
	s_mov_b32 m0, s44
	s_nop 0
	global_load_lds_dwordx4 v[222:223], off
	s_waitcnt vmcnt(8)
	s_waitcnt lgkmcnt(0)
	s_barrier
	s_setprio 1
	s_waitcnt lgkmcnt(0)
	s_nop 0
	v_mfma_f32_16x16x32_bf16 v[126:129], v[144:147], v[182:185], v[126:129]
	v_mfma_f32_16x16x32_bf16 v[122:125], v[158:161], v[182:185], v[122:125]
	v_mfma_f32_16x16x32_bf16 v[110:113], v[144:147], v[190:193], v[110:113]
	v_mfma_f32_16x16x32_bf16 v[106:109], v[158:161], v[190:193], v[106:109]
	v_mfma_f32_16x16x32_bf16 v[94:97], v[144:147], v[198:201], v[94:97]
	v_mfma_f32_16x16x32_bf16 v[90:93], v[158:161], v[198:201], v[90:93]
	v_mfma_f32_16x16x32_bf16 v[78:81], v[144:147], v[206:209], v[78:81]
	v_mfma_f32_16x16x32_bf16 v[74:77], v[158:161], v[206:209], v[74:77]
	v_mfma_f32_16x16x32_bf16 v[126:129], v[148:151], v[186:189], v[126:129]
	v_mfma_f32_16x16x32_bf16 v[122:125], v[162:165], v[186:189], v[122:125]
	v_mfma_f32_16x16x32_bf16 v[110:113], v[148:151], v[194:197], v[110:113]
	v_mfma_f32_16x16x32_bf16 v[106:109], v[162:165], v[194:197], v[106:109]
	v_mfma_f32_16x16x32_bf16 v[94:97], v[148:151], v[202:205], v[94:97]
	v_mfma_f32_16x16x32_bf16 v[90:93], v[162:165], v[202:205], v[90:93]
	v_mfma_f32_16x16x32_bf16 v[78:81], v[148:151], v[210:213], v[78:81]
	v_mfma_f32_16x16x32_bf16 v[74:77], v[162:165], v[210:213], v[74:77]
	s_setprio 0
	s_setprio 1
	v_mfma_f32_16x16x32_bf16 v[118:121], v[166:169], v[182:185], v[118:121]
	v_mfma_f32_16x16x32_bf16 v[114:117], v[174:177], v[182:185], v[114:117]
	v_mfma_f32_16x16x32_bf16 v[102:105], v[166:169], v[190:193], v[102:105]
	v_mfma_f32_16x16x32_bf16 v[98:101], v[174:177], v[190:193], v[98:101]
	v_mfma_f32_16x16x32_bf16 v[86:89], v[166:169], v[198:201], v[86:89]
	v_mfma_f32_16x16x32_bf16 v[82:85], v[174:177], v[198:201], v[82:85]
	v_mfma_f32_16x16x32_bf16 v[70:73], v[166:169], v[206:209], v[70:73]
	v_mfma_f32_16x16x32_bf16 v[66:69], v[174:177], v[206:209], v[66:69]
	v_mfma_f32_16x16x32_bf16 v[118:121], v[170:173], v[186:189], v[118:121]
	v_mfma_f32_16x16x32_bf16 v[114:117], v[178:181], v[186:189], v[114:117]
	v_mfma_f32_16x16x32_bf16 v[102:105], v[170:173], v[194:197], v[102:105]
	v_mfma_f32_16x16x32_bf16 v[98:101], v[178:181], v[194:197], v[98:101]
	v_mfma_f32_16x16x32_bf16 v[86:89], v[170:173], v[202:205], v[86:89]
	v_mfma_f32_16x16x32_bf16 v[82:85], v[178:181], v[202:205], v[82:85]
	v_mfma_f32_16x16x32_bf16 v[70:73], v[170:173], v[210:213], v[70:73]
	v_mfma_f32_16x16x32_bf16 v[66:69], v[178:181], v[210:213], v[66:69]
	s_setprio 0
	s_barrier
; #define PG8_STAGE2(bufoff, gbase, v0, v1) do { \
;         __builtin_amdgcn_global_load_lds((const unsigned*)((const char*)(gbase) + (v0)), (LAS unsigned*)(lds + (bufoff) + ldsw), 16, 0, 0); \
;         __builtin_amdgcn_global_load_lds((const unsigned*)((const char*)(gbase) + (v1)), (LAS unsigned*)(lds + (bufoff) + ldsw + 8192), 16, 0, 0); } while (0)
; #define PG8_STAGE(bufoff, gbase, voff) PG8_STAGE2(bufoff, gbase, (voff)[0], (voff)[1])
; #define PG8_LDA(dst, b, h) do { _Pragma("unroll") for (int m = 0; m < 4; ++m) _Pragma("unroll") for (int k = 0; k < 2; ++k) dst[m][k] = *(const LAS bf16x8*)(lds + PG8_SA(b, h) + aoff + m * 2048 + k * 1024); } while (0)
; #define PG8_LDB(dst, b, h) do { _Pragma("unroll") for (int n = 0; n < 2; ++n) _Pragma("unroll") for (int k = 0; k < 2; ++k) dst[n][k] = *(const LAS bf16x8*)(lds + PG8_SB(b, h) + boff + n * 2048 + k * 1024); } while (0)
; #define PG8_WAIT_V(n) asm volatile("s_waitcnt vmcnt(" #n ")" ::: "memory")
; #define PG8_WAIT_L(n) asm volatile("s_waitcnt lgkmcnt(" #n ")" ::: "memory")
; #define PG8_BAR __builtin_amdgcn_s_barrier()
; #define PG8_SCHED __builtin_amdgcn_sched_barrier(0)
; template <class Epi, class Sched, bool ALIGN_EPI, bool SP2, bool GATHER>
; DI void gemm_phase(LAS unsigned char* lds, const Gemm g, const Sched& S, const Epi& E) {
;     ...
;             PG8_LDB(B0, 0, 0); PG8_LDB(B1, 0, 1); PG8_SCHED; PG8_LDA(At, 0, 0); PG8_STAGE2(PG8_SA(1, 1), a1 + hstepA, gC[1][0], gC[1][1]);
;             PG8_WAIT_V(8); PG8_WAIT_L(0); PG8_BAR; PG8_MMA(0, 0, At, B0); PG8_MMA(0, 1, At, B1); PG8_BAR; PG8_SCHED;
;             PG8_LDA(At, 0, 1); PG8_STAGE(PG8_SB(0, 0), b2, voffB); PG8_STAGE(PG8_SB(0, 1), b2 + hstep, voffB); PG8_STAGE2(PG8_SA(0, 0), a2, x00, x01);
;             PG8_WAIT_V(8); PG8_WAIT_L(0); PG8_BAR; PG8_MMA(1, 0, At, B0); PG8_MMA(1, 1, At, B1); PG8_BAR; PG8_SCHED;
;             PG8_LDB(B0, 1, 0); PG8_LDB(B1, 1, 1); PG8_SCHED; PG8_LDA(At, 1, 0); PG8_STAGE2(PG8_SA(0, 1), a2 + hstepA, x10, x11);
;             PG8_WAIT_V(8); PG8_WAIT_L(0); PG8_BAR; PG8_MMA(0, 0, At, B0); PG8_MMA(0, 1, At, B1); PG8_BAR; PG8_SCHED;
;             PG8_LDA(At, 1, 1); PG8_STAGE(PG8_SB(1, 0), b3, voffB); PG8_STAGE(PG8_SB(1, 1), b3 + hstep, voffB); PG8_STAGE2(PG8_SA(1, 0), a3, x00, x01);
;             PG8_WAIT_V(8); PG8_WAIT_L(0); PG8_BAR; PG8_MMA(1, 0, At, B0); PG8_MMA(1, 1, At, B1); PG8_BAR; PG8_SCHED;
;         }
	s_add_i32 s34, s54, s41
	v_lshl_add_u64 v[214:215], v[214:215], 0, s[10:11]
	s_mov_b32 m0, s34
	ds_read_b128 v[182:185], v156 offset:49152
	ds_read_b128 v[186:189], v156 offset:50176
	ds_read_b128 v[190:193], v156 offset:51200
	ds_read_b128 v[194:197], v156 offset:52224
	ds_read_b128 v[198:201], v156 offset:53248
	ds_read_b128 v[202:205], v156 offset:54272
	ds_read_b128 v[206:209], v156 offset:55296
	ds_read_b128 v[210:213], v156 offset:56320
	global_load_lds_dwordx4 v[214:215], off
	s_add_i32 m0, s34, 0x2000
	s_add_u32 s30, s30, 0x20080
	v_lshl_add_u64 v[214:215], v[216:217], 0, s[10:11]
	s_addc_u32 s31, s31, 0
	s_add_i32 s34, s55, s41
	global_load_lds_dwordx4 v[214:215], off
	v_lshl_add_u64 v[214:215], s[30:31], 0, v[132:133]
	s_mov_b32 m0, s34
	s_nop 0
	global_load_lds_dwordx4 v[214:215], off
	v_lshl_add_u64 v[214:215], s[30:31], 0, v[136:137]
	s_add_i32 m0, s34, 0x2000
	s_nop 0
	global_load_lds_dwordx4 v[214:215], off
	v_lshl_add_u64 v[214:215], v[218:219], 0, s[10:11]
	s_mov_b32 m0, s46
	s_nop 0
	global_load_lds_dwordx4 v[214:215], off
	v_lshl_add_u64 v[214:215], v[220:221], 0, s[10:11]
	s_mov_b32 m0, s47
	s_nop 0
	global_load_lds_dwordx4 v[214:215], off
	s_waitcnt vmcnt(8)
	s_waitcnt lgkmcnt(0)
	s_barrier
	s_setprio 1
	s_waitcnt lgkmcnt(0)
	v_mfma_f32_16x16x32_bf16 v[62:65], v[144:147], v[182:185], v[62:65]
	v_mfma_f32_16x16x32_bf16 v[58:61], v[158:161], v[182:185], v[58:61]
	v_mfma_f32_16x16x32_bf16 v[46:49], v[144:147], v[190:193], v[46:49]
	v_mfma_f32_16x16x32_bf16 v[42:45], v[158:161], v[190:193], v[42:45]
	v_mfma_f32_16x16x32_bf16 v[14:17], v[144:147], v[198:201], v[14:17]
	v_mfma_f32_16x16x32_bf16 v[10:13], v[158:161], v[198:201], v[10:13]
	v_mfma_f32_16x16x32_bf16 v[6:9], v[144:147], v[206:209], v[6:9]
	v_mfma_f32_16x16x32_bf16 v[2:5], v[158:161], v[206:209], v[2:5]
	v_mfma_f32_16x16x32_bf16 v[62:65], v[148:151], v[186:189], v[62:65]
	v_mfma_f32_16x16x32_bf16 v[58:61], v[162:165], v[186:189], v[58:61]
	v_mfma_f32_16x16x32_bf16 v[46:49], v[148:151], v[194:197], v[46:49]
	v_mfma_f32_16x16x32_bf16 v[42:45], v[162:165], v[194:197], v[42:45]
	v_mfma_f32_16x16x32_bf16 v[14:17], v[148:151], v[202:205], v[14:17]
	v_mfma_f32_16x16x32_bf16 v[10:13], v[162:165], v[202:205], v[10:13]
	v_mfma_f32_16x16x32_bf16 v[6:9], v[148:151], v[210:213], v[6:9]
	v_mfma_f32_16x16x32_bf16 v[2:5], v[162:165], v[210:213], v[2:5]
	s_setprio 0
	s_setprio 1
	v_mfma_f32_16x16x32_bf16 v[54:57], v[166:169], v[182:185], v[54:57]
	v_mfma_f32_16x16x32_bf16 v[50:53], v[174:177], v[182:185], v[50:53]
	v_mfma_f32_16x16x32_bf16 v[30:33], v[166:169], v[190:193], v[30:33]
	v_mfma_f32_16x16x32_bf16 v[26:29], v[174:177], v[190:193], v[26:29]
	v_mfma_f32_16x16x32_bf16 v[34:37], v[166:169], v[198:201], v[34:37]
	v_mfma_f32_16x16x32_bf16 v[38:41], v[174:177], v[198:201], v[38:41]
	v_mfma_f32_16x16x32_bf16 v[18:21], v[166:169], v[206:209], v[18:21]
	v_mfma_f32_16x16x32_bf16 v[22:25], v[174:177], v[206:209], v[22:25]
	v_mfma_f32_16x16x32_bf16 v[54:57], v[170:173], v[186:189], v[54:57]
	v_mfma_f32_16x16x32_bf16 v[50:53], v[178:181], v[186:189], v[50:53]
	v_mfma_f32_16x16x32_bf16 v[30:33], v[170:173], v[194:197], v[30:33]
	v_mfma_f32_16x16x32_bf16 v[26:29], v[178:181], v[194:197], v[26:29]
	v_mfma_f32_16x16x32_bf16 v[34:37], v[170:173], v[202:205], v[34:37]
	v_mfma_f32_16x16x32_bf16 v[38:41], v[178:181], v[202:205], v[38:41]
	v_mfma_f32_16x16x32_bf16 v[18:21], v[170:173], v[210:213], v[18:21]
	v_mfma_f32_16x16x32_bf16 v[22:25], v[178:181], v[210:213], v[22:25]
	s_setprio 0
	s_barrier
	s_add_i32 s53, s53, 2
	s_add_u32 s28, s28, 0x100
	s_addc_u32 s29, s29, 0
	s_add_u32 s51, s51, 0x100
	s_addc_u32 s52, s52, 0
	s_cmp_gt_u32 s53, 5
	s_cbranch_scc1 .Lpeel_exit_p10
.LBB0_996:
	ds_read_b128 v[144:147], v154
	ds_read_b128 v[148:151], v154 offset:1024
	ds_read_b128 v[158:161], v154 offset:2048
	ds_read_b128 v[162:165], v154 offset:3072
	ds_read_b128 v[166:169], v155
	ds_read_b128 v[170:173], v155 offset:1024
	ds_read_b128 v[174:177], v155 offset:2048
	ds_read_b128 v[178:181], v155 offset:3072
	s_add_u32 s30, s28, 0xfffe0080
	s_addc_u32 s31, s29, -1
	s_cmp_eq_u32 s53, 4
	s_cselect_b32 s35, s15, s31
	s_cselect_b32 s34, s25, s30
	s_cselect_b32 s31, s17, s52
	s_cselect_b32 s30, s50, s51
	v_lshl_add_u64 v[214:215], s[28:29], 0, v[140:141]
	s_add_i32 m0, s27, 0xc000
	ds_read_b128 v[182:185], v156
	ds_read_b128 v[186:189], v156 offset:1024
	ds_read_b128 v[190:193], v156 offset:2048
	ds_read_b128 v[194:197], v156 offset:3072
	ds_read_b128 v[198:201], v156 offset:4096
	ds_read_b128 v[202:205], v156 offset:5120
	ds_read_b128 v[206:209], v156 offset:6144
	ds_read_b128 v[210:213], v156 offset:7168
	global_load_lds_dwordx4 v[214:215], off
	v_lshl_add_u64 v[214:215], s[28:29], 0, v[142:143]
	s_add_i32 m0, s27, 0xe000
	s_nop 0
	global_load_lds_dwordx4 v[214:215], off
	s_waitcnt vmcnt(8)
	s_waitcnt lgkmcnt(0)
	s_barrier
; #define PG8_STAGE2(bufoff, gbase, v0, v1) do { \
;         __builtin_amdgcn_global_load_lds((const unsigned*)((const char*)(gbase) + (v0)), (LAS unsigned*)(lds + (bufoff) + ldsw), 16, 0, 0); \
;         __builtin_amdgcn_global_load_lds((const unsigned*)((const char*)(gbase) + (v1)), (LAS unsigned*)(lds + (bufoff) + ldsw + 8192), 16, 0, 0); } while (0)
; #define PG8_STAGE(bufoff, gbase, voff) PG8_STAGE2(bufoff, gbase, (voff)[0], (voff)[1])
; #define PG8_LDA(dst, b, h) do { _Pragma("unroll") for (int m = 0; m < 4; ++m) _Pragma("unroll") for (int k = 0; k < 2; ++k) dst[m][k] = *(const LAS bf16x8*)(lds + PG8_SA(b, h) + aoff + m * 2048 + k * 1024); } while (0)
; #define PG8_LDB(dst, b, h) do { _Pragma("unroll") for (int n = 0; n < 2; ++n) _Pragma("unroll") for (int k = 0; k < 2; ++k) dst[n][k] = *(const LAS bf16x8*)(lds + PG8_SB(b, h) + boff + n * 2048 + k * 1024); } while (0)
; #define PG8_MMA(ai, bj, At, Bt) do { __builtin_amdgcn_s_setprio(1); _Pragma("unroll") for (int m = 0; m < 4; ++m) _Pragma("unroll") for (int n = 0; n < 2; ++n) _Pragma("unroll") for (int k = 0; k < 2; ++k) \
;         acc[ai][bj][m][n] = __builtin_amdgcn_mfma_f32_16x16x32_bf16(Bt[n][k], At[m][k], acc[ai][bj][m][n], 0, 0, 0); __builtin_amdgcn_s_setprio(0); } while (0)
; #define PG8_WAIT_V(n) asm volatile("s_waitcnt vmcnt(" #n ")" ::: "memory")
; #define PG8_WAIT_L(n) asm volatile("s_waitcnt lgkmcnt(" #n ")" ::: "memory")
; template <class Epi, class Sched, bool ALIGN_EPI, bool SP2, bool GATHER>
; DI void gemm_phase(LAS unsigned char* lds, const Gemm g, const Sched& S, const Epi& E) {
;     ...
;             PG8_WAIT_V(8); PG8_WAIT_L(0); PG8_BAR; PG8_MMA(0, 0, At, B0); PG8_MMA(0, 1, At, B1); PG8_BAR; PG8_SCHED;
;             PG8_LDA(At, 0, 1); PG8_STAGE(PG8_SB(0, 0), b2, voffB); PG8_STAGE(PG8_SB(0, 1), b2 + hstep, voffB); PG8_STAGE2(PG8_SA(0, 0), a2, x00, x01);
;             PG8_WAIT_V(8); PG8_WAIT_L(0); PG8_BAR; PG8_MMA(1, 0, At, B0); PG8_MMA(1, 1, At, B1); PG8_BAR; PG8_SCHED;
;             PG8_LDB(B0, 1, 0); PG8_LDB(B1, 1, 1); PG8_SCHED; PG8_LDA(At, 1, 0); PG8_STAGE2(PG8_SA(0, 1), a2 + hstepA, x10, x11);
;             PG8_WAIT_V(8); PG8_WAIT_L(0); PG8_BAR; PG8_MMA(0, 0, At, B0); PG8_MMA(0, 1, At, B1); PG8_BAR; PG8_SCHED;
;             PG8_LDA(At, 1, 1); PG8_STAGE(PG8_SB(1, 0), b3, voffB); PG8_STAGE(PG8_SB(1, 1), b3 + hstep, voffB); PG8_STAGE2(PG8_SA(1, 0), a3, x00, x01);
	s_setprio 1
	s_waitcnt lgkmcnt(0)
	s_nop 0
	v_mfma_f32_16x16x32_bf16 v[126:129], v[144:147], v[182:185], v[126:129]
	v_mfma_f32_16x16x32_bf16 v[122:125], v[158:161], v[182:185], v[122:125]
	v_mfma_f32_16x16x32_bf16 v[110:113], v[144:147], v[190:193], v[110:113]
	v_mfma_f32_16x16x32_bf16 v[106:109], v[158:161], v[190:193], v[106:109]
	v_mfma_f32_16x16x32_bf16 v[94:97], v[144:147], v[198:201], v[94:97]
	v_mfma_f32_16x16x32_bf16 v[90:93], v[158:161], v[198:201], v[90:93]
	v_mfma_f32_16x16x32_bf16 v[78:81], v[144:147], v[206:209], v[78:81]
	v_mfma_f32_16x16x32_bf16 v[74:77], v[158:161], v[206:209], v[74:77]
	v_mfma_f32_16x16x32_bf16 v[126:129], v[148:151], v[186:189], v[126:129]
	v_mfma_f32_16x16x32_bf16 v[122:125], v[162:165], v[186:189], v[122:125]
	v_mfma_f32_16x16x32_bf16 v[110:113], v[148:151], v[194:197], v[110:113]
	v_mfma_f32_16x16x32_bf16 v[106:109], v[162:165], v[194:197], v[106:109]
	v_mfma_f32_16x16x32_bf16 v[94:97], v[148:151], v[202:205], v[94:97]
	v_mfma_f32_16x16x32_bf16 v[90:93], v[162:165], v[202:205], v[90:93]
	v_mfma_f32_16x16x32_bf16 v[78:81], v[148:151], v[210:213], v[78:81]
	v_mfma_f32_16x16x32_bf16 v[74:77], v[162:165], v[210:213], v[74:77]
	s_setprio 0
	s_setprio 1
	v_mfma_f32_16x16x32_bf16 v[118:121], v[166:169], v[182:185], v[118:121]
	v_mfma_f32_16x16x32_bf16 v[114:117], v[174:177], v[182:185], v[114:117]
	v_mfma_f32_16x16x32_bf16 v[102:105], v[166:169], v[190:193], v[102:105]
	v_mfma_f32_16x16x32_bf16 v[98:101], v[174:177], v[190:193], v[98:101]
	v_mfma_f32_16x16x32_bf16 v[86:89], v[166:169], v[198:201], v[86:89]
	v_mfma_f32_16x16x32_bf16 v[82:85], v[174:177], v[198:201], v[82:85]
	v_mfma_f32_16x16x32_bf16 v[70:73], v[166:169], v[206:209], v[70:73]
	v_mfma_f32_16x16x32_bf16 v[66:69], v[174:177], v[206:209], v[66:69]
	v_mfma_f32_16x16x32_bf16 v[118:121], v[170:173], v[186:189], v[118:121]
	v_mfma_f32_16x16x32_bf16 v[114:117], v[178:181], v[186:189], v[114:117]
	v_mfma_f32_16x16x32_bf16 v[102:105], v[170:173], v[194:197], v[102:105]
	v_mfma_f32_16x16x32_bf16 v[98:101], v[178:181], v[194:197], v[98:101]
	v_mfma_f32_16x16x32_bf16 v[86:89], v[170:173], v[202:205], v[86:89]
	v_mfma_f32_16x16x32_bf16 v[82:85], v[178:181], v[202:205], v[82:85]
	v_mfma_f32_16x16x32_bf16 v[70:73], v[170:173], v[210:213], v[70:73]
	v_mfma_f32_16x16x32_bf16 v[66:69], v[178:181], v[210:213], v[66:69]
	s_setprio 0
	s_barrier
	s_add_i32 s54, s48, s41
	v_lshl_add_u64 v[214:215], s[30:31], 0, v[132:133]
	s_mov_b32 m0, s54
	ds_read_b128 v[182:185], v156 offset:16384
	ds_read_b128 v[186:189], v156 offset:17408
	ds_read_b128 v[190:193], v156 offset:18432
	ds_read_b128 v[194:197], v156 offset:19456
	ds_read_b128 v[198:201], v156 offset:20480
	ds_read_b128 v[202:205], v156 offset:21504
	ds_read_b128 v[206:209], v156 offset:22528
	ds_read_b128 v[210:213], v156 offset:23552
	global_load_lds_dwordx4 v[214:215], off
	s_add_i32 m0, s54, 0x2000
	s_add_u32 s54, s30, 0x20000
	v_lshl_add_u64 v[216:217], s[30:31], 0, v[136:137]
	s_addc_u32 s55, s31, 0
	s_add_i32 s56, s49, s41
	global_load_lds_dwordx4 v[216:217], off
	v_lshl_add_u64 v[218:219], s[54:55], 0, v[132:133]
	s_mov_b32 m0, s56
	v_lshl_add_u64 v[220:221], s[34:35], 0, v[134:135]
	global_load_lds_dwordx4 v[218:219], off
	v_lshl_add_u64 v[218:219], s[54:55], 0, v[136:137]
	s_add_i32 m0, s56, 0x2000
	s_nop 0
	global_load_lds_dwordx4 v[218:219], off
	v_lshl_add_u64 v[218:219], s[34:35], 0, v[130:131]
	s_mov_b32 m0, s27
	s_nop 0
	global_load_lds_dwordx4 v[218:219], off
	s_mov_b32 m0, s42
	s_nop 0
	global_load_lds_dwordx4 v[220:221], off
	s_waitcnt vmcnt(8)
	s_waitcnt lgkmcnt(0)
	s_barrier
	s_setprio 1
	s_waitcnt lgkmcnt(0)
	s_nop 0
	v_mfma_f32_16x16x32_bf16 v[62:65], v[144:147], v[182:185], v[62:65]
	v_mfma_f32_16x16x32_bf16 v[58:61], v[158:161], v[182:185], v[58:61]
	v_mfma_f32_16x16x32_bf16 v[46:49], v[144:147], v[190:193], v[46:49]
	v_mfma_f32_16x16x32_bf16 v[42:45], v[158:161], v[190:193], v[42:45]
	v_mfma_f32_16x16x32_bf16 v[14:17], v[144:147], v[198:201], v[14:17]
	v_mfma_f32_16x16x32_bf16 v[10:13], v[158:161], v[198:201], v[10:13]
	v_mfma_f32_16x16x32_bf16 v[6:9], v[144:147], v[206:209], v[6:9]
	v_mfma_f32_16x16x32_bf16 v[2:5], v[158:161], v[206:209], v[2:5]
	v_mfma_f32_16x16x32_bf16 v[62:65], v[148:151], v[186:189], v[62:65]
	v_mfma_f32_16x16x32_bf16 v[58:61], v[162:165], v[186:189], v[58:61]
	v_mfma_f32_16x16x32_bf16 v[46:49], v[148:151], v[194:197], v[46:49]
	v_mfma_f32_16x16x32_bf16 v[42:45], v[162:165], v[194:197], v[42:45]
	v_mfma_f32_16x16x32_bf16 v[14:17], v[148:151], v[202:205], v[14:17]
	v_mfma_f32_16x16x32_bf16 v[10:13], v[162:165], v[202:205], v[10:13]
	v_mfma_f32_16x16x32_bf16 v[6:9], v[148:151], v[210:213], v[6:9]
	v_mfma_f32_16x16x32_bf16 v[2:5], v[162:165], v[210:213], v[2:5]
	s_setprio 0
	s_setprio 1
	v_mfma_f32_16x16x32_bf16 v[54:57], v[166:169], v[182:185], v[54:57]
	v_mfma_f32_16x16x32_bf16 v[50:53], v[174:177], v[182:185], v[50:53]
	v_mfma_f32_16x16x32_bf16 v[30:33], v[166:169], v[190:193], v[30:33]
	v_mfma_f32_16x16x32_bf16 v[26:29], v[174:177], v[190:193], v[26:29]
	v_mfma_f32_16x16x32_bf16 v[34:37], v[166:169], v[198:201], v[34:37]
	v_mfma_f32_16x16x32_bf16 v[38:41], v[174:177], v[198:201], v[38:41]
	v_mfma_f32_16x16x32_bf16 v[18:21], v[166:169], v[206:209], v[18:21]
	v_mfma_f32_16x16x32_bf16 v[22:25], v[174:177], v[206:209], v[22:25]
	v_mfma_f32_16x16x32_bf16 v[54:57], v[170:173], v[186:189], v[54:57]
	v_mfma_f32_16x16x32_bf16 v[50:53], v[178:181], v[186:189], v[50:53]
	v_mfma_f32_16x16x32_bf16 v[30:33], v[170:173], v[194:197], v[30:33]
	v_mfma_f32_16x16x32_bf16 v[26:29], v[178:181], v[194:197], v[26:29]
	v_mfma_f32_16x16x32_bf16 v[34:37], v[170:173], v[202:205], v[34:37]
	v_mfma_f32_16x16x32_bf16 v[38:41], v[178:181], v[202:205], v[38:41]
	v_mfma_f32_16x16x32_bf16 v[18:21], v[170:173], v[210:213], v[18:21]
	v_mfma_f32_16x16x32_bf16 v[22:25], v[178:181], v[210:213], v[22:25]
	s_setprio 0
	s_barrier
; #define PG8_STAGE2(bufoff, gbase, v0, v1) do { \
;         __builtin_amdgcn_global_load_lds((const unsigned*)((const char*)(gbase) + (v0)), (LAS unsigned*)(lds + (bufoff) + ldsw), 16, 0, 0); \
;         __builtin_amdgcn_global_load_lds((const unsigned*)((const char*)(gbase) + (v1)), (LAS unsigned*)(lds + (bufoff) + ldsw + 8192), 16, 0, 0); } while (0)
; #define PG8_LDA(dst, b, h) do { _Pragma("unroll") for (int m = 0; m < 4; ++m) _Pragma("unroll") for (int k = 0; k < 2; ++k) dst[m][k] = *(const LAS bf16x8*)(lds + PG8_SA(b, h) + aoff + m * 2048 + k * 1024); } while (0)
; #define PG8_LDB(dst, b, h) do { _Pragma("unroll") for (int n = 0; n < 2; ++n) _Pragma("unroll") for (int k = 0; k < 2; ++k) dst[n][k] = *(const LAS bf16x8*)(lds + PG8_SB(b, h) + boff + n * 2048 + k * 1024); } while (0)
; #define PG8_MMA(ai, bj, At, Bt) do { __builtin_amdgcn_s_setprio(1); _Pragma("unroll") for (int m = 0; m < 4; ++m) _Pragma("unroll") for (int n = 0; n < 2; ++n) _Pragma("unroll") for (int k = 0; k < 2; ++k) \
;         acc[ai][bj][m][n] = __builtin_amdgcn_mfma_f32_16x16x32_bf16(Bt[n][k], At[m][k], acc[ai][bj][m][n], 0, 0, 0); __builtin_amdgcn_s_setprio(0); } while (0)
; #define PG8_WAIT_V(n) asm volatile("s_waitcnt vmcnt(" #n ")" ::: "memory")
; #define PG8_WAIT_L(n) asm volatile("s_waitcnt lgkmcnt(" #n ")" ::: "memory")
; #define PG8_BAR __builtin_amdgcn_s_barrier()
; #define PG8_SCHED __builtin_amdgcn_sched_barrier(0)
; template <class Epi, class Sched, bool ALIGN_EPI, bool SP2, bool GATHER>
; DI void gemm_phase(LAS unsigned char* lds, const Gemm g, const Sched& S, const Epi& E) {
;     ...
;             PG8_LDB(B0, 1, 0); PG8_LDB(B1, 1, 1); PG8_SCHED; PG8_LDA(At, 1, 0); PG8_STAGE2(PG8_SA(0, 1), a2 + hstepA, x10, x11);
;             PG8_WAIT_V(8); PG8_WAIT_L(0); PG8_BAR; PG8_MMA(0, 0, At, B0); PG8_MMA(0, 1, At, B1); PG8_BAR; PG8_SCHED;
	s_add_i32 s54, 0, 0x18000
	v_add_u32_e32 v138, s54, v152
	s_add_i32 s55, 0, 0x1c000
	ds_read_b128 v[144:147], v138
	ds_read_b128 v[148:151], v138 offset:1024
	ds_read_b128 v[158:161], v138 offset:2048
	ds_read_b128 v[162:165], v138 offset:3072
	v_add_u32_e32 v138, s55, v152
	ds_read_b128 v[166:169], v138
	ds_read_b128 v[170:173], v138 offset:1024
	ds_read_b128 v[174:177], v138 offset:2048
	ds_read_b128 v[178:181], v138 offset:3072
	s_add_u32 s34, s34, 0x20000
	s_addc_u32 s35, s35, 0
	s_mov_b32 m0, s43
	v_lshl_add_u64 v[222:223], s[34:35], 0, v[130:131]
	ds_read_b128 v[182:185], v156 offset:32768
	ds_read_b128 v[186:189], v156 offset:33792
	ds_read_b128 v[190:193], v156 offset:34816
	ds_read_b128 v[194:197], v156 offset:35840
	ds_read_b128 v[198:201], v156 offset:36864
	ds_read_b128 v[202:205], v156 offset:37888
	ds_read_b128 v[206:209], v156 offset:38912
	ds_read_b128 v[210:213], v156 offset:39936
	global_load_lds_dwordx4 v[222:223], off
	v_lshl_add_u64 v[222:223], s[34:35], 0, v[134:135]
	s_mov_b32 m0, s44
	s_nop 0
	global_load_lds_dwordx4 v[222:223], off
	s_waitcnt vmcnt(8)
	s_waitcnt lgkmcnt(0)
	s_barrier
	s_setprio 1
	s_waitcnt lgkmcnt(0)
	s_nop 0
	v_mfma_f32_16x16x32_bf16 v[126:129], v[144:147], v[182:185], v[126:129]
	v_mfma_f32_16x16x32_bf16 v[122:125], v[158:161], v[182:185], v[122:125]
	v_mfma_f32_16x16x32_bf16 v[110:113], v[144:147], v[190:193], v[110:113]
	v_mfma_f32_16x16x32_bf16 v[106:109], v[158:161], v[190:193], v[106:109]
	v_mfma_f32_16x16x32_bf16 v[94:97], v[144:147], v[198:201], v[94:97]
	v_mfma_f32_16x16x32_bf16 v[90:93], v[158:161], v[198:201], v[90:93]
	v_mfma_f32_16x16x32_bf16 v[78:81], v[144:147], v[206:209], v[78:81]
	v_mfma_f32_16x16x32_bf16 v[74:77], v[158:161], v[206:209], v[74:77]
	v_mfma_f32_16x16x32_bf16 v[126:129], v[148:151], v[186:189], v[126:129]
	v_mfma_f32_16x16x32_bf16 v[122:125], v[162:165], v[186:189], v[122:125]
	v_mfma_f32_16x16x32_bf16 v[110:113], v[148:151], v[194:197], v[110:113]
	v_mfma_f32_16x16x32_bf16 v[106:109], v[162:165], v[194:197], v[106:109]
	v_mfma_f32_16x16x32_bf16 v[94:97], v[148:151], v[202:205], v[94:97]
	v_mfma_f32_16x16x32_bf16 v[90:93], v[162:165], v[202:205], v[90:93]
	v_mfma_f32_16x16x32_bf16 v[78:81], v[148:151], v[210:213], v[78:81]
	v_mfma_f32_16x16x32_bf16 v[74:77], v[162:165], v[210:213], v[74:77]
	s_setprio 0
	s_setprio 1
	v_mfma_f32_16x16x32_bf16 v[118:121], v[166:169], v[182:185], v[118:121]
	v_mfma_f32_16x16x32_bf16 v[114:117], v[174:177], v[182:185], v[114:117]
	v_mfma_f32_16x16x32_bf16 v[102:105], v[166:169], v[190:193], v[102:105]
	v_mfma_f32_16x16x32_bf16 v[98:101], v[174:177], v[190:193], v[98:101]
	v_mfma_f32_16x16x32_bf16 v[86:89], v[166:169], v[198:201], v[86:89]
	v_mfma_f32_16x16x32_bf16 v[82:85], v[174:177], v[198:201], v[82:85]
	v_mfma_f32_16x16x32_bf16 v[70:73], v[166:169], v[206:209], v[70:73]
	v_mfma_f32_16x16x32_bf16 v[66:69], v[174:177], v[206:209], v[66:69]
	v_mfma_f32_16x16x32_bf16 v[118:121], v[170:173], v[186:189], v[118:121]
	v_mfma_f32_16x16x32_bf16 v[114:117], v[178:181], v[186:189], v[114:117]
	v_mfma_f32_16x16x32_bf16 v[102:105], v[170:173], v[194:197], v[102:105]
	v_mfma_f32_16x16x32_bf16 v[98:101], v[178:181], v[194:197], v[98:101]
	v_mfma_f32_16x16x32_bf16 v[86:89], v[170:173], v[202:205], v[86:89]
	v_mfma_f32_16x16x32_bf16 v[82:85], v[178:181], v[202:205], v[82:85]
	v_mfma_f32_16x16x32_bf16 v[70:73], v[170:173], v[210:213], v[70:73]
	v_mfma_f32_16x16x32_bf16 v[66:69], v[178:181], v[210:213], v[66:69]
	s_setprio 0
	s_barrier
; #define PG8_STAGE2(bufoff, gbase, v0, v1) do { \
;         __builtin_amdgcn_global_load_lds((const unsigned*)((const char*)(gbase) + (v0)), (LAS unsigned*)(lds + (bufoff) + ldsw), 16, 0, 0); \
;         __builtin_amdgcn_global_load_lds((const unsigned*)((const char*)(gbase) + (v1)), (LAS unsigned*)(lds + (bufoff) + ldsw + 8192), 16, 0, 0); } while (0)
; #define PG8_STAGE(bufoff, gbase, voff) PG8_STAGE2(bufoff, gbase, (voff)[0], (voff)[1])
; #define PG8_LDA(dst, b, h) do { _Pragma("unroll") for (int m = 0; m < 4; ++m) _Pragma("unroll") for (int k = 0; k < 2; ++k) dst[m][k] = *(const LAS bf16x8*)(lds + PG8_SA(b, h) + aoff + m * 2048 + k * 1024); } while (0)
; #define PG8_MMA(ai, bj, At, Bt) do { __builtin_amdgcn_s_setprio(1); _Pragma("unroll") for (int m = 0; m < 4; ++m) _Pragma("unroll") for (int n = 0; n < 2; ++n) _Pragma("unroll") for (int k = 0; k < 2; ++k) \
;         acc[ai][bj][m][n] = __builtin_amdgcn_mfma_f32_16x16x32_bf16(Bt[n][k], At[m][k], acc[ai][bj][m][n], 0, 0, 0); __builtin_amdgcn_s_setprio(0); } while (0)
; #define PG8_WAIT_V(n) asm volatile("s_waitcnt vmcnt(" #n ")" ::: "memory")
; #define PG8_WAIT_L(n) asm volatile("s_waitcnt lgkmcnt(" #n ")" ::: "memory")
; #define PG8_BAR __builtin_amdgcn_s_barrier()
; #define PG8_SCHED __builtin_amdgcn_sched_barrier(0)
; template <class Epi, class Sched, bool ALIGN_EPI, bool SP2, bool GATHER>
; DI void gemm_phase(LAS unsigned char* lds, const Gemm g, const Sched& S, const Epi& E) {
;     ...
;             PG8_LDA(At, 1, 1); PG8_STAGE(PG8_SB(1, 0), b3, voffB); PG8_STAGE(PG8_SB(1, 1), b3 + hstep, voffB); PG8_STAGE2(PG8_SA(1, 0), a3, x00, x01);
;             PG8_WAIT_V(8); PG8_WAIT_L(0); PG8_BAR; PG8_MMA(1, 0, At, B0); PG8_MMA(1, 1, At, B1); PG8_BAR; PG8_SCHED;
;         }
	s_add_i32 s34, s54, s41
	v_lshl_add_u64 v[214:215], v[214:215], 0, s[10:11]
	s_mov_b32 m0, s34
	ds_read_b128 v[182:185], v156 offset:49152
	ds_read_b128 v[186:189], v156 offset:50176
	ds_read_b128 v[190:193], v156 offset:51200
	ds_read_b128 v[194:197], v156 offset:52224
	ds_read_b128 v[198:201], v156 offset:53248
	ds_read_b128 v[202:205], v156 offset:54272
	ds_read_b128 v[206:209], v156 offset:55296
	ds_read_b128 v[210:213], v156 offset:56320
	global_load_lds_dwordx4 v[214:215], off
	s_add_i32 m0, s34, 0x2000
	s_add_u32 s30, s30, 0x20080
	v_lshl_add_u64 v[214:215], v[216:217], 0, s[10:11]
	s_addc_u32 s31, s31, 0
	s_add_i32 s34, s55, s41
	global_load_lds_dwordx4 v[214:215], off
	v_lshl_add_u64 v[214:215], s[30:31], 0, v[132:133]
	s_mov_b32 m0, s34
	s_nop 0
	global_load_lds_dwordx4 v[214:215], off
	v_lshl_add_u64 v[214:215], s[30:31], 0, v[136:137]
	s_add_i32 m0, s34, 0x2000
	s_nop 0
	global_load_lds_dwordx4 v[214:215], off
	v_lshl_add_u64 v[214:215], v[218:219], 0, s[10:11]
	s_mov_b32 m0, s46
	s_nop 0
	global_load_lds_dwordx4 v[214:215], off
	v_lshl_add_u64 v[214:215], v[220:221], 0, s[10:11]
	s_mov_b32 m0, s47
	s_nop 0
	global_load_lds_dwordx4 v[214:215], off
	s_waitcnt vmcnt(8)
	s_waitcnt lgkmcnt(0)
	s_barrier
	s_setprio 1
	s_waitcnt lgkmcnt(0)
	v_mfma_f32_16x16x32_bf16 v[62:65], v[144:147], v[182:185], v[62:65]
	v_mfma_f32_16x16x32_bf16 v[58:61], v[158:161], v[182:185], v[58:61]
	v_mfma_f32_16x16x32_bf16 v[46:49], v[144:147], v[190:193], v[46:49]
	v_mfma_f32_16x16x32_bf16 v[42:45], v[158:161], v[190:193], v[42:45]
	v_mfma_f32_16x16x32_bf16 v[14:17], v[144:147], v[198:201], v[14:17]
	v_mfma_f32_16x16x32_bf16 v[10:13], v[158:161], v[198:201], v[10:13]
	v_mfma_f32_16x16x32_bf16 v[6:9], v[144:147], v[206:209], v[6:9]
	v_mfma_f32_16x16x32_bf16 v[2:5], v[158:161], v[206:209], v[2:5]
	v_mfma_f32_16x16x32_bf16 v[62:65], v[148:151], v[186:189], v[62:65]
	v_mfma_f32_16x16x32_bf16 v[58:61], v[162:165], v[186:189], v[58:61]
	v_mfma_f32_16x16x32_bf16 v[46:49], v[148:151], v[194:197], v[46:49]
	v_mfma_f32_16x16x32_bf16 v[42:45], v[162:165], v[194:197], v[42:45]
	v_mfma_f32_16x16x32_bf16 v[14:17], v[148:151], v[202:205], v[14:17]
	v_mfma_f32_16x16x32_bf16 v[10:13], v[162:165], v[202:205], v[10:13]
	v_mfma_f32_16x16x32_bf16 v[6:9], v[148:151], v[210:213], v[6:9]
	v_mfma_f32_16x16x32_bf16 v[2:5], v[162:165], v[210:213], v[2:5]
	s_setprio 0
	s_setprio 1
	v_mfma_f32_16x16x32_bf16 v[54:57], v[166:169], v[182:185], v[54:57]
	v_mfma_f32_16x16x32_bf16 v[50:53], v[174:177], v[182:185], v[50:53]
	v_mfma_f32_16x16x32_bf16 v[30:33], v[166:169], v[190:193], v[30:33]
	v_mfma_f32_16x16x32_bf16 v[26:29], v[174:177], v[190:193], v[26:29]
	v_mfma_f32_16x16x32_bf16 v[34:37], v[166:169], v[198:201], v[34:37]
	v_mfma_f32_16x16x32_bf16 v[38:41], v[174:177], v[198:201], v[38:41]
	v_mfma_f32_16x16x32_bf16 v[18:21], v[166:169], v[206:209], v[18:21]
	v_mfma_f32_16x16x32_bf16 v[22:25], v[174:177], v[206:209], v[22:25]
	v_mfma_f32_16x16x32_bf16 v[54:57], v[170:173], v[186:189], v[54:57]
	v_mfma_f32_16x16x32_bf16 v[50:53], v[178:181], v[186:189], v[50:53]
	v_mfma_f32_16x16x32_bf16 v[30:33], v[170:173], v[194:197], v[30:33]
	v_mfma_f32_16x16x32_bf16 v[26:29], v[178:181], v[194:197], v[26:29]
	v_mfma_f32_16x16x32_bf16 v[34:37], v[170:173], v[202:205], v[34:37]
	v_mfma_f32_16x16x32_bf16 v[38:41], v[178:181], v[202:205], v[38:41]
	v_mfma_f32_16x16x32_bf16 v[18:21], v[170:173], v[210:213], v[18:21]
	v_mfma_f32_16x16x32_bf16 v[22:25], v[178:181], v[210:213], v[22:25]
	s_setprio 0
	s_barrier
	s_add_i32 s53, s53, 2
	s_add_u32 s28, s28, 0x100
	s_addc_u32 s29, s29, 0
	s_add_u32 s51, s51, 0x100
	s_addc_u32 s52, s52, 0
	s_cmp_gt_u32 s53, 5
	s_cbranch_scc0 .LBB0_996
